# all per-segment s_setprio toggles removed from the GEMM K-loops (loops are paced by DMA arrival)
# speedup vs baseline: 1.0217x; 1.0056x over previous
; #define G_STAGE(bufoff, gbase, voff) do { _Pragma("unroll") for (int _i = 0; _i < 2; ++_i) \
;         __builtin_amdgcn_global_load_lds((const unsigned*)((const char*)(gbase) + (voff)[_i]), (LAS unsigned*)(lds + (bufoff) + ldsw + _i * 8192), 16, 0, 0); } while (0)
; #define G_LDA(dst, b, h) do { _Pragma("unroll") for (int m = 0; m < 4; ++m) G_LD8(dst[m], lds + G_SA(b, h) + aoff + m * 2048); } while (0)
; #define G_LDB(dst, b, h) do { _Pragma("unroll") for (int n = 0; n < 2; ++n) G_LD8(dst[n], lds + G_SB(b, h) + boff + n * 2048); } while (0)
; #define G_WAIT_V(n) asm volatile("s_waitcnt vmcnt(" #n ")" ::: "memory")
; #define G_WAIT_L(n) asm volatile("s_waitcnt lgkmcnt(" #n ")" ::: "memory")
; #define G_BAR __builtin_amdgcn_s_barrier()
; #define G_SCHED __builtin_amdgcn_sched_barrier(0)
;     ...
;             const char* a11 = cur.a1 + (size_t)(t + 1) * kstep;
;             const char* a02 = last ? nxt.a0 : cur.a0 + (size_t)(t + 2) * kstep; const char* a12 = last ? nxt.a1 : cur.a1 + (size_t)(t + 2) * kstep;
;             const char* b02 = last ? nxt.b0 : cur.b0 + (size_t)(t + 2) * kstep; const char* b12 = last ? nxt.b1 : cur.b1 + (size_t)(t + 2) * kstep;
;             G_LDB(B0, 0, 0); G_LDB(B1, 0, 1); G_SCHED; G_LDA(At, 0, 0); G_STAGE(G_SA(1, 1), a11, vA1);
;             if constexpr (GATHER) { if (last) { int tz = tid; asm volatile("" : "+v"(tz));
; #pragma unroll
;                 for (int i = 0; i < 2; ++i) { int R, C; stage_rc(tz * 16 + i * 8192, R, C); gc0[i] = S.row_off(nxt, R, lds) + (unsigned)C * 2u; gc1[i] = S.row_off(nxt, 128 + R, lds) + (unsigned)C * 2u; } } }
;             G_WAIT_L(0); G_BAR; G_MMA(0, 0, At, B0); G_MMA(0, 1, At, B1); G_WAIT_V(8); G_BAR; G_SCHED;
;             G_LDA(At, 0, 1); G_STAGE(G_SB(0, 0), b02, voffB); G_STAGE(G_SB(0, 1), b12, voffB); G_STAGE(G_SA(0, 0), a02, vA0);
;             G_WAIT_L(0); G_BAR; G_MMA(1, 0, At, B0); G_MMA(1, 1, At, B1); G_WAIT_V(8); G_BAR; G_SCHED;
;             G_LDB(B0, 1, 0); G_LDB(B1, 1, 1); G_SCHED; G_LDA(At, 1, 0); G_STAGE(G_SA(0, 1), a12, vA1);
;             G_WAIT_L(0); G_BAR; G_MMA(0, 0, At, B0); G_MMA(0, 1, At, B1); G_WAIT_V(8); G_BAR; G_SCHED;
;             G_LDA(At, 1, 1); G_STAGE(G_SB(1, 0), b02 + kstep, voffB); G_STAGE(G_SB(1, 1), b12 + kstep, voffB); G_STAGE(G_SA(1, 0), a02 + kstep, vA0);
;             G_WAIT_L(0); G_BAR; G_MMA(1, 0, At, B0); G_MMA(1, 1, At, B1); G_WAIT_V(8); G_BAR; G_SCHED;
.LBB0_179:
	v_add_u32_e32 v144, s91, v163
	v_add_u32_e32 v170, s3, v163
	ds_read_b128 v[34:37], v144
	ds_read_b128 v[38:41], v144 offset:1024
	ds_read_b128 v[42:45], v144 offset:2048
	ds_read_b128 v[144:147], v144 offset:3072
	ds_read_b128 v[150:153], v170
	ds_read_b128 v[154:157], v170 offset:1024
	ds_read_b128 v[166:169], v170 offset:2048
	ds_read_b128 v[170:173], v170 offset:3072
	s_add_i32 s63, s59, 2
	s_add_u32 s73, s74, 0x80
	s_addc_u32 s76, s75, 0
	s_add_i32 s83, s91, s97
	s_add_i32 m0, s22, 0xc000
	s_add_i32 s82, s22, 0xe000
	s_add_i32 s89, s83, 0x2000
	s_cmp_eq_u32 s20, s59
	s_cselect_b32 s79, s65, s33
	s_cselect_b32 s78, s64, s19
	s_cselect_b32 s81, s69, s2
	s_cselect_b32 s80, s68, s0
	s_cselect_b32 s77, s67, s76
	s_cselect_b32 s76, s66, s73
	ds_read_b128 v[174:177], v164
	ds_read_b128 v[178:181], v164 offset:1024
	ds_read_b128 v[182:185], v164 offset:2048
	ds_read_b128 v[186:189], v164 offset:3072
	ds_read_b128 v[190:193], v164 offset:4096
	ds_read_b128 v[194:197], v164 offset:5120
	ds_read_b128 v[198:201], v164 offset:6144
	ds_read_b128 v[202:205], v164 offset:7168
	global_load_lds_dwordx4 v240, s[74:75]
	s_mov_b32 m0, s82
	s_nop 0
	global_load_lds_dwordx4 v242, s[74:75]
	s_waitcnt lgkmcnt(0)
	v_mov_b32_e32 v33, v149
	s_waitcnt vmcnt(8)
	s_barrier
	s_waitcnt lgkmcnt(0)
	v_mfma_i32_16x16x64_i8 v[140:143], v[34:37], v[174:177], v[140:143]
	v_mfma_i32_16x16x64_i8 v[132:135], v[42:45], v[174:177], v[132:135]
	v_mfma_i32_16x16x64_i8 v[124:127], v[34:37], v[182:185], v[124:127]
	v_mfma_i32_16x16x64_i8 v[116:119], v[42:45], v[182:185], v[116:119]
	v_mfma_i32_16x16x64_i8 v[108:111], v[34:37], v[190:193], v[108:111]
	v_mfma_i32_16x16x64_i8 v[100:103], v[42:45], v[190:193], v[100:103]
	v_mfma_i32_16x16x64_i8 v[92:95], v[34:37], v[198:201], v[92:95]
	v_mfma_i32_16x16x64_i8 v[84:87], v[42:45], v[198:201], v[84:87]
	v_mfma_i32_16x16x64_i8 v[140:143], v[38:41], v[178:181], v[140:143]
	v_mfma_i32_16x16x64_i8 v[132:135], v[144:147], v[178:181], v[132:135]
	v_mfma_i32_16x16x64_i8 v[124:127], v[38:41], v[186:189], v[124:127]
	v_mfma_i32_16x16x64_i8 v[116:119], v[144:147], v[186:189], v[116:119]
	v_mfma_i32_16x16x64_i8 v[108:111], v[38:41], v[194:197], v[108:111]
	v_mfma_i32_16x16x64_i8 v[100:103], v[144:147], v[194:197], v[100:103]
	v_mfma_i32_16x16x64_i8 v[92:95], v[38:41], v[202:205], v[92:95]
	v_mfma_i32_16x16x64_i8 v[84:87], v[144:147], v[202:205], v[84:87]
	v_mfma_i32_16x16x64_i8 v[136:139], v[150:153], v[174:177], v[136:139]
	v_mfma_i32_16x16x64_i8 v[128:131], v[166:169], v[174:177], v[128:131]
	v_mfma_i32_16x16x64_i8 v[120:123], v[150:153], v[182:185], v[120:123]
	v_mfma_i32_16x16x64_i8 v[112:115], v[166:169], v[182:185], v[112:115]
	v_mfma_i32_16x16x64_i8 v[104:107], v[150:153], v[190:193], v[104:107]
	v_mfma_i32_16x16x64_i8 v[96:99], v[166:169], v[190:193], v[96:99]
	v_mfma_i32_16x16x64_i8 v[88:91], v[150:153], v[198:201], v[88:91]
	v_mfma_i32_16x16x64_i8 v[80:83], v[166:169], v[198:201], v[80:83]
	v_mfma_i32_16x16x64_i8 v[136:139], v[154:157], v[178:181], v[136:139]
	v_mfma_i32_16x16x64_i8 v[128:131], v[170:173], v[178:181], v[128:131]
	v_mfma_i32_16x16x64_i8 v[120:123], v[154:157], v[186:189], v[120:123]
	v_mfma_i32_16x16x64_i8 v[112:115], v[170:173], v[186:189], v[112:115]
	v_mfma_i32_16x16x64_i8 v[104:107], v[154:157], v[194:197], v[104:107]
	v_mfma_i32_16x16x64_i8 v[96:99], v[170:173], v[194:197], v[96:99]
	v_mfma_i32_16x16x64_i8 v[88:91], v[154:157], v[202:205], v[88:91]
	v_mfma_i32_16x16x64_i8 v[80:83], v[170:173], v[202:205], v[80:83]
	s_waitcnt vmcnt(8)
	s_barrier
	s_mov_b32 m0, s83
	ds_read_b128 v[174:177], v164 offset:16384
	ds_read_b128 v[178:181], v164 offset:17408
	ds_read_b128 v[182:185], v164 offset:18432
	ds_read_b128 v[186:189], v164 offset:19456
	ds_read_b128 v[190:193], v164 offset:20480
	ds_read_b128 v[194:197], v164 offset:21504
	ds_read_b128 v[198:201], v164 offset:22528
	ds_read_b128 v[202:205], v164 offset:23552
	v_mov_b32_e32 v47, v149
	global_load_lds_dwordx4 v244, s[80:81]
	v_mov_b32_e32 v159, v149
	s_mov_b32 m0, s89
	v_lshl_add_u64 v[206:207], s[80:81], 0, v[244:245]
	v_lshl_add_u64 v[208:209], s[80:81], 0, v[246:247]
	global_load_lds_dwordx4 v246, s[80:81]
	s_cselect_b32 s81, s71, s6
	s_cselect_b32 s80, s70, s5
	s_add_i32 s59, s3, s97
	s_mov_b32 m0, s59
	v_lshl_add_u64 v[210:211], s[80:81], 0, v[244:245]
	global_load_lds_dwordx4 v244, s[80:81]
	s_add_i32 m0, s59, 0x2000
	v_lshl_add_u64 v[212:213], s[80:81], 0, v[246:247]
	global_load_lds_dwordx4 v246, s[80:81]
	s_mov_b32 m0, s22
	v_lshl_add_u64 v[158:159], s[78:79], 0, v[240:241]
	global_load_lds_dwordx4 v240, s[78:79]
	s_mov_b32 m0, s23
	v_lshl_add_u64 v[214:215], s[78:79], 0, v[242:243]
	global_load_lds_dwordx4 v242, s[78:79]
	s_waitcnt lgkmcnt(0)
	s_waitcnt vmcnt(8)
	s_barrier
; #define G_STAGE(bufoff, gbase, voff) do { _Pragma("unroll") for (int _i = 0; _i < 2; ++_i) \
;         __builtin_amdgcn_global_load_lds((const unsigned*)((const char*)(gbase) + (voff)[_i]), (LAS unsigned*)(lds + (bufoff) + ldsw + _i * 8192), 16, 0, 0); } while (0)
; #define G_LDA(dst, b, h) do { _Pragma("unroll") for (int m = 0; m < 4; ++m) G_LD8(dst[m], lds + G_SA(b, h) + aoff + m * 2048); } while (0)
; #define G_LDB(dst, b, h) do { _Pragma("unroll") for (int n = 0; n < 2; ++n) G_LD8(dst[n], lds + G_SB(b, h) + boff + n * 2048); } while (0)
; #define G_WAIT_V(n) asm volatile("s_waitcnt vmcnt(" #n ")" ::: "memory")
; #define G_WAIT_L(n) asm volatile("s_waitcnt lgkmcnt(" #n ")" ::: "memory")
; #define G_BAR __builtin_amdgcn_s_barrier()
; #define G_SCHED __builtin_amdgcn_sched_barrier(0)
;     __device__ __forceinline__ unsigned row_off(const Unit& u, int r, LAS unsigned char* lds) const { return (unsigned)((const LAS int*)(lds + LDS_STAGE + u.q * 4096))[r] * (unsigned)rowbytes; }
;     ...
;             G_LDB(B0, 0, 0); G_LDB(B1, 0, 1); G_SCHED; G_LDA(At, 0, 0); G_STAGE(G_SA(1, 1), a11, vA1);
;             if constexpr (GATHER) { if (last) { int tz = tid; asm volatile("" : "+v"(tz));
; #pragma unroll
;                 for (int i = 0; i < 2; ++i) { int R, C; stage_rc(tz * 16 + i * 8192, R, C); gc0[i] = S.row_off(nxt, R, lds) + (unsigned)C * 2u; gc1[i] = S.row_off(nxt, 128 + R, lds) + (unsigned)C * 2u; } } }
;             G_WAIT_L(0); G_BAR; G_MMA(0, 0, At, B0); G_MMA(0, 1, At, B1); G_WAIT_V(8); G_BAR; G_SCHED;
;             G_LDA(At, 0, 1); G_STAGE(G_SB(0, 0), b02, voffB); G_STAGE(G_SB(0, 1), b12, voffB); G_STAGE(G_SA(0, 0), a02, vA0);
;             G_WAIT_L(0); G_BAR; G_MMA(1, 0, At, B0); G_MMA(1, 1, At, B1); G_WAIT_V(8); G_BAR; G_SCHED;
;             G_LDB(B0, 1, 0); G_LDB(B1, 1, 1); G_SCHED; G_LDA(At, 1, 0); G_STAGE(G_SA(0, 1), a12, vA1);
;             G_WAIT_L(0); G_BAR; G_MMA(0, 0, At, B0); G_MMA(0, 1, At, B1); G_WAIT_V(8); G_BAR; G_SCHED;
;             G_LDA(At, 1, 1); G_STAGE(G_SB(1, 0), b02 + kstep, voffB); G_STAGE(G_SB(1, 1), b12 + kstep, voffB); G_STAGE(G_SA(1, 0), a02 + kstep, vA0);
;             G_WAIT_L(0); G_BAR; G_MMA(1, 0, At, B0); G_MMA(1, 1, At, B1); G_WAIT_V(8); G_BAR; G_SCHED;
	s_waitcnt lgkmcnt(0)
	v_mfma_i32_16x16x64_i8 v[76:79], v[34:37], v[174:177], v[76:79]
	v_mfma_i32_16x16x64_i8 v[68:71], v[42:45], v[174:177], v[68:71]
	v_mfma_i32_16x16x64_i8 v[60:63], v[34:37], v[182:185], v[60:63]
	v_mfma_i32_16x16x64_i8 v[52:55], v[42:45], v[182:185], v[52:55]
	v_mfma_i32_16x16x64_i8 v[28:31], v[34:37], v[190:193], v[28:31]
	v_mfma_i32_16x16x64_i8 v[20:23], v[42:45], v[190:193], v[20:23]
	v_mfma_i32_16x16x64_i8 v[12:15], v[34:37], v[198:201], v[12:15]
	v_mfma_i32_16x16x64_i8 v[4:7], v[42:45], v[198:201], v[4:7]
	v_mfma_i32_16x16x64_i8 v[76:79], v[38:41], v[178:181], v[76:79]
	v_mfma_i32_16x16x64_i8 v[68:71], v[144:147], v[178:181], v[68:71]
	v_mfma_i32_16x16x64_i8 v[60:63], v[38:41], v[186:189], v[60:63]
	v_mfma_i32_16x16x64_i8 v[52:55], v[144:147], v[186:189], v[52:55]
	v_mfma_i32_16x16x64_i8 v[28:31], v[38:41], v[194:197], v[28:31]
	v_mfma_i32_16x16x64_i8 v[20:23], v[144:147], v[194:197], v[20:23]
	v_mfma_i32_16x16x64_i8 v[12:15], v[38:41], v[202:205], v[12:15]
	v_mfma_i32_16x16x64_i8 v[4:7], v[144:147], v[202:205], v[4:7]
	v_mfma_i32_16x16x64_i8 v[46:49], v[166:169], v[182:185], v[48:51]
	v_mfma_i32_16x16x64_i8 v[24:27], v[150:153], v[190:193], v[24:27]
	v_mfma_i32_16x16x64_i8 v[16:19], v[166:169], v[190:193], v[16:19]
	v_mfma_i32_16x16x64_i8 v[8:11], v[150:153], v[198:201], v[8:11]
	v_mfma_i32_16x16x64_i8 v[0:3], v[166:169], v[198:201], v[0:3]
	v_mfma_i32_16x16x64_i8 v[34:37], v[150:153], v[174:177], v[72:75]
	v_mfma_i32_16x16x64_i8 v[38:41], v[166:169], v[174:177], v[64:67]
	v_mfma_i32_16x16x64_i8 v[42:45], v[150:153], v[182:185], v[56:59]
	v_mfma_i32_16x16x64_i8 v[46:49], v[170:173], v[186:189], v[46:49]
	v_mfma_i32_16x16x64_i8 v[24:27], v[154:157], v[194:197], v[24:27]
	v_mfma_i32_16x16x64_i8 v[16:19], v[170:173], v[194:197], v[16:19]
	v_mfma_i32_16x16x64_i8 v[8:11], v[154:157], v[202:205], v[8:11]
	v_mfma_i32_16x16x64_i8 v[0:3], v[170:173], v[202:205], v[0:3]
	v_mfma_i32_16x16x64_i8 v[34:37], v[154:157], v[178:181], v[34:37]
	v_mfma_i32_16x16x64_i8 v[38:41], v[170:173], v[178:181], v[38:41]
	v_mfma_i32_16x16x64_i8 v[42:45], v[154:157], v[186:189], v[42:45]
	s_waitcnt vmcnt(8)
	s_barrier
	s_add_i32 s59, 0, 0x18000
	v_add_u32_e32 v33, s59, v163
	s_add_i32 s73, 0, 0x1c000
	ds_read_b128 v[56:59], v33
	ds_read_b128 v[64:67], v33 offset:1024
	ds_read_b128 v[72:75], v33 offset:2048
	ds_read_b128 v[144:147], v33 offset:3072
	v_add_u32_e32 v33, s73, v163
	ds_read_b128 v[150:153], v33
	ds_read_b128 v[154:157], v33 offset:1024
	ds_read_b128 v[166:169], v33 offset:2048
	ds_read_b128 v[170:173], v33 offset:3072
	s_mov_b32 m0, s55
	ds_read_b128 v[174:177], v164 offset:32768
	ds_read_b128 v[178:181], v164 offset:33792
	ds_read_b128 v[182:185], v164 offset:34816
	ds_read_b128 v[186:189], v164 offset:35840
	ds_read_b128 v[190:193], v164 offset:36864
	ds_read_b128 v[194:197], v164 offset:37888
	ds_read_b128 v[198:201], v164 offset:38912
	ds_read_b128 v[202:205], v164 offset:39936
	global_load_lds_dwordx4 v240, s[76:77]
	s_mov_b32 m0, s84
	s_nop 0
	global_load_lds_dwordx4 v242, s[76:77]
	s_waitcnt lgkmcnt(0)
	s_waitcnt vmcnt(8)
	s_barrier
	s_waitcnt lgkmcnt(0)
	v_mfma_i32_16x16x64_i8 v[140:143], v[56:59], v[174:177], v[140:143]
	v_mfma_i32_16x16x64_i8 v[132:135], v[72:75], v[174:177], v[132:135]
	v_mfma_i32_16x16x64_i8 v[124:127], v[56:59], v[182:185], v[124:127]
	v_mfma_i32_16x16x64_i8 v[116:119], v[72:75], v[182:185], v[116:119]
	v_mfma_i32_16x16x64_i8 v[108:111], v[56:59], v[190:193], v[108:111]
	v_mfma_i32_16x16x64_i8 v[100:103], v[72:75], v[190:193], v[100:103]
	v_mfma_i32_16x16x64_i8 v[92:95], v[56:59], v[198:201], v[92:95]
	v_mfma_i32_16x16x64_i8 v[84:87], v[72:75], v[198:201], v[84:87]
	v_mfma_i32_16x16x64_i8 v[140:143], v[64:67], v[178:181], v[140:143]
	v_mfma_i32_16x16x64_i8 v[132:135], v[144:147], v[178:181], v[132:135]
	v_mfma_i32_16x16x64_i8 v[124:127], v[64:67], v[186:189], v[124:127]
	v_mfma_i32_16x16x64_i8 v[116:119], v[144:147], v[186:189], v[116:119]
	v_mfma_i32_16x16x64_i8 v[108:111], v[64:67], v[194:197], v[108:111]
	v_mfma_i32_16x16x64_i8 v[100:103], v[144:147], v[194:197], v[100:103]
	v_mfma_i32_16x16x64_i8 v[92:95], v[64:67], v[202:205], v[92:95]
	v_mfma_i32_16x16x64_i8 v[84:87], v[144:147], v[202:205], v[84:87]
	v_mfma_i32_16x16x64_i8 v[136:139], v[150:153], v[174:177], v[136:139]
	v_mfma_i32_16x16x64_i8 v[128:131], v[166:169], v[174:177], v[128:131]
	v_mfma_i32_16x16x64_i8 v[120:123], v[150:153], v[182:185], v[120:123]
	v_mfma_i32_16x16x64_i8 v[112:115], v[166:169], v[182:185], v[112:115]
	v_mfma_i32_16x16x64_i8 v[104:107], v[150:153], v[190:193], v[104:107]
	v_mfma_i32_16x16x64_i8 v[96:99], v[166:169], v[190:193], v[96:99]
	v_mfma_i32_16x16x64_i8 v[88:91], v[150:153], v[198:201], v[88:91]
	v_mfma_i32_16x16x64_i8 v[80:83], v[166:169], v[198:201], v[80:83]
	v_mfma_i32_16x16x64_i8 v[136:139], v[154:157], v[178:181], v[136:139]
	v_mfma_i32_16x16x64_i8 v[128:131], v[170:173], v[178:181], v[128:131]
	v_mfma_i32_16x16x64_i8 v[120:123], v[154:157], v[186:189], v[120:123]
	v_mfma_i32_16x16x64_i8 v[112:115], v[170:173], v[186:189], v[112:115]
	v_mfma_i32_16x16x64_i8 v[104:107], v[154:157], v[194:197], v[104:107]
	v_mfma_i32_16x16x64_i8 v[96:99], v[170:173], v[194:197], v[96:99]
	v_mfma_i32_16x16x64_i8 v[88:91], v[154:157], v[202:205], v[88:91]
	v_mfma_i32_16x16x64_i8 v[80:83], v[170:173], v[202:205], v[80:83]
	s_waitcnt vmcnt(8)
	s_barrier
; #define G_STAGE(bufoff, gbase, voff) do { _Pragma("unroll") for (int _i = 0; _i < 2; ++_i) \
;         __builtin_amdgcn_global_load_lds((const unsigned*)((const char*)(gbase) + (voff)[_i]), (LAS unsigned*)(lds + (bufoff) + ldsw + _i * 8192), 16, 0, 0); } while (0)
; #define G_LDA(dst, b, h) do { _Pragma("unroll") for (int m = 0; m < 4; ++m) G_LD8(dst[m], lds + G_SA(b, h) + aoff + m * 2048); } while (0)
; #define G_LDB(dst, b, h) do { _Pragma("unroll") for (int n = 0; n < 2; ++n) G_LD8(dst[n], lds + G_SB(b, h) + boff + n * 2048); } while (0)
; #define G_WAIT_V(n) asm volatile("s_waitcnt vmcnt(" #n ")" ::: "memory")
; #define G_WAIT_L(n) asm volatile("s_waitcnt lgkmcnt(" #n ")" ::: "memory")
; #define G_BAR __builtin_amdgcn_s_barrier()
; #define G_SCHED __builtin_amdgcn_sched_barrier(0)
;     ...
;             G_LDA(At, 0, 1); G_STAGE(G_SB(0, 0), b02, voffB); G_STAGE(G_SB(0, 1), b12, voffB); G_STAGE(G_SA(0, 0), a02, vA0);
;             G_WAIT_L(0); G_BAR; G_MMA(1, 0, At, B0); G_MMA(1, 1, At, B1); G_WAIT_V(8); G_BAR; G_SCHED;
;             G_LDB(B0, 1, 0); G_LDB(B1, 1, 1); G_SCHED; G_LDA(At, 1, 0); G_STAGE(G_SA(0, 1), a12, vA1);
;             G_WAIT_L(0); G_BAR; G_MMA(0, 0, At, B0); G_MMA(0, 1, At, B1); G_WAIT_V(8); G_BAR; G_SCHED;
;             G_LDA(At, 1, 1); G_STAGE(G_SB(1, 0), b02 + kstep, voffB); G_STAGE(G_SB(1, 1), b12 + kstep, voffB); G_STAGE(G_SA(1, 0), a02 + kstep, vA0);
;             G_WAIT_L(0); G_BAR; G_MMA(1, 0, At, B0); G_MMA(1, 1, At, B1); G_WAIT_V(8); G_BAR; G_SCHED;
	s_add_i32 s59, s59, s97
	v_lshl_add_u64 v[32:33], v[206:207], 0, s[46:47]
	s_mov_b32 m0, s59
	ds_read_b128 v[174:177], v164 offset:49152
	ds_read_b128 v[178:181], v164 offset:50176
	ds_read_b128 v[182:185], v164 offset:51200
	ds_read_b128 v[186:189], v164 offset:52224
	ds_read_b128 v[190:193], v164 offset:53248
	ds_read_b128 v[194:197], v164 offset:54272
	ds_read_b128 v[198:201], v164 offset:55296
	ds_read_b128 v[202:205], v164 offset:56320
	global_load_lds_dwordx4 v[32:33], off
	v_lshl_add_u64 v[32:33], v[208:209], 0, s[46:47]
	s_add_i32 m0, s59, 0x2000
	s_add_i32 s59, s73, s97
	global_load_lds_dwordx4 v[32:33], off
	v_lshl_add_u64 v[32:33], v[210:211], 0, s[46:47]
	s_mov_b32 m0, s59
	s_nop 0
	global_load_lds_dwordx4 v[32:33], off
	v_lshl_add_u64 v[32:33], v[212:213], 0, s[46:47]
	s_add_i32 m0, s59, 0x2000
	s_nop 0
	global_load_lds_dwordx4 v[32:33], off
	v_lshl_add_u64 v[32:33], v[158:159], 0, s[46:47]
	s_mov_b32 m0, s86
	s_nop 0
	global_load_lds_dwordx4 v[32:33], off
	v_lshl_add_u64 v[32:33], v[214:215], 0, s[46:47]
	s_mov_b32 m0, s87
	s_nop 0
	global_load_lds_dwordx4 v[32:33], off
	s_waitcnt lgkmcnt(0)
	s_waitcnt vmcnt(8)
	s_barrier
	s_waitcnt lgkmcnt(0)
	v_mfma_i32_16x16x64_i8 v[76:79], v[56:59], v[174:177], v[76:79]
	v_mfma_i32_16x16x64_i8 v[68:71], v[72:75], v[174:177], v[68:71]
	v_mfma_i32_16x16x64_i8 v[60:63], v[56:59], v[182:185], v[60:63]
	v_mfma_i32_16x16x64_i8 v[50:53], v[72:75], v[182:185], v[52:55]
	v_mfma_i32_16x16x64_i8 v[28:31], v[56:59], v[190:193], v[28:31]
	v_mfma_i32_16x16x64_i8 v[20:23], v[72:75], v[190:193], v[20:23]
	v_mfma_i32_16x16x64_i8 v[12:15], v[56:59], v[198:201], v[12:15]
	v_mfma_i32_16x16x64_i8 v[4:7], v[72:75], v[198:201], v[4:7]
	v_mfma_i32_16x16x64_i8 v[76:79], v[64:67], v[178:181], v[76:79]
	v_mfma_i32_16x16x64_i8 v[68:71], v[144:147], v[178:181], v[68:71]
	v_mfma_i32_16x16x64_i8 v[60:63], v[64:67], v[186:189], v[60:63]
	v_mfma_i32_16x16x64_i8 v[52:55], v[144:147], v[186:189], v[50:53]
	v_mfma_i32_16x16x64_i8 v[28:31], v[64:67], v[194:197], v[28:31]
	v_mfma_i32_16x16x64_i8 v[20:23], v[144:147], v[194:197], v[20:23]
	v_mfma_i32_16x16x64_i8 v[12:15], v[64:67], v[202:205], v[12:15]
	v_mfma_i32_16x16x64_i8 v[4:7], v[144:147], v[202:205], v[4:7]
	v_mfma_i32_16x16x64_i8 v[32:35], v[150:153], v[174:177], v[34:37]
	v_mfma_i32_16x16x64_i8 v[72:75], v[154:157], v[178:181], v[32:35]
	v_mfma_i32_16x16x64_i8 v[32:35], v[166:169], v[174:177], v[38:41]
	v_mfma_i32_16x16x64_i8 v[64:67], v[170:173], v[178:181], v[32:35]
	v_mfma_i32_16x16x64_i8 v[32:35], v[150:153], v[182:185], v[42:45]
	v_mfma_i32_16x16x64_i8 v[56:59], v[154:157], v[186:189], v[32:35]
	v_mfma_i32_16x16x64_i8 v[32:35], v[166:169], v[182:185], v[46:49]
	v_mfma_i32_16x16x64_i8 v[24:27], v[150:153], v[190:193], v[24:27]
	v_mfma_i32_16x16x64_i8 v[16:19], v[166:169], v[190:193], v[16:19]
	v_mfma_i32_16x16x64_i8 v[8:11], v[150:153], v[198:201], v[8:11]
	v_mfma_i32_16x16x64_i8 v[0:3], v[166:169], v[198:201], v[0:3]
	v_mfma_i32_16x16x64_i8 v[48:51], v[170:173], v[186:189], v[32:35]
	v_mfma_i32_16x16x64_i8 v[24:27], v[154:157], v[194:197], v[24:27]
	v_mfma_i32_16x16x64_i8 v[16:19], v[170:173], v[194:197], v[16:19]
	v_mfma_i32_16x16x64_i8 v[8:11], v[154:157], v[202:205], v[8:11]
	v_mfma_i32_16x16x64_i8 v[0:3], v[170:173], v[202:205], v[0:3]
	s_waitcnt vmcnt(8)
	s_barrier
	s_add_u32 s0, s0, 0x100
	s_addc_u32 s2, s2, 0
	s_add_u32 s5, s5, 0x100
	s_addc_u32 s6, s6, 0
	s_add_u32 s19, s19, 0x100
	s_addc_u32 s33, s33, 0
	s_add_u32 s74, s74, 0x100
	s_addc_u32 s75, s75, 0
	s_cmp_ge_i32 s63, s25
	s_mov_b32 s59, s63
	s_cbranch_scc0 .LBB0_179
	s_and_b64 vcc, exec, s[50:51]
	s_cbranch_vccz .LBB0_182

; #define G_STAGE(bufoff, gbase, voff) do { _Pragma("unroll") for (int _i = 0; _i < 2; ++_i) \
;         __builtin_amdgcn_global_load_lds((const unsigned*)((const char*)(gbase) + (voff)[_i]), (LAS unsigned*)(lds + (bufoff) + ldsw + _i * 8192), 16, 0, 0); } while (0)
; #define G_LDA(dst, b, h) do { _Pragma("unroll") for (int m = 0; m < 4; ++m) G_LD8(dst[m], lds + G_SA(b, h) + aoff + m * 2048); } while (0)
; #define G_LDB(dst, b, h) do { _Pragma("unroll") for (int n = 0; n < 2; ++n) G_LD8(dst[n], lds + G_SB(b, h) + boff + n * 2048); } while (0)
; #define G_WAIT_V(n) asm volatile("s_waitcnt vmcnt(" #n ")" ::: "memory")
; #define G_WAIT_L(n) asm volatile("s_waitcnt lgkmcnt(" #n ")" ::: "memory")
; #define G_BAR __builtin_amdgcn_s_barrier()
; #define G_SCHED __builtin_amdgcn_sched_barrier(0)
;     ...
;             const char* a11 = cur.a1 + (size_t)(t + 1) * kstep;
;             const char* a02 = last ? nxt.a0 : cur.a0 + (size_t)(t + 2) * kstep; const char* a12 = last ? nxt.a1 : cur.a1 + (size_t)(t + 2) * kstep;
;             const char* b02 = last ? nxt.b0 : cur.b0 + (size_t)(t + 2) * kstep; const char* b12 = last ? nxt.b1 : cur.b1 + (size_t)(t + 2) * kstep;
;             G_LDB(B0, 0, 0); G_LDB(B1, 0, 1); G_SCHED; G_LDA(At, 0, 0); G_STAGE(G_SA(1, 1), a11, vA1);
;             if constexpr (GATHER) { if (last) { int tz = tid; asm volatile("" : "+v"(tz));
; #pragma unroll
;                 for (int i = 0; i < 2; ++i) { int R, C; stage_rc(tz * 16 + i * 8192, R, C); gc0[i] = S.row_off(nxt, R, lds) + (unsigned)C * 2u; gc1[i] = S.row_off(nxt, 128 + R, lds) + (unsigned)C * 2u; } } }
;             G_WAIT_L(0); G_BAR; G_MMA(0, 0, At, B0); G_MMA(0, 1, At, B1); G_WAIT_V(8); G_BAR; G_SCHED;
;             G_LDA(At, 0, 1); G_STAGE(G_SB(0, 0), b02, voffB); G_STAGE(G_SB(0, 1), b12, voffB); G_STAGE(G_SA(0, 0), a02, vA0);
;             G_WAIT_L(0); G_BAR; G_MMA(1, 0, At, B0); G_MMA(1, 1, At, B1); G_WAIT_V(8); G_BAR; G_SCHED;
;             G_LDB(B0, 1, 0); G_LDB(B1, 1, 1); G_SCHED; G_LDA(At, 1, 0); G_STAGE(G_SA(0, 1), a12, vA1);
;             G_WAIT_L(0); G_BAR; G_MMA(0, 0, At, B0); G_MMA(0, 1, At, B1); G_WAIT_V(8); G_BAR; G_SCHED;
;             G_LDA(At, 1, 1); G_STAGE(G_SB(1, 0), b02 + kstep, voffB); G_STAGE(G_SB(1, 1), b12 + kstep, voffB); G_STAGE(G_SA(1, 0), a02 + kstep, vA0);
;             G_WAIT_L(0); G_BAR; G_MMA(1, 0, At, B0); G_MMA(1, 1, At, B1); G_WAIT_V(8); G_BAR; G_SCHED;
.LBB0_249:
	v_add_u32_e32 v144, s23, v151
	v_add_u32_e32 v166, s24, v151
	ds_read_b128 v[132:135], v144
	ds_read_b128 v[136:139], v144 offset:1024
	ds_read_b128 v[140:143], v144 offset:2048
	ds_read_b128 v[144:147], v144 offset:3072
	ds_read_b128 v[154:157], v166
	ds_read_b128 v[158:161], v166 offset:1024
	ds_read_b128 v[162:165], v166 offset:2048
	ds_read_b128 v[166:169], v166 offset:3072
	s_add_i32 s68, s58, 2
	s_add_u32 s69, s56, 0x80
	s_addc_u32 s59, s57, 0
	s_add_i32 s71, s23, s97
	s_add_i32 m0, s2, 0xc000
	s_add_i32 s70, s2, 0xe000
	s_add_i32 s72, s71, 0x2000
	s_cmp_eq_u32 s22, s58
	s_cselect_b32 s58, s46, s69
	s_cselect_b32 s61, s45, s67
	s_cselect_b32 s60, s44, s66
	s_cselect_b32 s63, s49, s55
	s_cselect_b32 s62, s48, s43
	s_cselect_b32 s59, s47, s59
	ds_read_b128 v[170:173], v152
	ds_read_b128 v[174:177], v152 offset:1024
	ds_read_b128 v[178:181], v152 offset:2048
	ds_read_b128 v[182:185], v152 offset:3072
	ds_read_b128 v[186:189], v152 offset:4096
	ds_read_b128 v[190:193], v152 offset:5120
	ds_read_b128 v[194:197], v152 offset:6144
	ds_read_b128 v[198:201], v152 offset:7168
	global_load_lds_dwordx4 v240, s[56:57]
	s_mov_b32 m0, s70
	s_nop 0
	global_load_lds_dwordx4 v242, s[56:57]
	s_waitcnt lgkmcnt(0)
	v_mov_b32_e32 v131, v129
	s_waitcnt vmcnt(8)
	s_barrier
	s_waitcnt lgkmcnt(0)
	v_mfma_i32_16x16x64_i8 v[124:127], v[132:135], v[170:173], v[124:127]
	v_mfma_i32_16x16x64_i8 v[120:123], v[140:143], v[170:173], v[120:123]
	v_mfma_i32_16x16x64_i8 v[108:111], v[132:135], v[178:181], v[108:111]
	v_mfma_i32_16x16x64_i8 v[104:107], v[140:143], v[178:181], v[104:107]
	v_mfma_i32_16x16x64_i8 v[92:95], v[132:135], v[186:189], v[92:95]
	v_mfma_i32_16x16x64_i8 v[88:91], v[140:143], v[186:189], v[88:91]
	v_mfma_i32_16x16x64_i8 v[76:79], v[132:135], v[194:197], v[76:79]
	v_mfma_i32_16x16x64_i8 v[72:75], v[140:143], v[194:197], v[72:75]
	v_mfma_i32_16x16x64_i8 v[124:127], v[136:139], v[174:177], v[124:127]
	v_mfma_i32_16x16x64_i8 v[120:123], v[144:147], v[174:177], v[120:123]
	v_mfma_i32_16x16x64_i8 v[108:111], v[136:139], v[182:185], v[108:111]
	v_mfma_i32_16x16x64_i8 v[104:107], v[144:147], v[182:185], v[104:107]
	v_mfma_i32_16x16x64_i8 v[92:95], v[136:139], v[190:193], v[92:95]
	v_mfma_i32_16x16x64_i8 v[88:91], v[144:147], v[190:193], v[88:91]
	v_mfma_i32_16x16x64_i8 v[76:79], v[136:139], v[198:201], v[76:79]
	v_mfma_i32_16x16x64_i8 v[72:75], v[144:147], v[198:201], v[72:75]
	v_mfma_i32_16x16x64_i8 v[116:119], v[154:157], v[170:173], v[116:119]
	v_mfma_i32_16x16x64_i8 v[112:115], v[162:165], v[170:173], v[112:115]
	v_mfma_i32_16x16x64_i8 v[100:103], v[154:157], v[178:181], v[100:103]
	v_mfma_i32_16x16x64_i8 v[96:99], v[162:165], v[178:181], v[96:99]
	v_mfma_i32_16x16x64_i8 v[84:87], v[154:157], v[186:189], v[84:87]
	v_mfma_i32_16x16x64_i8 v[80:83], v[162:165], v[186:189], v[80:83]
	v_mfma_i32_16x16x64_i8 v[68:71], v[154:157], v[194:197], v[68:71]
	v_mfma_i32_16x16x64_i8 v[64:67], v[162:165], v[194:197], v[64:67]
	v_mfma_i32_16x16x64_i8 v[116:119], v[158:161], v[174:177], v[116:119]
	v_mfma_i32_16x16x64_i8 v[112:115], v[166:169], v[174:177], v[112:115]
	v_mfma_i32_16x16x64_i8 v[100:103], v[158:161], v[182:185], v[100:103]
	v_mfma_i32_16x16x64_i8 v[96:99], v[166:169], v[182:185], v[96:99]
	v_mfma_i32_16x16x64_i8 v[84:87], v[158:161], v[190:193], v[84:87]
	v_mfma_i32_16x16x64_i8 v[80:83], v[166:169], v[190:193], v[80:83]
	v_mfma_i32_16x16x64_i8 v[68:71], v[158:161], v[198:201], v[68:71]
	v_mfma_i32_16x16x64_i8 v[64:67], v[166:169], v[198:201], v[64:67]
	s_waitcnt vmcnt(8)
	s_barrier
	s_mov_b32 m0, s71
	ds_read_b128 v[170:173], v152 offset:16384
	ds_read_b128 v[174:177], v152 offset:17408
	ds_read_b128 v[178:181], v152 offset:18432
	ds_read_b128 v[182:185], v152 offset:19456
	ds_read_b128 v[186:189], v152 offset:20480
	ds_read_b128 v[190:193], v152 offset:21504
	ds_read_b128 v[194:197], v152 offset:22528
	ds_read_b128 v[198:201], v152 offset:23552
	v_mov_b32_e32 v203, v129
	global_load_lds_dwordx4 v244, s[62:63]
	v_mov_b32_e32 v205, v129
	s_mov_b32 m0, s72
	v_lshl_add_u64 v[206:207], s[62:63], 0, v[244:245]
	v_lshl_add_u64 v[208:209], s[62:63], 0, v[246:247]
	global_load_lds_dwordx4 v246, s[62:63]
	s_cselect_b32 s63, s51, s65
	s_cselect_b32 s62, s50, s64
	s_add_i32 s69, s24, s97
	s_mov_b32 m0, s69
	v_lshl_add_u64 v[210:211], s[62:63], 0, v[244:245]
	global_load_lds_dwordx4 v244, s[62:63]
	s_add_i32 m0, s69, 0x2000
	v_lshl_add_u64 v[202:203], s[62:63], 0, v[246:247]
	global_load_lds_dwordx4 v246, s[62:63]
	s_mov_b32 m0, s2
	v_lshl_add_u64 v[204:205], s[60:61], 0, v[240:241]
	global_load_lds_dwordx4 v240, s[60:61]
	s_mov_b32 m0, s10
	v_lshl_add_u64 v[212:213], s[60:61], 0, v[242:243]
	global_load_lds_dwordx4 v242, s[60:61]
	s_waitcnt lgkmcnt(0)
	s_waitcnt vmcnt(8)
	s_barrier
; #define G_STAGE(bufoff, gbase, voff) do { _Pragma("unroll") for (int _i = 0; _i < 2; ++_i) \
;         __builtin_amdgcn_global_load_lds((const unsigned*)((const char*)(gbase) + (voff)[_i]), (LAS unsigned*)(lds + (bufoff) + ldsw + _i * 8192), 16, 0, 0); } while (0)
; #define G_LDA(dst, b, h) do { _Pragma("unroll") for (int m = 0; m < 4; ++m) G_LD8(dst[m], lds + G_SA(b, h) + aoff + m * 2048); } while (0)
; #define G_LDB(dst, b, h) do { _Pragma("unroll") for (int n = 0; n < 2; ++n) G_LD8(dst[n], lds + G_SB(b, h) + boff + n * 2048); } while (0)
; #define G_WAIT_V(n) asm volatile("s_waitcnt vmcnt(" #n ")" ::: "memory")
; #define G_WAIT_L(n) asm volatile("s_waitcnt lgkmcnt(" #n ")" ::: "memory")
; #define G_BAR __builtin_amdgcn_s_barrier()
; #define G_SCHED __builtin_amdgcn_sched_barrier(0)
;     __device__ __forceinline__ unsigned row_off(const Unit& u, int r, LAS unsigned char* lds) const { return (unsigned)((const LAS int*)(lds + LDS_STAGE + u.q * 4096))[r] * (unsigned)rowbytes; }
;     ...
;             G_LDB(B0, 0, 0); G_LDB(B1, 0, 1); G_SCHED; G_LDA(At, 0, 0); G_STAGE(G_SA(1, 1), a11, vA1);
;             if constexpr (GATHER) { if (last) { int tz = tid; asm volatile("" : "+v"(tz));
; #pragma unroll
;                 for (int i = 0; i < 2; ++i) { int R, C; stage_rc(tz * 16 + i * 8192, R, C); gc0[i] = S.row_off(nxt, R, lds) + (unsigned)C * 2u; gc1[i] = S.row_off(nxt, 128 + R, lds) + (unsigned)C * 2u; } } }
;             G_WAIT_L(0); G_BAR; G_MMA(0, 0, At, B0); G_MMA(0, 1, At, B1); G_WAIT_V(8); G_BAR; G_SCHED;
;             G_LDA(At, 0, 1); G_STAGE(G_SB(0, 0), b02, voffB); G_STAGE(G_SB(0, 1), b12, voffB); G_STAGE(G_SA(0, 0), a02, vA0);
;             G_WAIT_L(0); G_BAR; G_MMA(1, 0, At, B0); G_MMA(1, 1, At, B1); G_WAIT_V(8); G_BAR; G_SCHED;
;             G_LDB(B0, 1, 0); G_LDB(B1, 1, 1); G_SCHED; G_LDA(At, 1, 0); G_STAGE(G_SA(0, 1), a12, vA1);
;             G_WAIT_L(0); G_BAR; G_MMA(0, 0, At, B0); G_MMA(0, 1, At, B1); G_WAIT_V(8); G_BAR; G_SCHED;
;             G_LDA(At, 1, 1); G_STAGE(G_SB(1, 0), b02 + kstep, voffB); G_STAGE(G_SB(1, 1), b12 + kstep, voffB); G_STAGE(G_SA(1, 0), a02 + kstep, vA0);
;             G_WAIT_L(0); G_BAR; G_MMA(1, 0, At, B0); G_MMA(1, 1, At, B1); G_WAIT_V(8); G_BAR; G_SCHED;
	s_waitcnt lgkmcnt(0)
	v_mfma_i32_16x16x64_i8 v[60:63], v[132:135], v[170:173], v[60:63]
	v_mfma_i32_16x16x64_i8 v[56:59], v[140:143], v[170:173], v[56:59]
	v_mfma_i32_16x16x64_i8 v[44:47], v[132:135], v[178:181], v[44:47]
	v_mfma_i32_16x16x64_i8 v[40:43], v[140:143], v[178:181], v[40:43]
	v_mfma_i32_16x16x64_i8 v[28:31], v[132:135], v[186:189], v[28:31]
	v_mfma_i32_16x16x64_i8 v[24:27], v[140:143], v[186:189], v[24:27]
	v_mfma_i32_16x16x64_i8 v[12:15], v[132:135], v[194:197], v[12:15]
	v_mfma_i32_16x16x64_i8 v[8:11], v[140:143], v[194:197], v[8:11]
	v_mfma_i32_16x16x64_i8 v[60:63], v[136:139], v[174:177], v[60:63]
	v_mfma_i32_16x16x64_i8 v[56:59], v[144:147], v[174:177], v[56:59]
	v_mfma_i32_16x16x64_i8 v[44:47], v[136:139], v[182:185], v[44:47]
	v_mfma_i32_16x16x64_i8 v[40:43], v[144:147], v[182:185], v[40:43]
	v_mfma_i32_16x16x64_i8 v[28:31], v[136:139], v[190:193], v[28:31]
	v_mfma_i32_16x16x64_i8 v[24:27], v[144:147], v[190:193], v[24:27]
	v_mfma_i32_16x16x64_i8 v[12:15], v[136:139], v[198:201], v[12:15]
	v_mfma_i32_16x16x64_i8 v[8:11], v[144:147], v[198:201], v[8:11]
	v_mfma_i32_16x16x64_i8 v[52:55], v[154:157], v[170:173], v[52:55]
	v_mfma_i32_16x16x64_i8 v[48:51], v[162:165], v[170:173], v[48:51]
	v_mfma_i32_16x16x64_i8 v[36:39], v[154:157], v[178:181], v[36:39]
	v_mfma_i32_16x16x64_i8 v[32:35], v[162:165], v[178:181], v[32:35]
	v_mfma_i32_16x16x64_i8 v[20:23], v[154:157], v[186:189], v[20:23]
	v_mfma_i32_16x16x64_i8 v[16:19], v[162:165], v[186:189], v[16:19]
	v_mfma_i32_16x16x64_i8 v[4:7], v[154:157], v[194:197], v[4:7]
	v_mfma_i32_16x16x64_i8 v[0:3], v[162:165], v[194:197], v[0:3]
	v_mfma_i32_16x16x64_i8 v[52:55], v[158:161], v[174:177], v[52:55]
	v_mfma_i32_16x16x64_i8 v[48:51], v[166:169], v[174:177], v[48:51]
	v_mfma_i32_16x16x64_i8 v[36:39], v[158:161], v[182:185], v[36:39]
	v_mfma_i32_16x16x64_i8 v[32:35], v[166:169], v[182:185], v[32:35]
	v_mfma_i32_16x16x64_i8 v[20:23], v[158:161], v[190:193], v[20:23]
	v_mfma_i32_16x16x64_i8 v[16:19], v[166:169], v[190:193], v[16:19]
	v_mfma_i32_16x16x64_i8 v[4:7], v[158:161], v[198:201], v[4:7]
	v_mfma_i32_16x16x64_i8 v[0:3], v[166:169], v[198:201], v[0:3]
	s_waitcnt vmcnt(8)
	s_barrier
	s_add_i32 s60, 0, 0x18000
	v_add_u32_e32 v131, s60, v151
	s_add_i32 s61, 0, 0x1c000
	ds_read_b128 v[132:135], v131
	ds_read_b128 v[136:139], v131 offset:1024
	ds_read_b128 v[140:143], v131 offset:2048
	ds_read_b128 v[144:147], v131 offset:3072
	v_add_u32_e32 v131, s61, v151
	ds_read_b128 v[154:157], v131
	ds_read_b128 v[158:161], v131 offset:1024
	ds_read_b128 v[162:165], v131 offset:2048
	ds_read_b128 v[166:169], v131 offset:3072
	s_mov_b32 m0, s11
	ds_read_b128 v[170:173], v152 offset:32768
	ds_read_b128 v[174:177], v152 offset:33792
	ds_read_b128 v[178:181], v152 offset:34816
	ds_read_b128 v[182:185], v152 offset:35840
	ds_read_b128 v[186:189], v152 offset:36864
	ds_read_b128 v[190:193], v152 offset:37888
	ds_read_b128 v[194:197], v152 offset:38912
	ds_read_b128 v[198:201], v152 offset:39936
	global_load_lds_dwordx4 v240, s[58:59]
	s_mov_b32 m0, s18
	s_nop 0
	global_load_lds_dwordx4 v242, s[58:59]
	s_waitcnt lgkmcnt(0)
	s_waitcnt vmcnt(8)
	s_barrier
	s_waitcnt lgkmcnt(0)
	v_mfma_i32_16x16x64_i8 v[124:127], v[132:135], v[170:173], v[124:127]
	v_mfma_i32_16x16x64_i8 v[120:123], v[140:143], v[170:173], v[120:123]
	v_mfma_i32_16x16x64_i8 v[108:111], v[132:135], v[178:181], v[108:111]
	v_mfma_i32_16x16x64_i8 v[104:107], v[140:143], v[178:181], v[104:107]
	v_mfma_i32_16x16x64_i8 v[92:95], v[132:135], v[186:189], v[92:95]
	v_mfma_i32_16x16x64_i8 v[88:91], v[140:143], v[186:189], v[88:91]
	v_mfma_i32_16x16x64_i8 v[76:79], v[132:135], v[194:197], v[76:79]
	v_mfma_i32_16x16x64_i8 v[72:75], v[140:143], v[194:197], v[72:75]
	v_mfma_i32_16x16x64_i8 v[124:127], v[136:139], v[174:177], v[124:127]
	v_mfma_i32_16x16x64_i8 v[120:123], v[144:147], v[174:177], v[120:123]
	v_mfma_i32_16x16x64_i8 v[108:111], v[136:139], v[182:185], v[108:111]
	v_mfma_i32_16x16x64_i8 v[104:107], v[144:147], v[182:185], v[104:107]
	v_mfma_i32_16x16x64_i8 v[92:95], v[136:139], v[190:193], v[92:95]
	v_mfma_i32_16x16x64_i8 v[88:91], v[144:147], v[190:193], v[88:91]
	v_mfma_i32_16x16x64_i8 v[76:79], v[136:139], v[198:201], v[76:79]
	v_mfma_i32_16x16x64_i8 v[72:75], v[144:147], v[198:201], v[72:75]
	v_mfma_i32_16x16x64_i8 v[116:119], v[154:157], v[170:173], v[116:119]
	v_mfma_i32_16x16x64_i8 v[112:115], v[162:165], v[170:173], v[112:115]
	v_mfma_i32_16x16x64_i8 v[100:103], v[154:157], v[178:181], v[100:103]
	v_mfma_i32_16x16x64_i8 v[96:99], v[162:165], v[178:181], v[96:99]
	v_mfma_i32_16x16x64_i8 v[84:87], v[154:157], v[186:189], v[84:87]
	v_mfma_i32_16x16x64_i8 v[80:83], v[162:165], v[186:189], v[80:83]
	v_mfma_i32_16x16x64_i8 v[68:71], v[154:157], v[194:197], v[68:71]
	v_mfma_i32_16x16x64_i8 v[64:67], v[162:165], v[194:197], v[64:67]
	v_mfma_i32_16x16x64_i8 v[116:119], v[158:161], v[174:177], v[116:119]
	v_mfma_i32_16x16x64_i8 v[112:115], v[166:169], v[174:177], v[112:115]
	v_mfma_i32_16x16x64_i8 v[100:103], v[158:161], v[182:185], v[100:103]
	v_mfma_i32_16x16x64_i8 v[96:99], v[166:169], v[182:185], v[96:99]
	v_mfma_i32_16x16x64_i8 v[84:87], v[158:161], v[190:193], v[84:87]
	v_mfma_i32_16x16x64_i8 v[80:83], v[166:169], v[190:193], v[80:83]
	v_mfma_i32_16x16x64_i8 v[68:71], v[158:161], v[198:201], v[68:71]
	v_mfma_i32_16x16x64_i8 v[64:67], v[166:169], v[198:201], v[64:67]
	s_waitcnt vmcnt(8)
	s_barrier
; #define G_STAGE(bufoff, gbase, voff) do { _Pragma("unroll") for (int _i = 0; _i < 2; ++_i) \
;         __builtin_amdgcn_global_load_lds((const unsigned*)((const char*)(gbase) + (voff)[_i]), (LAS unsigned*)(lds + (bufoff) + ldsw + _i * 8192), 16, 0, 0); } while (0)
; #define G_LDA(dst, b, h) do { _Pragma("unroll") for (int m = 0; m < 4; ++m) G_LD8(dst[m], lds + G_SA(b, h) + aoff + m * 2048); } while (0)
; #define G_LDB(dst, b, h) do { _Pragma("unroll") for (int n = 0; n < 2; ++n) G_LD8(dst[n], lds + G_SB(b, h) + boff + n * 2048); } while (0)
; #define G_WAIT_V(n) asm volatile("s_waitcnt vmcnt(" #n ")" ::: "memory")
; #define G_WAIT_L(n) asm volatile("s_waitcnt lgkmcnt(" #n ")" ::: "memory")
; #define G_BAR __builtin_amdgcn_s_barrier()
; #define G_SCHED __builtin_amdgcn_sched_barrier(0)
;     ...
;             G_LDA(At, 0, 1); G_STAGE(G_SB(0, 0), b02, voffB); G_STAGE(G_SB(0, 1), b12, voffB); G_STAGE(G_SA(0, 0), a02, vA0);
;             G_WAIT_L(0); G_BAR; G_MMA(1, 0, At, B0); G_MMA(1, 1, At, B1); G_WAIT_V(8); G_BAR; G_SCHED;
;             G_LDB(B0, 1, 0); G_LDB(B1, 1, 1); G_SCHED; G_LDA(At, 1, 0); G_STAGE(G_SA(0, 1), a12, vA1);
;             G_WAIT_L(0); G_BAR; G_MMA(0, 0, At, B0); G_MMA(0, 1, At, B1); G_WAIT_V(8); G_BAR; G_SCHED;
;             G_LDA(At, 1, 1); G_STAGE(G_SB(1, 0), b02 + kstep, voffB); G_STAGE(G_SB(1, 1), b12 + kstep, voffB); G_STAGE(G_SA(1, 0), a02 + kstep, vA0);
;             G_WAIT_L(0); G_BAR; G_MMA(1, 0, At, B0); G_MMA(1, 1, At, B1); G_WAIT_V(8); G_BAR; G_SCHED;
	s_add_i32 s58, s60, s97
	v_lshl_add_u64 v[130:131], v[206:207], 0, s[8:9]
	s_mov_b32 m0, s58
	ds_read_b128 v[170:173], v152 offset:49152
	ds_read_b128 v[174:177], v152 offset:50176
	ds_read_b128 v[178:181], v152 offset:51200
	ds_read_b128 v[182:185], v152 offset:52224
	ds_read_b128 v[186:189], v152 offset:53248
	ds_read_b128 v[190:193], v152 offset:54272
	ds_read_b128 v[194:197], v152 offset:55296
	ds_read_b128 v[198:201], v152 offset:56320
	global_load_lds_dwordx4 v[130:131], off
	v_lshl_add_u64 v[130:131], v[208:209], 0, s[8:9]
	s_add_i32 m0, s58, 0x2000
	s_add_i32 s58, s61, s97
	global_load_lds_dwordx4 v[130:131], off
	v_lshl_add_u64 v[130:131], v[210:211], 0, s[8:9]
	s_mov_b32 m0, s58
	s_nop 0
	global_load_lds_dwordx4 v[130:131], off
	v_lshl_add_u64 v[130:131], v[202:203], 0, s[8:9]
	s_add_i32 m0, s58, 0x2000
	s_nop 0
	global_load_lds_dwordx4 v[130:131], off
	v_lshl_add_u64 v[130:131], v[204:205], 0, s[8:9]
	s_mov_b32 m0, s20
	s_nop 0
	global_load_lds_dwordx4 v[130:131], off
	v_lshl_add_u64 v[130:131], v[212:213], 0, s[8:9]
	s_mov_b32 m0, s21
	s_nop 0
	global_load_lds_dwordx4 v[130:131], off
	s_waitcnt lgkmcnt(0)
	s_waitcnt vmcnt(8)
	s_barrier
	s_waitcnt lgkmcnt(0)
	v_mfma_i32_16x16x64_i8 v[60:63], v[132:135], v[170:173], v[60:63]
	v_mfma_i32_16x16x64_i8 v[56:59], v[140:143], v[170:173], v[56:59]
	v_mfma_i32_16x16x64_i8 v[44:47], v[132:135], v[178:181], v[44:47]
	v_mfma_i32_16x16x64_i8 v[40:43], v[140:143], v[178:181], v[40:43]
	v_mfma_i32_16x16x64_i8 v[28:31], v[132:135], v[186:189], v[28:31]
	v_mfma_i32_16x16x64_i8 v[24:27], v[140:143], v[186:189], v[24:27]
	v_mfma_i32_16x16x64_i8 v[12:15], v[132:135], v[194:197], v[12:15]
	v_mfma_i32_16x16x64_i8 v[8:11], v[140:143], v[194:197], v[8:11]
	v_mfma_i32_16x16x64_i8 v[60:63], v[136:139], v[174:177], v[60:63]
	v_mfma_i32_16x16x64_i8 v[56:59], v[144:147], v[174:177], v[56:59]
	v_mfma_i32_16x16x64_i8 v[44:47], v[136:139], v[182:185], v[44:47]
	v_mfma_i32_16x16x64_i8 v[40:43], v[144:147], v[182:185], v[40:43]
	v_mfma_i32_16x16x64_i8 v[28:31], v[136:139], v[190:193], v[28:31]
	v_mfma_i32_16x16x64_i8 v[24:27], v[144:147], v[190:193], v[24:27]
	v_mfma_i32_16x16x64_i8 v[12:15], v[136:139], v[198:201], v[12:15]
	v_mfma_i32_16x16x64_i8 v[8:11], v[144:147], v[198:201], v[8:11]
	v_mfma_i32_16x16x64_i8 v[52:55], v[154:157], v[170:173], v[52:55]
	v_mfma_i32_16x16x64_i8 v[48:51], v[162:165], v[170:173], v[48:51]
	v_mfma_i32_16x16x64_i8 v[36:39], v[154:157], v[178:181], v[36:39]
	v_mfma_i32_16x16x64_i8 v[32:35], v[162:165], v[178:181], v[32:35]
	v_mfma_i32_16x16x64_i8 v[20:23], v[154:157], v[186:189], v[20:23]
	v_mfma_i32_16x16x64_i8 v[16:19], v[162:165], v[186:189], v[16:19]
	v_mfma_i32_16x16x64_i8 v[4:7], v[154:157], v[194:197], v[4:7]
	v_mfma_i32_16x16x64_i8 v[0:3], v[162:165], v[194:197], v[0:3]
	v_mfma_i32_16x16x64_i8 v[52:55], v[158:161], v[174:177], v[52:55]
	v_mfma_i32_16x16x64_i8 v[48:51], v[166:169], v[174:177], v[48:51]
	v_mfma_i32_16x16x64_i8 v[36:39], v[158:161], v[182:185], v[36:39]
	v_mfma_i32_16x16x64_i8 v[32:35], v[166:169], v[182:185], v[32:35]
	v_mfma_i32_16x16x64_i8 v[20:23], v[158:161], v[190:193], v[20:23]
	v_mfma_i32_16x16x64_i8 v[16:19], v[166:169], v[190:193], v[16:19]
	v_mfma_i32_16x16x64_i8 v[4:7], v[158:161], v[198:201], v[4:7]
	v_mfma_i32_16x16x64_i8 v[0:3], v[166:169], v[198:201], v[0:3]
	s_waitcnt vmcnt(8)
	s_barrier
	s_add_u32 s43, s43, 0x100
	s_addc_u32 s55, s55, 0
	s_add_u32 s64, s64, 0x100
	s_addc_u32 s65, s65, 0
	s_add_u32 s66, s66, 0x100
	s_addc_u32 s67, s67, 0
	s_add_u32 s56, s56, 0x100
	s_addc_u32 s57, s57, 0
	s_cmp_ge_i32 s68, s0
	s_mov_b32 s58, s68
	s_cbranch_scc0 .LBB0_249
	s_and_b64 vcc, exec, s[40:41]
	s_cbranch_vccz .LBB0_252

; #define G_STAGE(bufoff, gbase, voff) do { _Pragma("unroll") for (int _i = 0; _i < 2; ++_i) \
;         __builtin_amdgcn_global_load_lds((const unsigned*)((const char*)(gbase) + (voff)[_i]), (LAS unsigned*)(lds + (bufoff) + ldsw + _i * 8192), 16, 0, 0); } while (0)
; #define G_LDA(dst, b, h) do { _Pragma("unroll") for (int m = 0; m < 4; ++m) G_LD8(dst[m], lds + G_SA(b, h) + aoff + m * 2048); } while (0)
; #define G_LDB(dst, b, h) do { _Pragma("unroll") for (int n = 0; n < 2; ++n) G_LD8(dst[n], lds + G_SB(b, h) + boff + n * 2048); } while (0)
; #define G_WAIT_V(n) asm volatile("s_waitcnt vmcnt(" #n ")" ::: "memory")
; #define G_WAIT_L(n) asm volatile("s_waitcnt lgkmcnt(" #n ")" ::: "memory")
; #define G_BAR __builtin_amdgcn_s_barrier()
; #define G_SCHED __builtin_amdgcn_sched_barrier(0)
;     ...
;             const char* a11 = cur.a1 + (size_t)(t + 1) * kstep;
;             const char* a02 = last ? nxt.a0 : cur.a0 + (size_t)(t + 2) * kstep; const char* a12 = last ? nxt.a1 : cur.a1 + (size_t)(t + 2) * kstep;
;             const char* b02 = last ? nxt.b0 : cur.b0 + (size_t)(t + 2) * kstep; const char* b12 = last ? nxt.b1 : cur.b1 + (size_t)(t + 2) * kstep;
;             G_LDB(B0, 0, 0); G_LDB(B1, 0, 1); G_SCHED; G_LDA(At, 0, 0); G_STAGE(G_SA(1, 1), a11, vA1);
;             if constexpr (GATHER) { if (last) { int tz = tid; asm volatile("" : "+v"(tz));
; #pragma unroll
;                 for (int i = 0; i < 2; ++i) { int R, C; stage_rc(tz * 16 + i * 8192, R, C); gc0[i] = S.row_off(nxt, R, lds) + (unsigned)C * 2u; gc1[i] = S.row_off(nxt, 128 + R, lds) + (unsigned)C * 2u; } } }
;             G_WAIT_L(0); G_BAR; G_MMA(0, 0, At, B0); G_MMA(0, 1, At, B1); G_WAIT_V(8); G_BAR; G_SCHED;
;             G_LDA(At, 0, 1); G_STAGE(G_SB(0, 0), b02, voffB); G_STAGE(G_SB(0, 1), b12, voffB); G_STAGE(G_SA(0, 0), a02, vA0);
;             G_WAIT_L(0); G_BAR; G_MMA(1, 0, At, B0); G_MMA(1, 1, At, B1); G_WAIT_V(8); G_BAR; G_SCHED;
;             G_LDB(B0, 1, 0); G_LDB(B1, 1, 1); G_SCHED; G_LDA(At, 1, 0); G_STAGE(G_SA(0, 1), a12, vA1);
;             G_WAIT_L(0); G_BAR; G_MMA(0, 0, At, B0); G_MMA(0, 1, At, B1); G_WAIT_V(8); G_BAR; G_SCHED;
;             G_LDA(At, 1, 1); G_STAGE(G_SB(1, 0), b02 + kstep, voffB); G_STAGE(G_SB(1, 1), b12 + kstep, voffB); G_STAGE(G_SA(1, 0), a02 + kstep, vA0);
;             G_WAIT_L(0); G_BAR; G_MMA(1, 0, At, B0); G_MMA(1, 1, At, B1); G_WAIT_V(8); G_BAR; G_SCHED;
.LBB0_284:
	v_add_u32_e32 v144, s24, v157
	v_add_u32_e32 v168, s25, v157
	ds_read_b128 v[100:103], v144
	ds_read_b128 v[112:115], v144 offset:1024
	ds_read_b128 v[120:123], v144 offset:2048
	ds_read_b128 v[144:147], v144 offset:3072
	ds_read_b128 v[150:153], v168
	ds_read_b128 v[160:163], v168 offset:1024
	ds_read_b128 v[164:167], v168 offset:2048
	ds_read_b128 v[168:171], v168 offset:3072
	s_add_i32 s76, s64, 2
	s_add_u32 s77, s62, 0x80
	s_addc_u32 s65, s63, 0
	s_add_i32 s79, s24, s97
	s_add_i32 m0, s0, 0xc000
	s_add_i32 s78, s0, 0xe000
	s_add_i32 s80, s79, 0x2000
	s_cmp_eq_u32 s23, s64
	s_cselect_b32 s64, s50, s77
	s_cselect_b32 s67, s49, s75
	s_cselect_b32 s66, s48, s71
	s_cselect_b32 s69, s53, s59
	s_cselect_b32 s68, s52, s45
	s_cselect_b32 s65, s51, s65
	ds_read_b128 v[172:175], v158
	ds_read_b128 v[176:179], v158 offset:1024
	ds_read_b128 v[180:183], v158 offset:2048
	ds_read_b128 v[184:187], v158 offset:3072
	ds_read_b128 v[188:191], v158 offset:4096
	ds_read_b128 v[192:195], v158 offset:5120
	ds_read_b128 v[196:199], v158 offset:6144
	ds_read_b128 v[200:203], v158 offset:7168
	global_load_lds_dwordx4 v240, s[62:63]
	s_mov_b32 m0, s78
	s_nop 0
	global_load_lds_dwordx4 v242, s[62:63]
	s_waitcnt lgkmcnt(0)
	v_mov_b32_e32 v93, v149
	s_waitcnt vmcnt(8)
	s_barrier
	s_waitcnt lgkmcnt(0)
	v_mfma_i32_16x16x64_i8 v[140:143], v[100:103], v[172:175], v[140:143]
	v_mfma_i32_16x16x64_i8 v[132:135], v[120:123], v[172:175], v[132:135]
	v_mfma_i32_16x16x64_i8 v[94:97], v[100:103], v[180:183], v[96:99]
	v_mfma_i32_16x16x64_i8 v[88:91], v[120:123], v[180:183], v[88:91]
	v_mfma_i32_16x16x64_i8 v[60:63], v[100:103], v[188:191], v[60:63]
	v_mfma_i32_16x16x64_i8 v[56:59], v[120:123], v[188:191], v[56:59]
	v_mfma_i32_16x16x64_i8 v[28:31], v[100:103], v[196:199], v[28:31]
	v_mfma_i32_16x16x64_i8 v[24:27], v[120:123], v[196:199], v[24:27]
	v_mfma_i32_16x16x64_i8 v[140:143], v[112:115], v[176:179], v[140:143]
	v_mfma_i32_16x16x64_i8 v[132:135], v[144:147], v[176:179], v[132:135]
	v_mfma_i32_16x16x64_i8 v[94:97], v[112:115], v[184:187], v[94:97]
	v_mfma_i32_16x16x64_i8 v[88:91], v[144:147], v[184:187], v[88:91]
	v_mfma_i32_16x16x64_i8 v[60:63], v[112:115], v[192:195], v[60:63]
	v_mfma_i32_16x16x64_i8 v[56:59], v[144:147], v[192:195], v[56:59]
	v_mfma_i32_16x16x64_i8 v[28:31], v[112:115], v[200:203], v[28:31]
	v_mfma_i32_16x16x64_i8 v[24:27], v[144:147], v[200:203], v[24:27]
	v_mfma_i32_16x16x64_i8 v[124:127], v[150:153], v[172:175], v[124:127]
	v_mfma_i32_16x16x64_i8 v[108:111], v[164:167], v[172:175], v[108:111]
	v_mfma_i32_16x16x64_i8 v[76:79], v[150:153], v[180:183], v[76:79]
	v_mfma_i32_16x16x64_i8 v[72:75], v[164:167], v[180:183], v[72:75]
	v_mfma_i32_16x16x64_i8 v[44:47], v[150:153], v[188:191], v[44:47]
	v_mfma_i32_16x16x64_i8 v[40:43], v[164:167], v[188:191], v[40:43]
	v_mfma_i32_16x16x64_i8 v[12:15], v[150:153], v[196:199], v[12:15]
	v_mfma_i32_16x16x64_i8 v[8:11], v[164:167], v[196:199], v[8:11]
	v_mfma_i32_16x16x64_i8 v[124:127], v[160:163], v[176:179], v[124:127]
	v_mfma_i32_16x16x64_i8 v[108:111], v[168:171], v[176:179], v[108:111]
	v_mfma_i32_16x16x64_i8 v[76:79], v[160:163], v[184:187], v[76:79]
	v_mfma_i32_16x16x64_i8 v[72:75], v[168:171], v[184:187], v[72:75]
	v_mfma_i32_16x16x64_i8 v[44:47], v[160:163], v[192:195], v[44:47]
	v_mfma_i32_16x16x64_i8 v[40:43], v[168:171], v[192:195], v[40:43]
	v_mfma_i32_16x16x64_i8 v[12:15], v[160:163], v[200:203], v[12:15]
	v_mfma_i32_16x16x64_i8 v[8:11], v[168:171], v[200:203], v[8:11]
	s_waitcnt vmcnt(8)
	s_barrier
	s_mov_b32 m0, s79
	ds_read_b128 v[172:175], v158 offset:16384
	ds_read_b128 v[176:179], v158 offset:17408
	ds_read_b128 v[180:183], v158 offset:18432
	ds_read_b128 v[184:187], v158 offset:19456
	ds_read_b128 v[188:191], v158 offset:20480
	ds_read_b128 v[192:195], v158 offset:21504
	ds_read_b128 v[196:199], v158 offset:22528
	ds_read_b128 v[200:203], v158 offset:23552
	v_mov_b32_e32 v205, v149
	global_load_lds_dwordx4 v244, s[68:69]
	v_mov_b32_e32 v207, v149
	s_mov_b32 m0, s80
	v_lshl_add_u64 v[208:209], s[68:69], 0, v[244:245]
	v_lshl_add_u64 v[210:211], s[68:69], 0, v[246:247]
	global_load_lds_dwordx4 v246, s[68:69]
	s_cselect_b32 s69, s55, s70
	s_cselect_b32 s68, s54, s61
	s_add_i32 s77, s25, s97
	s_mov_b32 m0, s77
	v_lshl_add_u64 v[212:213], s[68:69], 0, v[244:245]
	global_load_lds_dwordx4 v244, s[68:69]
	s_add_i32 m0, s77, 0x2000
	v_lshl_add_u64 v[204:205], s[68:69], 0, v[246:247]
	global_load_lds_dwordx4 v246, s[68:69]
	s_mov_b32 m0, s0
	v_lshl_add_u64 v[206:207], s[66:67], 0, v[240:241]
	global_load_lds_dwordx4 v240, s[66:67]
	s_mov_b32 m0, s11
	v_lshl_add_u64 v[214:215], s[66:67], 0, v[242:243]
	global_load_lds_dwordx4 v242, s[66:67]
	s_waitcnt lgkmcnt(0)
	s_waitcnt vmcnt(8)
	s_barrier
; #define G_STAGE(bufoff, gbase, voff) do { _Pragma("unroll") for (int _i = 0; _i < 2; ++_i) \
;         __builtin_amdgcn_global_load_lds((const unsigned*)((const char*)(gbase) + (voff)[_i]), (LAS unsigned*)(lds + (bufoff) + ldsw + _i * 8192), 16, 0, 0); } while (0)
; #define G_LDA(dst, b, h) do { _Pragma("unroll") for (int m = 0; m < 4; ++m) G_LD8(dst[m], lds + G_SA(b, h) + aoff + m * 2048); } while (0)
; #define G_LDB(dst, b, h) do { _Pragma("unroll") for (int n = 0; n < 2; ++n) G_LD8(dst[n], lds + G_SB(b, h) + boff + n * 2048); } while (0)
; #define G_WAIT_V(n) asm volatile("s_waitcnt vmcnt(" #n ")" ::: "memory")
; #define G_WAIT_L(n) asm volatile("s_waitcnt lgkmcnt(" #n ")" ::: "memory")
; #define G_BAR __builtin_amdgcn_s_barrier()
; #define G_SCHED __builtin_amdgcn_sched_barrier(0)
;     __device__ __forceinline__ unsigned row_off(const Unit& u, int r, LAS unsigned char* lds) const { return (unsigned)((const LAS int*)(lds + LDS_STAGE + u.q * 4096))[r] * (unsigned)rowbytes; }
;     ...
;             G_LDB(B0, 0, 0); G_LDB(B1, 0, 1); G_SCHED; G_LDA(At, 0, 0); G_STAGE(G_SA(1, 1), a11, vA1);
;             if constexpr (GATHER) { if (last) { int tz = tid; asm volatile("" : "+v"(tz));
; #pragma unroll
;                 for (int i = 0; i < 2; ++i) { int R, C; stage_rc(tz * 16 + i * 8192, R, C); gc0[i] = S.row_off(nxt, R, lds) + (unsigned)C * 2u; gc1[i] = S.row_off(nxt, 128 + R, lds) + (unsigned)C * 2u; } } }
;             G_WAIT_L(0); G_BAR; G_MMA(0, 0, At, B0); G_MMA(0, 1, At, B1); G_WAIT_V(8); G_BAR; G_SCHED;
;             G_LDA(At, 0, 1); G_STAGE(G_SB(0, 0), b02, voffB); G_STAGE(G_SB(0, 1), b12, voffB); G_STAGE(G_SA(0, 0), a02, vA0);
;             G_WAIT_L(0); G_BAR; G_MMA(1, 0, At, B0); G_MMA(1, 1, At, B1); G_WAIT_V(8); G_BAR; G_SCHED;
;             G_LDB(B0, 1, 0); G_LDB(B1, 1, 1); G_SCHED; G_LDA(At, 1, 0); G_STAGE(G_SA(0, 1), a12, vA1);
;             G_WAIT_L(0); G_BAR; G_MMA(0, 0, At, B0); G_MMA(0, 1, At, B1); G_WAIT_V(8); G_BAR; G_SCHED;
;             G_LDA(At, 1, 1); G_STAGE(G_SB(1, 0), b02 + kstep, voffB); G_STAGE(G_SB(1, 1), b12 + kstep, voffB); G_STAGE(G_SA(1, 0), a02 + kstep, vA0);
;             G_WAIT_L(0); G_BAR; G_MMA(1, 0, At, B0); G_MMA(1, 1, At, B1); G_WAIT_V(8); G_BAR; G_SCHED;
	s_waitcnt lgkmcnt(0)
	v_mfma_i32_16x16x64_i8 v[136:139], v[100:103], v[172:175], v[136:139]
	v_mfma_i32_16x16x64_i8 v[128:131], v[120:123], v[172:175], v[128:131]
	v_mfma_i32_16x16x64_i8 v[84:87], v[100:103], v[180:183], v[84:87]
	v_mfma_i32_16x16x64_i8 v[80:83], v[120:123], v[180:183], v[80:83]
	v_mfma_i32_16x16x64_i8 v[52:55], v[100:103], v[188:191], v[52:55]
	v_mfma_i32_16x16x64_i8 v[48:51], v[120:123], v[188:191], v[48:51]
	v_mfma_i32_16x16x64_i8 v[20:23], v[100:103], v[196:199], v[20:23]
	v_mfma_i32_16x16x64_i8 v[16:19], v[120:123], v[196:199], v[16:19]
	v_mfma_i32_16x16x64_i8 v[136:139], v[112:115], v[176:179], v[136:139]
	v_mfma_i32_16x16x64_i8 v[128:131], v[144:147], v[176:179], v[128:131]
	v_mfma_i32_16x16x64_i8 v[84:87], v[112:115], v[184:187], v[84:87]
	v_mfma_i32_16x16x64_i8 v[80:83], v[144:147], v[184:187], v[80:83]
	v_mfma_i32_16x16x64_i8 v[52:55], v[112:115], v[192:195], v[52:55]
	v_mfma_i32_16x16x64_i8 v[48:51], v[144:147], v[192:195], v[48:51]
	v_mfma_i32_16x16x64_i8 v[20:23], v[112:115], v[200:203], v[20:23]
	v_mfma_i32_16x16x64_i8 v[16:19], v[144:147], v[200:203], v[16:19]
	v_mfma_i32_16x16x64_i8 v[104:107], v[164:167], v[172:175], v[104:107]
	v_mfma_i32_16x16x64_i8 v[68:71], v[150:153], v[180:183], v[68:71]
	v_mfma_i32_16x16x64_i8 v[64:67], v[164:167], v[180:183], v[64:67]
	v_mfma_i32_16x16x64_i8 v[36:39], v[150:153], v[188:191], v[36:39]
	v_mfma_i32_16x16x64_i8 v[32:35], v[164:167], v[188:191], v[32:35]
	v_mfma_i32_16x16x64_i8 v[4:7], v[150:153], v[196:199], v[4:7]
	v_mfma_i32_16x16x64_i8 v[0:3], v[164:167], v[196:199], v[0:3]
	v_mfma_i32_16x16x64_i8 v[98:101], v[150:153], v[172:175], v[116:119]
	v_mfma_i32_16x16x64_i8 v[104:107], v[168:171], v[176:179], v[104:107]
	v_mfma_i32_16x16x64_i8 v[68:71], v[160:163], v[184:187], v[68:71]
	v_mfma_i32_16x16x64_i8 v[64:67], v[168:171], v[184:187], v[64:67]
	v_mfma_i32_16x16x64_i8 v[36:39], v[160:163], v[192:195], v[36:39]
	v_mfma_i32_16x16x64_i8 v[32:35], v[168:171], v[192:195], v[32:35]
	v_mfma_i32_16x16x64_i8 v[4:7], v[160:163], v[200:203], v[4:7]
	v_mfma_i32_16x16x64_i8 v[0:3], v[168:171], v[200:203], v[0:3]
	v_mfma_i32_16x16x64_i8 v[100:103], v[160:163], v[176:179], v[98:101]
	s_waitcnt vmcnt(8)
	s_barrier
	s_add_i32 s66, 0, 0x18000
	v_add_u32_e32 v93, s66, v157
	s_add_i32 s67, 0, 0x1c000
	ds_read_b128 v[112:115], v93
	ds_read_b128 v[116:119], v93 offset:1024
	ds_read_b128 v[120:123], v93 offset:2048
	ds_read_b128 v[144:147], v93 offset:3072
	v_add_u32_e32 v93, s67, v157
	ds_read_b128 v[150:153], v93
	ds_read_b128 v[160:163], v93 offset:1024
	ds_read_b128 v[164:167], v93 offset:2048
	ds_read_b128 v[168:171], v93 offset:3072
	s_mov_b32 m0, s18
	ds_read_b128 v[172:175], v158 offset:32768
	ds_read_b128 v[176:179], v158 offset:33792
	ds_read_b128 v[180:183], v158 offset:34816
	ds_read_b128 v[184:187], v158 offset:35840
	ds_read_b128 v[188:191], v158 offset:36864
	ds_read_b128 v[192:195], v158 offset:37888
	ds_read_b128 v[196:199], v158 offset:38912
	ds_read_b128 v[200:203], v158 offset:39936
	global_load_lds_dwordx4 v240, s[64:65]
	s_mov_b32 m0, s19
	s_nop 0
	global_load_lds_dwordx4 v242, s[64:65]
	s_waitcnt lgkmcnt(0)
	s_waitcnt vmcnt(8)
	s_barrier
	s_waitcnt lgkmcnt(0)
	v_mfma_i32_16x16x64_i8 v[140:143], v[112:115], v[172:175], v[140:143]
	v_mfma_i32_16x16x64_i8 v[132:135], v[120:123], v[172:175], v[132:135]
	v_mfma_i32_16x16x64_i8 v[92:95], v[112:115], v[180:183], v[94:97]
	v_mfma_i32_16x16x64_i8 v[88:91], v[120:123], v[180:183], v[88:91]
	v_mfma_i32_16x16x64_i8 v[60:63], v[112:115], v[188:191], v[60:63]
	v_mfma_i32_16x16x64_i8 v[56:59], v[120:123], v[188:191], v[56:59]
	v_mfma_i32_16x16x64_i8 v[28:31], v[112:115], v[196:199], v[28:31]
	v_mfma_i32_16x16x64_i8 v[24:27], v[120:123], v[196:199], v[24:27]
	v_mfma_i32_16x16x64_i8 v[140:143], v[116:119], v[176:179], v[140:143]
	v_mfma_i32_16x16x64_i8 v[132:135], v[144:147], v[176:179], v[132:135]
	v_mfma_i32_16x16x64_i8 v[96:99], v[116:119], v[184:187], v[92:95]
	v_mfma_i32_16x16x64_i8 v[88:91], v[144:147], v[184:187], v[88:91]
	v_mfma_i32_16x16x64_i8 v[60:63], v[116:119], v[192:195], v[60:63]
	v_mfma_i32_16x16x64_i8 v[56:59], v[144:147], v[192:195], v[56:59]
	v_mfma_i32_16x16x64_i8 v[28:31], v[116:119], v[200:203], v[28:31]
	v_mfma_i32_16x16x64_i8 v[24:27], v[144:147], v[200:203], v[24:27]
	v_mfma_i32_16x16x64_i8 v[92:95], v[150:153], v[172:175], v[124:127]
	v_mfma_i32_16x16x64_i8 v[124:127], v[160:163], v[176:179], v[92:95]
	v_mfma_i32_16x16x64_i8 v[92:95], v[164:167], v[172:175], v[108:111]
	v_mfma_i32_16x16x64_i8 v[76:79], v[150:153], v[180:183], v[76:79]
	v_mfma_i32_16x16x64_i8 v[72:75], v[164:167], v[180:183], v[72:75]
	v_mfma_i32_16x16x64_i8 v[44:47], v[150:153], v[188:191], v[44:47]
	v_mfma_i32_16x16x64_i8 v[40:43], v[164:167], v[188:191], v[40:43]
	v_mfma_i32_16x16x64_i8 v[12:15], v[150:153], v[196:199], v[12:15]
	v_mfma_i32_16x16x64_i8 v[8:11], v[164:167], v[196:199], v[8:11]
	v_mfma_i32_16x16x64_i8 v[108:111], v[168:171], v[176:179], v[92:95]
	v_mfma_i32_16x16x64_i8 v[76:79], v[160:163], v[184:187], v[76:79]
	v_mfma_i32_16x16x64_i8 v[72:75], v[168:171], v[184:187], v[72:75]
	v_mfma_i32_16x16x64_i8 v[44:47], v[160:163], v[192:195], v[44:47]
	v_mfma_i32_16x16x64_i8 v[40:43], v[168:171], v[192:195], v[40:43]
	v_mfma_i32_16x16x64_i8 v[12:15], v[160:163], v[200:203], v[12:15]
	v_mfma_i32_16x16x64_i8 v[8:11], v[168:171], v[200:203], v[8:11]
	s_waitcnt vmcnt(8)
	s_barrier
; #define G_STAGE(bufoff, gbase, voff) do { _Pragma("unroll") for (int _i = 0; _i < 2; ++_i) \
;         __builtin_amdgcn_global_load_lds((const unsigned*)((const char*)(gbase) + (voff)[_i]), (LAS unsigned*)(lds + (bufoff) + ldsw + _i * 8192), 16, 0, 0); } while (0)
; #define G_LDA(dst, b, h) do { _Pragma("unroll") for (int m = 0; m < 4; ++m) G_LD8(dst[m], lds + G_SA(b, h) + aoff + m * 2048); } while (0)
; #define G_LDB(dst, b, h) do { _Pragma("unroll") for (int n = 0; n < 2; ++n) G_LD8(dst[n], lds + G_SB(b, h) + boff + n * 2048); } while (0)
; #define G_WAIT_V(n) asm volatile("s_waitcnt vmcnt(" #n ")" ::: "memory")
; #define G_WAIT_L(n) asm volatile("s_waitcnt lgkmcnt(" #n ")" ::: "memory")
; #define G_BAR __builtin_amdgcn_s_barrier()
; #define G_SCHED __builtin_amdgcn_sched_barrier(0)
;     ...
;             G_LDA(At, 0, 1); G_STAGE(G_SB(0, 0), b02, voffB); G_STAGE(G_SB(0, 1), b12, voffB); G_STAGE(G_SA(0, 0), a02, vA0);
;             G_WAIT_L(0); G_BAR; G_MMA(1, 0, At, B0); G_MMA(1, 1, At, B1); G_WAIT_V(8); G_BAR; G_SCHED;
;             G_LDB(B0, 1, 0); G_LDB(B1, 1, 1); G_SCHED; G_LDA(At, 1, 0); G_STAGE(G_SA(0, 1), a12, vA1);
;             G_WAIT_L(0); G_BAR; G_MMA(0, 0, At, B0); G_MMA(0, 1, At, B1); G_WAIT_V(8); G_BAR; G_SCHED;
;             G_LDA(At, 1, 1); G_STAGE(G_SB(1, 0), b02 + kstep, voffB); G_STAGE(G_SB(1, 1), b12 + kstep, voffB); G_STAGE(G_SA(1, 0), a02 + kstep, vA0);
;             G_WAIT_L(0); G_BAR; G_MMA(1, 0, At, B0); G_MMA(1, 1, At, B1); G_WAIT_V(8); G_BAR; G_SCHED;
	s_add_i32 s64, s66, s97
	v_lshl_add_u64 v[200:201], v[208:209], 0, s[38:39]
	s_mov_b32 m0, s64
	ds_read_b128 v[92:95], v158 offset:49152
	ds_read_b128 v[172:175], v158 offset:50176
	ds_read_b128 v[176:179], v158 offset:51200
	ds_read_b128 v[180:183], v158 offset:52224
	ds_read_b128 v[184:187], v158 offset:53248
	ds_read_b128 v[188:191], v158 offset:54272
	ds_read_b128 v[192:195], v158 offset:55296
	ds_read_b128 v[196:199], v158 offset:56320
	global_load_lds_dwordx4 v[200:201], off
	v_lshl_add_u64 v[200:201], v[210:211], 0, s[38:39]
	s_add_i32 m0, s64, 0x2000
	s_add_i32 s64, s67, s97
	global_load_lds_dwordx4 v[200:201], off
	v_lshl_add_u64 v[200:201], v[212:213], 0, s[38:39]
	s_mov_b32 m0, s64
	s_nop 0
	global_load_lds_dwordx4 v[200:201], off
	v_lshl_add_u64 v[200:201], v[204:205], 0, s[38:39]
	s_add_i32 m0, s64, 0x2000
	s_nop 0
	global_load_lds_dwordx4 v[200:201], off
	v_lshl_add_u64 v[200:201], v[206:207], 0, s[38:39]
	s_mov_b32 m0, s21
	s_nop 0
	global_load_lds_dwordx4 v[200:201], off
	v_lshl_add_u64 v[200:201], v[214:215], 0, s[38:39]
	s_mov_b32 m0, s22
	s_nop 0
	global_load_lds_dwordx4 v[200:201], off
	s_waitcnt lgkmcnt(0)
	s_waitcnt vmcnt(8)
	s_barrier
	s_waitcnt lgkmcnt(0)
	v_mfma_i32_16x16x64_i8 v[136:139], v[112:115], v[92:95], v[136:139]
	v_mfma_i32_16x16x64_i8 v[128:131], v[120:123], v[92:95], v[128:131]
	v_mfma_i32_16x16x64_i8 v[84:87], v[112:115], v[176:179], v[84:87]
	v_mfma_i32_16x16x64_i8 v[80:83], v[120:123], v[176:179], v[80:83]
	v_mfma_i32_16x16x64_i8 v[52:55], v[112:115], v[184:187], v[52:55]
	v_mfma_i32_16x16x64_i8 v[48:51], v[120:123], v[184:187], v[48:51]
	v_mfma_i32_16x16x64_i8 v[20:23], v[112:115], v[192:195], v[20:23]
	v_mfma_i32_16x16x64_i8 v[16:19], v[120:123], v[192:195], v[16:19]
	v_mfma_i32_16x16x64_i8 v[136:139], v[116:119], v[172:175], v[136:139]
	v_mfma_i32_16x16x64_i8 v[128:131], v[144:147], v[172:175], v[128:131]
	v_mfma_i32_16x16x64_i8 v[84:87], v[116:119], v[180:183], v[84:87]
	v_mfma_i32_16x16x64_i8 v[80:83], v[144:147], v[180:183], v[80:83]
	v_mfma_i32_16x16x64_i8 v[52:55], v[116:119], v[188:191], v[52:55]
	v_mfma_i32_16x16x64_i8 v[48:51], v[144:147], v[188:191], v[48:51]
	v_mfma_i32_16x16x64_i8 v[20:23], v[116:119], v[196:199], v[20:23]
	v_mfma_i32_16x16x64_i8 v[16:19], v[144:147], v[196:199], v[16:19]
	v_mfma_i32_16x16x64_i8 v[100:103], v[150:153], v[92:95], v[100:103]
	v_mfma_i32_16x16x64_i8 v[92:95], v[164:167], v[92:95], v[104:107]
	v_mfma_i32_16x16x64_i8 v[68:71], v[150:153], v[176:179], v[68:71]
	v_mfma_i32_16x16x64_i8 v[64:67], v[164:167], v[176:179], v[64:67]
	v_mfma_i32_16x16x64_i8 v[36:39], v[150:153], v[184:187], v[36:39]
	v_mfma_i32_16x16x64_i8 v[32:35], v[164:167], v[184:187], v[32:35]
	v_mfma_i32_16x16x64_i8 v[4:7], v[150:153], v[192:195], v[4:7]
	v_mfma_i32_16x16x64_i8 v[0:3], v[164:167], v[192:195], v[0:3]
	v_mfma_i32_16x16x64_i8 v[116:119], v[160:163], v[172:175], v[100:103]
	v_mfma_i32_16x16x64_i8 v[104:107], v[168:171], v[172:175], v[92:95]
	v_mfma_i32_16x16x64_i8 v[68:71], v[160:163], v[180:183], v[68:71]
	v_mfma_i32_16x16x64_i8 v[64:67], v[168:171], v[180:183], v[64:67]
	v_mfma_i32_16x16x64_i8 v[36:39], v[160:163], v[188:191], v[36:39]
	v_mfma_i32_16x16x64_i8 v[32:35], v[168:171], v[188:191], v[32:35]
	v_mfma_i32_16x16x64_i8 v[4:7], v[160:163], v[196:199], v[4:7]
	v_mfma_i32_16x16x64_i8 v[0:3], v[168:171], v[196:199], v[0:3]
	s_waitcnt vmcnt(8)
	s_barrier
	s_add_u32 s45, s45, 0x100
	s_addc_u32 s59, s59, 0
	s_add_u32 s61, s61, 0x100
	s_addc_u32 s70, s70, 0
	s_add_u32 s71, s71, 0x100
	s_addc_u32 s75, s75, 0
	s_add_u32 s62, s62, 0x100
	s_addc_u32 s63, s63, 0
	s_cmp_ge_i32 s76, s3
	s_mov_b32 s64, s76
	s_cbranch_scc0 .LBB0_284
	v_readlane_b32 s78, v255, 11
	v_readlane_b32 s79, v255, 13
	s_branch .LBB0_289

; #define G_STAGE(bufoff, gbase, voff) do { _Pragma("unroll") for (int _i = 0; _i < 2; ++_i) \
;         __builtin_amdgcn_global_load_lds((const unsigned*)((const char*)(gbase) + (voff)[_i]), (LAS unsigned*)(lds + (bufoff) + ldsw + _i * 8192), 16, 0, 0); } while (0)
; #define G_LDA(dst, b, h) do { _Pragma("unroll") for (int m = 0; m < 4; ++m) G_LD8(dst[m], lds + G_SA(b, h) + aoff + m * 2048); } while (0)
; #define G_LDB(dst, b, h) do { _Pragma("unroll") for (int n = 0; n < 2; ++n) G_LD8(dst[n], lds + G_SB(b, h) + boff + n * 2048); } while (0)
; #define G_WAIT_V(n) asm volatile("s_waitcnt vmcnt(" #n ")" ::: "memory")
; #define G_WAIT_L(n) asm volatile("s_waitcnt lgkmcnt(" #n ")" ::: "memory")
; #define G_BAR __builtin_amdgcn_s_barrier()
; #define G_SCHED __builtin_amdgcn_sched_barrier(0)
;     ...
;             const char* a11 = cur.a1 + (size_t)(t + 1) * kstep;
;             const char* a02 = last ? nxt.a0 : cur.a0 + (size_t)(t + 2) * kstep; const char* a12 = last ? nxt.a1 : cur.a1 + (size_t)(t + 2) * kstep;
;             const char* b02 = last ? nxt.b0 : cur.b0 + (size_t)(t + 2) * kstep; const char* b12 = last ? nxt.b1 : cur.b1 + (size_t)(t + 2) * kstep;
;             G_LDB(B0, 0, 0); G_LDB(B1, 0, 1); G_SCHED; G_LDA(At, 0, 0); G_STAGE(G_SA(1, 1), a11, vA1);
;             if constexpr (GATHER) { if (last) { int tz = tid; asm volatile("" : "+v"(tz));
; #pragma unroll
;                 for (int i = 0; i < 2; ++i) { int R, C; stage_rc(tz * 16 + i * 8192, R, C); gc0[i] = S.row_off(nxt, R, lds) + (unsigned)C * 2u; gc1[i] = S.row_off(nxt, 128 + R, lds) + (unsigned)C * 2u; } } }
;             G_WAIT_L(0); G_BAR; G_MMA(0, 0, At, B0); G_MMA(0, 1, At, B1); G_WAIT_V(8); G_BAR; G_SCHED;
;             G_LDA(At, 0, 1); G_STAGE(G_SB(0, 0), b02, voffB); G_STAGE(G_SB(0, 1), b12, voffB); G_STAGE(G_SA(0, 0), a02, vA0);
;             G_WAIT_L(0); G_BAR; G_MMA(1, 0, At, B0); G_MMA(1, 1, At, B1); G_WAIT_V(8); G_BAR; G_SCHED;
;             G_LDB(B0, 1, 0); G_LDB(B1, 1, 1); G_SCHED; G_LDA(At, 1, 0); G_STAGE(G_SA(0, 1), a12, vA1);
;             G_WAIT_L(0); G_BAR; G_MMA(0, 0, At, B0); G_MMA(0, 1, At, B1); G_WAIT_V(8); G_BAR; G_SCHED;
;             G_LDA(At, 1, 1); G_STAGE(G_SB(1, 0), b02 + kstep, voffB); G_STAGE(G_SB(1, 1), b12 + kstep, voffB); G_STAGE(G_SA(1, 0), a02 + kstep, vA0);
;             G_WAIT_L(0); G_BAR; G_MMA(1, 0, At, B0); G_MMA(1, 1, At, B1); G_WAIT_V(8); G_BAR; G_SCHED;
.LBB0_522:
	s_add_i32 s79, s56, 2
	ds_read_b128 v[142:145], v138
	ds_read_b128 v[146:149], v138 offset:1024
	ds_read_b128 v[150:153], v138 offset:2048
	ds_read_b128 v[154:157], v138 offset:3072
	ds_read_b128 v[158:161], v139
	ds_read_b128 v[162:165], v139 offset:1024
	ds_read_b128 v[166:169], v139 offset:2048
	ds_read_b128 v[170:173], v139 offset:3072
	s_add_u32 s80, s54, 0x80
	s_addc_u32 s57, s55, 0
	s_add_i32 s82, s72, s20
	s_add_i32 m0, s27, 0xc000
	s_add_i32 s81, s27, 0xe000
	s_add_i32 s83, s82, 0x2000
	s_cmp_eq_u32 s71, s56
	s_cselect_b32 s56, s48, s80
	s_cselect_b32 s59, s51, s78
	s_cselect_b32 s58, s50, s77
	s_cselect_b32 s61, s45, s63
	s_cselect_b32 s60, s44, s62
	s_cselect_b32 s57, s49, s57
	ds_read_b128 v[174:177], v140
	ds_read_b128 v[178:181], v140 offset:1024
	ds_read_b128 v[182:185], v140 offset:2048
	ds_read_b128 v[186:189], v140 offset:3072
	ds_read_b128 v[190:193], v140 offset:4096
	ds_read_b128 v[194:197], v140 offset:5120
	ds_read_b128 v[198:201], v140 offset:6144
	ds_read_b128 v[202:205], v140 offset:7168
	global_load_lds_dwordx4 v240, s[54:55]
	s_mov_b32 m0, s81
	s_nop 0
	global_load_lds_dwordx4 v242, s[54:55]
	s_waitcnt lgkmcnt(0)
	v_mov_b32_e32 v131, v129
	s_waitcnt vmcnt(8)
	s_barrier
	s_waitcnt lgkmcnt(0)
	v_mfma_f32_16x16x32_bf16 v[124:127], v[142:145], v[174:177], v[124:127]
	v_mfma_f32_16x16x32_bf16 v[120:123], v[150:153], v[174:177], v[120:123]
	v_mfma_f32_16x16x32_bf16 v[92:95], v[142:145], v[182:185], v[92:95]
	v_mfma_f32_16x16x32_bf16 v[88:91], v[150:153], v[182:185], v[88:91]
	v_mfma_f32_16x16x32_bf16 v[60:63], v[142:145], v[190:193], v[60:63]
	v_mfma_f32_16x16x32_bf16 v[56:59], v[150:153], v[190:193], v[56:59]
	v_mfma_f32_16x16x32_bf16 v[28:31], v[142:145], v[198:201], v[28:31]
	v_mfma_f32_16x16x32_bf16 v[24:27], v[150:153], v[198:201], v[24:27]
	v_mfma_f32_16x16x32_bf16 v[124:127], v[146:149], v[178:181], v[124:127]
	v_mfma_f32_16x16x32_bf16 v[120:123], v[154:157], v[178:181], v[120:123]
	v_mfma_f32_16x16x32_bf16 v[92:95], v[146:149], v[186:189], v[92:95]
	v_mfma_f32_16x16x32_bf16 v[88:91], v[154:157], v[186:189], v[88:91]
	v_mfma_f32_16x16x32_bf16 v[60:63], v[146:149], v[194:197], v[60:63]
	v_mfma_f32_16x16x32_bf16 v[56:59], v[154:157], v[194:197], v[56:59]
	v_mfma_f32_16x16x32_bf16 v[28:31], v[146:149], v[202:205], v[28:31]
	v_mfma_f32_16x16x32_bf16 v[24:27], v[154:157], v[202:205], v[24:27]
	v_mfma_f32_16x16x32_bf16 v[112:115], v[158:161], v[174:177], v[112:115]
	v_mfma_f32_16x16x32_bf16 v[104:107], v[166:169], v[174:177], v[104:107]
	v_mfma_f32_16x16x32_bf16 v[80:83], v[158:161], v[182:185], v[80:83]
	v_mfma_f32_16x16x32_bf16 v[72:75], v[166:169], v[182:185], v[72:75]
	v_mfma_f32_16x16x32_bf16 v[48:51], v[158:161], v[190:193], v[48:51]
	v_mfma_f32_16x16x32_bf16 v[40:43], v[166:169], v[190:193], v[40:43]
	v_mfma_f32_16x16x32_bf16 v[16:19], v[158:161], v[198:201], v[16:19]
	v_mfma_f32_16x16x32_bf16 v[8:11], v[166:169], v[198:201], v[8:11]
	v_mfma_f32_16x16x32_bf16 v[112:115], v[162:165], v[178:181], v[112:115]
	v_mfma_f32_16x16x32_bf16 v[104:107], v[170:173], v[178:181], v[104:107]
	v_mfma_f32_16x16x32_bf16 v[80:83], v[162:165], v[186:189], v[80:83]
	v_mfma_f32_16x16x32_bf16 v[72:75], v[170:173], v[186:189], v[72:75]
	v_mfma_f32_16x16x32_bf16 v[48:51], v[162:165], v[194:197], v[48:51]
	v_mfma_f32_16x16x32_bf16 v[40:43], v[170:173], v[194:197], v[40:43]
	v_mfma_f32_16x16x32_bf16 v[16:19], v[162:165], v[202:205], v[16:19]
	v_mfma_f32_16x16x32_bf16 v[8:11], v[170:173], v[202:205], v[8:11]
	s_waitcnt vmcnt(8)
	s_barrier
	s_mov_b32 m0, s82
	ds_read_b128 v[174:177], v140 offset:16384
	ds_read_b128 v[178:181], v140 offset:17408
	ds_read_b128 v[182:185], v140 offset:18432
	ds_read_b128 v[186:189], v140 offset:19456
	ds_read_b128 v[190:193], v140 offset:20480
	ds_read_b128 v[194:197], v140 offset:21504
	ds_read_b128 v[198:201], v140 offset:22528
	ds_read_b128 v[202:205], v140 offset:23552
	v_mov_b32_e32 v133, v129
	global_load_lds_dwordx4 v244, s[60:61]
	v_mov_b32_e32 v207, v129
	s_mov_b32 m0, s83
	v_lshl_add_u64 v[208:209], s[60:61], 0, v[244:245]
	v_lshl_add_u64 v[210:211], s[60:61], 0, v[246:247]
	global_load_lds_dwordx4 v246, s[60:61]
	s_cselect_b32 s61, s47, s75
	s_cselect_b32 s60, s46, s64
	s_add_i32 s80, s73, s20
	s_mov_b32 m0, s80
	v_lshl_add_u64 v[212:213], s[60:61], 0, v[244:245]
	global_load_lds_dwordx4 v244, s[60:61]
	s_add_i32 m0, s80, 0x2000
	v_lshl_add_u64 v[214:215], s[60:61], 0, v[246:247]
	global_load_lds_dwordx4 v246, s[60:61]
	s_mov_b32 m0, s27
	v_lshl_add_u64 v[206:207], s[58:59], 0, v[240:241]
	global_load_lds_dwordx4 v240, s[58:59]
	s_mov_b32 m0, s33
	v_lshl_add_u64 v[216:217], s[58:59], 0, v[242:243]
	global_load_lds_dwordx4 v242, s[58:59]
	s_waitcnt lgkmcnt(0)
	s_waitcnt vmcnt(8)
	s_barrier
; #define G_STAGE(bufoff, gbase, voff) do { _Pragma("unroll") for (int _i = 0; _i < 2; ++_i) \
;         __builtin_amdgcn_global_load_lds((const unsigned*)((const char*)(gbase) + (voff)[_i]), (LAS unsigned*)(lds + (bufoff) + ldsw + _i * 8192), 16, 0, 0); } while (0)
; #define G_LDA(dst, b, h) do { _Pragma("unroll") for (int m = 0; m < 4; ++m) G_LD8(dst[m], lds + G_SA(b, h) + aoff + m * 2048); } while (0)
; #define G_LDB(dst, b, h) do { _Pragma("unroll") for (int n = 0; n < 2; ++n) G_LD8(dst[n], lds + G_SB(b, h) + boff + n * 2048); } while (0)
; #define G_WAIT_V(n) asm volatile("s_waitcnt vmcnt(" #n ")" ::: "memory")
; #define G_WAIT_L(n) asm volatile("s_waitcnt lgkmcnt(" #n ")" ::: "memory")
; #define G_BAR __builtin_amdgcn_s_barrier()
; #define G_SCHED __builtin_amdgcn_sched_barrier(0)
;     __device__ __forceinline__ unsigned row_off(const Unit& u, int r, LAS unsigned char* lds) const { return (unsigned)((const LAS int*)(lds + LDS_STAGE + u.q * 4096))[r] * (unsigned)rowbytes; }
;     ...
;             G_LDB(B0, 0, 0); G_LDB(B1, 0, 1); G_SCHED; G_LDA(At, 0, 0); G_STAGE(G_SA(1, 1), a11, vA1);
;             if constexpr (GATHER) { if (last) { int tz = tid; asm volatile("" : "+v"(tz));
; #pragma unroll
;                 for (int i = 0; i < 2; ++i) { int R, C; stage_rc(tz * 16 + i * 8192, R, C); gc0[i] = S.row_off(nxt, R, lds) + (unsigned)C * 2u; gc1[i] = S.row_off(nxt, 128 + R, lds) + (unsigned)C * 2u; } } }
;             G_WAIT_L(0); G_BAR; G_MMA(0, 0, At, B0); G_MMA(0, 1, At, B1); G_WAIT_V(8); G_BAR; G_SCHED;
;             G_LDA(At, 0, 1); G_STAGE(G_SB(0, 0), b02, voffB); G_STAGE(G_SB(0, 1), b12, voffB); G_STAGE(G_SA(0, 0), a02, vA0);
;             G_WAIT_L(0); G_BAR; G_MMA(1, 0, At, B0); G_MMA(1, 1, At, B1); G_WAIT_V(8); G_BAR; G_SCHED;
;             G_LDB(B0, 1, 0); G_LDB(B1, 1, 1); G_SCHED; G_LDA(At, 1, 0); G_STAGE(G_SA(0, 1), a12, vA1);
;             G_WAIT_L(0); G_BAR; G_MMA(0, 0, At, B0); G_MMA(0, 1, At, B1); G_WAIT_V(8); G_BAR; G_SCHED;
;             G_LDA(At, 1, 1); G_STAGE(G_SB(1, 0), b02 + kstep, voffB); G_STAGE(G_SB(1, 1), b12 + kstep, voffB); G_STAGE(G_SA(1, 0), a02 + kstep, vA0);
;             G_WAIT_L(0); G_BAR; G_MMA(1, 0, At, B0); G_MMA(1, 1, At, B1); G_WAIT_V(8); G_BAR; G_SCHED;
	s_waitcnt lgkmcnt(0)
	v_mfma_f32_16x16x32_bf16 v[116:119], v[142:145], v[174:177], v[116:119]
	v_mfma_f32_16x16x32_bf16 v[108:111], v[150:153], v[174:177], v[108:111]
	v_mfma_f32_16x16x32_bf16 v[84:87], v[142:145], v[182:185], v[84:87]
	v_mfma_f32_16x16x32_bf16 v[76:79], v[150:153], v[182:185], v[76:79]
	v_mfma_f32_16x16x32_bf16 v[52:55], v[142:145], v[190:193], v[52:55]
	v_mfma_f32_16x16x32_bf16 v[44:47], v[150:153], v[190:193], v[44:47]
	v_mfma_f32_16x16x32_bf16 v[20:23], v[142:145], v[198:201], v[20:23]
	v_mfma_f32_16x16x32_bf16 v[12:15], v[150:153], v[198:201], v[12:15]
	v_mfma_f32_16x16x32_bf16 v[116:119], v[146:149], v[178:181], v[116:119]
	v_mfma_f32_16x16x32_bf16 v[108:111], v[154:157], v[178:181], v[108:111]
	v_mfma_f32_16x16x32_bf16 v[84:87], v[146:149], v[186:189], v[84:87]
	v_mfma_f32_16x16x32_bf16 v[76:79], v[154:157], v[186:189], v[76:79]
	v_mfma_f32_16x16x32_bf16 v[52:55], v[146:149], v[194:197], v[52:55]
	v_mfma_f32_16x16x32_bf16 v[44:47], v[154:157], v[194:197], v[44:47]
	v_mfma_f32_16x16x32_bf16 v[20:23], v[146:149], v[202:205], v[20:23]
	v_mfma_f32_16x16x32_bf16 v[12:15], v[154:157], v[202:205], v[12:15]
	v_mfma_f32_16x16x32_bf16 v[100:103], v[158:161], v[174:177], v[100:103]
	v_mfma_f32_16x16x32_bf16 v[96:99], v[166:169], v[174:177], v[96:99]
	v_mfma_f32_16x16x32_bf16 v[68:71], v[158:161], v[182:185], v[68:71]
	v_mfma_f32_16x16x32_bf16 v[64:67], v[166:169], v[182:185], v[64:67]
	v_mfma_f32_16x16x32_bf16 v[36:39], v[158:161], v[190:193], v[36:39]
	v_mfma_f32_16x16x32_bf16 v[32:35], v[166:169], v[190:193], v[32:35]
	v_mfma_f32_16x16x32_bf16 v[4:7], v[158:161], v[198:201], v[4:7]
	v_mfma_f32_16x16x32_bf16 v[0:3], v[166:169], v[198:201], v[0:3]
	v_mfma_f32_16x16x32_bf16 v[100:103], v[162:165], v[178:181], v[100:103]
	v_mfma_f32_16x16x32_bf16 v[96:99], v[170:173], v[178:181], v[96:99]
	v_mfma_f32_16x16x32_bf16 v[68:71], v[162:165], v[186:189], v[68:71]
	v_mfma_f32_16x16x32_bf16 v[64:67], v[170:173], v[186:189], v[64:67]
	v_mfma_f32_16x16x32_bf16 v[36:39], v[162:165], v[194:197], v[36:39]
	v_mfma_f32_16x16x32_bf16 v[32:35], v[170:173], v[194:197], v[32:35]
	v_mfma_f32_16x16x32_bf16 v[4:7], v[162:165], v[202:205], v[4:7]
	v_mfma_f32_16x16x32_bf16 v[0:3], v[170:173], v[202:205], v[0:3]
	s_waitcnt vmcnt(8)
	s_barrier
	s_add_i32 s58, 0, 0x18000
	v_add_u32_e32 v131, s58, v137
	s_add_i32 s59, 0, 0x1c000
	ds_read_b128 v[142:145], v131
	ds_read_b128 v[146:149], v131 offset:1024
	ds_read_b128 v[150:153], v131 offset:2048
	ds_read_b128 v[154:157], v131 offset:3072
	v_add_u32_e32 v131, s59, v137
	ds_read_b128 v[158:161], v131
	ds_read_b128 v[162:165], v131 offset:1024
	ds_read_b128 v[166:169], v131 offset:2048
	ds_read_b128 v[170:173], v131 offset:3072
	s_mov_b32 m0, s66
	ds_read_b128 v[174:177], v140 offset:32768
	ds_read_b128 v[178:181], v140 offset:33792
	ds_read_b128 v[182:185], v140 offset:34816
	ds_read_b128 v[186:189], v140 offset:35840
	ds_read_b128 v[190:193], v140 offset:36864
	ds_read_b128 v[194:197], v140 offset:37888
	ds_read_b128 v[198:201], v140 offset:38912
	ds_read_b128 v[202:205], v140 offset:39936
	global_load_lds_dwordx4 v240, s[56:57]
	s_mov_b32 m0, s67
	s_nop 0
	global_load_lds_dwordx4 v242, s[56:57]
	s_waitcnt lgkmcnt(0)
	s_waitcnt vmcnt(8)
	s_barrier
	s_waitcnt lgkmcnt(0)
	v_mfma_f32_16x16x32_bf16 v[124:127], v[142:145], v[174:177], v[124:127]
	v_mfma_f32_16x16x32_bf16 v[120:123], v[150:153], v[174:177], v[120:123]
	v_mfma_f32_16x16x32_bf16 v[92:95], v[142:145], v[182:185], v[92:95]
	v_mfma_f32_16x16x32_bf16 v[88:91], v[150:153], v[182:185], v[88:91]
	v_mfma_f32_16x16x32_bf16 v[60:63], v[142:145], v[190:193], v[60:63]
	v_mfma_f32_16x16x32_bf16 v[56:59], v[150:153], v[190:193], v[56:59]
	v_mfma_f32_16x16x32_bf16 v[28:31], v[142:145], v[198:201], v[28:31]
	v_mfma_f32_16x16x32_bf16 v[24:27], v[150:153], v[198:201], v[24:27]
	v_mfma_f32_16x16x32_bf16 v[124:127], v[146:149], v[178:181], v[124:127]
	v_mfma_f32_16x16x32_bf16 v[120:123], v[154:157], v[178:181], v[120:123]
	v_mfma_f32_16x16x32_bf16 v[92:95], v[146:149], v[186:189], v[92:95]
	v_mfma_f32_16x16x32_bf16 v[88:91], v[154:157], v[186:189], v[88:91]
	v_mfma_f32_16x16x32_bf16 v[60:63], v[146:149], v[194:197], v[60:63]
	v_mfma_f32_16x16x32_bf16 v[56:59], v[154:157], v[194:197], v[56:59]
	v_mfma_f32_16x16x32_bf16 v[28:31], v[146:149], v[202:205], v[28:31]
	v_mfma_f32_16x16x32_bf16 v[24:27], v[154:157], v[202:205], v[24:27]
	v_mfma_f32_16x16x32_bf16 v[112:115], v[158:161], v[174:177], v[112:115]
	v_mfma_f32_16x16x32_bf16 v[104:107], v[166:169], v[174:177], v[104:107]
	v_mfma_f32_16x16x32_bf16 v[80:83], v[158:161], v[182:185], v[80:83]
	v_mfma_f32_16x16x32_bf16 v[72:75], v[166:169], v[182:185], v[72:75]
	v_mfma_f32_16x16x32_bf16 v[48:51], v[158:161], v[190:193], v[48:51]
	v_mfma_f32_16x16x32_bf16 v[40:43], v[166:169], v[190:193], v[40:43]
	v_mfma_f32_16x16x32_bf16 v[16:19], v[158:161], v[198:201], v[16:19]
	v_mfma_f32_16x16x32_bf16 v[8:11], v[166:169], v[198:201], v[8:11]
	v_mfma_f32_16x16x32_bf16 v[112:115], v[162:165], v[178:181], v[112:115]
	v_mfma_f32_16x16x32_bf16 v[104:107], v[170:173], v[178:181], v[104:107]
	v_mfma_f32_16x16x32_bf16 v[80:83], v[162:165], v[186:189], v[80:83]
	v_mfma_f32_16x16x32_bf16 v[72:75], v[170:173], v[186:189], v[72:75]
	v_mfma_f32_16x16x32_bf16 v[48:51], v[162:165], v[194:197], v[48:51]
	v_mfma_f32_16x16x32_bf16 v[40:43], v[170:173], v[194:197], v[40:43]
	v_mfma_f32_16x16x32_bf16 v[16:19], v[162:165], v[202:205], v[16:19]
	v_mfma_f32_16x16x32_bf16 v[8:11], v[170:173], v[202:205], v[8:11]
	s_waitcnt vmcnt(8)
	s_barrier
; #define G_STAGE(bufoff, gbase, voff) do { _Pragma("unroll") for (int _i = 0; _i < 2; ++_i) \
;         __builtin_amdgcn_global_load_lds((const unsigned*)((const char*)(gbase) + (voff)[_i]), (LAS unsigned*)(lds + (bufoff) + ldsw + _i * 8192), 16, 0, 0); } while (0)
; #define G_LDA(dst, b, h) do { _Pragma("unroll") for (int m = 0; m < 4; ++m) G_LD8(dst[m], lds + G_SA(b, h) + aoff + m * 2048); } while (0)
; #define G_LDB(dst, b, h) do { _Pragma("unroll") for (int n = 0; n < 2; ++n) G_LD8(dst[n], lds + G_SB(b, h) + boff + n * 2048); } while (0)
; #define G_WAIT_V(n) asm volatile("s_waitcnt vmcnt(" #n ")" ::: "memory")
; #define G_WAIT_L(n) asm volatile("s_waitcnt lgkmcnt(" #n ")" ::: "memory")
; #define G_BAR __builtin_amdgcn_s_barrier()
; #define G_SCHED __builtin_amdgcn_sched_barrier(0)
;     ...
;             G_LDA(At, 0, 1); G_STAGE(G_SB(0, 0), b02, voffB); G_STAGE(G_SB(0, 1), b12, voffB); G_STAGE(G_SA(0, 0), a02, vA0);
;             G_WAIT_L(0); G_BAR; G_MMA(1, 0, At, B0); G_MMA(1, 1, At, B1); G_WAIT_V(8); G_BAR; G_SCHED;
;             G_LDB(B0, 1, 0); G_LDB(B1, 1, 1); G_SCHED; G_LDA(At, 1, 0); G_STAGE(G_SA(0, 1), a12, vA1);
;             G_WAIT_L(0); G_BAR; G_MMA(0, 0, At, B0); G_MMA(0, 1, At, B1); G_WAIT_V(8); G_BAR; G_SCHED;
;             G_LDA(At, 1, 1); G_STAGE(G_SB(1, 0), b02 + kstep, voffB); G_STAGE(G_SB(1, 1), b12 + kstep, voffB); G_STAGE(G_SA(1, 0), a02 + kstep, vA0);
;             G_WAIT_L(0); G_BAR; G_MMA(1, 0, At, B0); G_MMA(1, 1, At, B1); G_WAIT_V(8); G_BAR; G_SCHED;
	s_add_i32 s56, s58, s20
	v_lshl_add_u64 v[202:203], v[208:209], 0, s[40:41]
	s_mov_b32 m0, s56
	ds_read_b128 v[130:133], v140 offset:49152
	ds_read_b128 v[174:177], v140 offset:50176
	ds_read_b128 v[178:181], v140 offset:51200
	ds_read_b128 v[182:185], v140 offset:52224
	ds_read_b128 v[186:189], v140 offset:53248
	ds_read_b128 v[190:193], v140 offset:54272
	ds_read_b128 v[194:197], v140 offset:55296
	ds_read_b128 v[198:201], v140 offset:56320
	global_load_lds_dwordx4 v[202:203], off
	v_lshl_add_u64 v[202:203], v[210:211], 0, s[40:41]
	s_add_i32 m0, s56, 0x2000
	s_add_i32 s56, s59, s20
	global_load_lds_dwordx4 v[202:203], off
	v_lshl_add_u64 v[202:203], v[212:213], 0, s[40:41]
	s_mov_b32 m0, s56
	s_nop 0
	global_load_lds_dwordx4 v[202:203], off
	v_lshl_add_u64 v[202:203], v[214:215], 0, s[40:41]
	s_add_i32 m0, s56, 0x2000
	s_nop 0
	global_load_lds_dwordx4 v[202:203], off
	v_lshl_add_u64 v[202:203], v[206:207], 0, s[40:41]
	s_mov_b32 m0, s69
	s_nop 0
	global_load_lds_dwordx4 v[202:203], off
	v_lshl_add_u64 v[202:203], v[216:217], 0, s[40:41]
	s_mov_b32 m0, s70
	s_nop 0
	global_load_lds_dwordx4 v[202:203], off
	s_waitcnt lgkmcnt(0)
	s_waitcnt vmcnt(8)
	s_barrier
	s_waitcnt lgkmcnt(0)
	v_mfma_f32_16x16x32_bf16 v[116:119], v[142:145], v[130:133], v[116:119]
	v_mfma_f32_16x16x32_bf16 v[108:111], v[150:153], v[130:133], v[108:111]
	v_mfma_f32_16x16x32_bf16 v[84:87], v[142:145], v[178:181], v[84:87]
	v_mfma_f32_16x16x32_bf16 v[76:79], v[150:153], v[178:181], v[76:79]
	v_mfma_f32_16x16x32_bf16 v[52:55], v[142:145], v[186:189], v[52:55]
	v_mfma_f32_16x16x32_bf16 v[44:47], v[150:153], v[186:189], v[44:47]
	v_mfma_f32_16x16x32_bf16 v[20:23], v[142:145], v[194:197], v[20:23]
	v_mfma_f32_16x16x32_bf16 v[12:15], v[150:153], v[194:197], v[12:15]
	v_mfma_f32_16x16x32_bf16 v[116:119], v[146:149], v[174:177], v[116:119]
	v_mfma_f32_16x16x32_bf16 v[108:111], v[154:157], v[174:177], v[108:111]
	v_mfma_f32_16x16x32_bf16 v[84:87], v[146:149], v[182:185], v[84:87]
	v_mfma_f32_16x16x32_bf16 v[76:79], v[154:157], v[182:185], v[76:79]
	v_mfma_f32_16x16x32_bf16 v[52:55], v[146:149], v[190:193], v[52:55]
	v_mfma_f32_16x16x32_bf16 v[44:47], v[154:157], v[190:193], v[44:47]
	v_mfma_f32_16x16x32_bf16 v[20:23], v[146:149], v[198:201], v[20:23]
	v_mfma_f32_16x16x32_bf16 v[12:15], v[154:157], v[198:201], v[12:15]
	v_mfma_f32_16x16x32_bf16 v[100:103], v[158:161], v[130:133], v[100:103]
	v_mfma_f32_16x16x32_bf16 v[96:99], v[166:169], v[130:133], v[96:99]
	v_mfma_f32_16x16x32_bf16 v[68:71], v[158:161], v[178:181], v[68:71]
	v_mfma_f32_16x16x32_bf16 v[64:67], v[166:169], v[178:181], v[64:67]
	v_mfma_f32_16x16x32_bf16 v[36:39], v[158:161], v[186:189], v[36:39]
	v_mfma_f32_16x16x32_bf16 v[32:35], v[166:169], v[186:189], v[32:35]
	v_mfma_f32_16x16x32_bf16 v[4:7], v[158:161], v[194:197], v[4:7]
	v_mfma_f32_16x16x32_bf16 v[0:3], v[166:169], v[194:197], v[0:3]
	v_mfma_f32_16x16x32_bf16 v[100:103], v[162:165], v[174:177], v[100:103]
	v_mfma_f32_16x16x32_bf16 v[96:99], v[170:173], v[174:177], v[96:99]
	v_mfma_f32_16x16x32_bf16 v[68:71], v[162:165], v[182:185], v[68:71]
	v_mfma_f32_16x16x32_bf16 v[64:67], v[170:173], v[182:185], v[64:67]
	v_mfma_f32_16x16x32_bf16 v[36:39], v[162:165], v[190:193], v[36:39]
	v_mfma_f32_16x16x32_bf16 v[32:35], v[170:173], v[190:193], v[32:35]
	v_mfma_f32_16x16x32_bf16 v[4:7], v[162:165], v[198:201], v[4:7]
	v_mfma_f32_16x16x32_bf16 v[0:3], v[170:173], v[198:201], v[0:3]
	s_waitcnt vmcnt(8)
	s_barrier
	s_add_u32 s62, s62, 0x100
	s_addc_u32 s63, s63, 0
	s_add_u32 s64, s64, 0x100
	s_addc_u32 s75, s75, 0
	s_add_u32 s77, s77, 0x100
	s_addc_u32 s78, s78, 0
	s_add_u32 s54, s54, 0x100
	s_addc_u32 s55, s55, 0
	s_cmp_ge_i32 s79, s0
	s_mov_b32 s56, s79
	s_cbranch_scc0 .LBB0_522
	v_readlane_b32 s78, v255, 11
	v_readlane_b32 s79, v255, 13
	s_and_b64 vcc, exec, s[42:43]
	s_cbranch_vccz .LBB0_525

; #define G_STAGE(bufoff, gbase, voff) do { _Pragma("unroll") for (int _i = 0; _i < 2; ++_i) \
;         __builtin_amdgcn_global_load_lds((const unsigned*)((const char*)(gbase) + (voff)[_i]), (LAS unsigned*)(lds + (bufoff) + ldsw + _i * 8192), 16, 0, 0); } while (0)
; #define G_LDA(dst, b, h) do { _Pragma("unroll") for (int m = 0; m < 4; ++m) G_LD8(dst[m], lds + G_SA(b, h) + aoff + m * 2048); } while (0)
; #define G_LDB(dst, b, h) do { _Pragma("unroll") for (int n = 0; n < 2; ++n) G_LD8(dst[n], lds + G_SB(b, h) + boff + n * 2048); } while (0)
; #define G_WAIT_V(n) asm volatile("s_waitcnt vmcnt(" #n ")" ::: "memory")
; #define G_WAIT_L(n) asm volatile("s_waitcnt lgkmcnt(" #n ")" ::: "memory")
; #define G_BAR __builtin_amdgcn_s_barrier()
; #define G_SCHED __builtin_amdgcn_sched_barrier(0)
;     ...
;             const char* a11 = cur.a1 + (size_t)(t + 1) * kstep;
;             const char* a02 = last ? nxt.a0 : cur.a0 + (size_t)(t + 2) * kstep; const char* a12 = last ? nxt.a1 : cur.a1 + (size_t)(t + 2) * kstep;
;             const char* b02 = last ? nxt.b0 : cur.b0 + (size_t)(t + 2) * kstep; const char* b12 = last ? nxt.b1 : cur.b1 + (size_t)(t + 2) * kstep;
;             G_LDB(B0, 0, 0); G_LDB(B1, 0, 1); G_SCHED; G_LDA(At, 0, 0); G_STAGE(G_SA(1, 1), a11, vA1);
;             if constexpr (GATHER) { if (last) { int tz = tid; asm volatile("" : "+v"(tz));
; #pragma unroll
;                 for (int i = 0; i < 2; ++i) { int R, C; stage_rc(tz * 16 + i * 8192, R, C); gc0[i] = S.row_off(nxt, R, lds) + (unsigned)C * 2u; gc1[i] = S.row_off(nxt, 128 + R, lds) + (unsigned)C * 2u; } } }
;             G_WAIT_L(0); G_BAR; G_MMA(0, 0, At, B0); G_MMA(0, 1, At, B1); G_WAIT_V(8); G_BAR; G_SCHED;
;             G_LDA(At, 0, 1); G_STAGE(G_SB(0, 0), b02, voffB); G_STAGE(G_SB(0, 1), b12, voffB); G_STAGE(G_SA(0, 0), a02, vA0);
;             G_WAIT_L(0); G_BAR; G_MMA(1, 0, At, B0); G_MMA(1, 1, At, B1); G_WAIT_V(8); G_BAR; G_SCHED;
;             G_LDB(B0, 1, 0); G_LDB(B1, 1, 1); G_SCHED; G_LDA(At, 1, 0); G_STAGE(G_SA(0, 1), a12, vA1);
;             G_WAIT_L(0); G_BAR; G_MMA(0, 0, At, B0); G_MMA(0, 1, At, B1); G_WAIT_V(8); G_BAR; G_SCHED;
;             G_LDA(At, 1, 1); G_STAGE(G_SB(1, 0), b02 + kstep, voffB); G_STAGE(G_SB(1, 1), b12 + kstep, voffB); G_STAGE(G_SA(1, 0), a02 + kstep, vA0);
;             G_WAIT_L(0); G_BAR; G_MMA(1, 0, At, B0); G_MMA(1, 1, At, B1); G_WAIT_V(8); G_BAR; G_SCHED;
.LBB0_549:
	s_add_i32 s80, s58, 2
	ds_read_b128 v[130:133], v138
	ds_read_b128 v[142:145], v138 offset:1024
	ds_read_b128 v[146:149], v138 offset:2048
	ds_read_b128 v[150:153], v138 offset:3072
	ds_read_b128 v[154:157], v139
	ds_read_b128 v[158:161], v139 offset:1024
	ds_read_b128 v[162:165], v139 offset:2048
	ds_read_b128 v[166:169], v139 offset:3072
	s_add_u32 s81, s56, 0x80
	s_addc_u32 s59, s57, 0
	s_add_i32 s83, s75, s20
	s_add_i32 m0, s67, 0xc000
	s_add_i32 s82, s67, 0xe000
	s_add_i32 s84, s83, 0x2000
	s_cmp_eq_u32 s74, s58
	s_cselect_b32 s58, s44, s81
	s_cselect_b32 s61, s43, s79
	s_cselect_b32 s60, s42, s65
	s_cselect_b32 s63, s47, s53
	s_cselect_b32 s62, s46, s41
	s_cselect_b32 s59, s45, s59
	ds_read_b128 v[170:173], v140
	ds_read_b128 v[174:177], v140 offset:1024
	ds_read_b128 v[178:181], v140 offset:2048
	ds_read_b128 v[182:185], v140 offset:3072
	ds_read_b128 v[186:189], v140 offset:4096
	ds_read_b128 v[190:193], v140 offset:5120
	ds_read_b128 v[194:197], v140 offset:6144
	ds_read_b128 v[198:201], v140 offset:7168
	global_load_lds_dwordx4 v240, s[56:57]
	s_mov_b32 m0, s82
	v_mov_b32_e32 v205, v129
	global_load_lds_dwordx4 v242, s[56:57]
	s_waitcnt lgkmcnt(0)
	s_waitcnt vmcnt(8)
	s_barrier
	s_waitcnt lgkmcnt(0)
	v_mfma_f32_16x16x32_bf16 v[124:127], v[130:133], v[170:173], v[124:127]
	v_mfma_f32_16x16x32_bf16 v[120:123], v[146:149], v[170:173], v[120:123]
	v_mfma_f32_16x16x32_bf16 v[108:111], v[130:133], v[178:181], v[108:111]
	v_mfma_f32_16x16x32_bf16 v[104:107], v[146:149], v[178:181], v[104:107]
	v_mfma_f32_16x16x32_bf16 v[92:95], v[130:133], v[186:189], v[92:95]
	v_mfma_f32_16x16x32_bf16 v[88:91], v[146:149], v[186:189], v[88:91]
	v_mfma_f32_16x16x32_bf16 v[76:79], v[130:133], v[194:197], v[76:79]
	v_mfma_f32_16x16x32_bf16 v[72:75], v[146:149], v[194:197], v[72:75]
	v_mfma_f32_16x16x32_bf16 v[124:127], v[142:145], v[174:177], v[124:127]
	v_mfma_f32_16x16x32_bf16 v[120:123], v[150:153], v[174:177], v[120:123]
	v_mfma_f32_16x16x32_bf16 v[108:111], v[142:145], v[182:185], v[108:111]
	v_mfma_f32_16x16x32_bf16 v[104:107], v[150:153], v[182:185], v[104:107]
	v_mfma_f32_16x16x32_bf16 v[92:95], v[142:145], v[190:193], v[92:95]
	v_mfma_f32_16x16x32_bf16 v[88:91], v[150:153], v[190:193], v[88:91]
	v_mfma_f32_16x16x32_bf16 v[76:79], v[142:145], v[198:201], v[76:79]
	v_mfma_f32_16x16x32_bf16 v[72:75], v[150:153], v[198:201], v[72:75]
	v_mfma_f32_16x16x32_bf16 v[116:119], v[154:157], v[170:173], v[116:119]
	v_mfma_f32_16x16x32_bf16 v[112:115], v[162:165], v[170:173], v[112:115]
	v_mfma_f32_16x16x32_bf16 v[100:103], v[154:157], v[178:181], v[100:103]
	v_mfma_f32_16x16x32_bf16 v[96:99], v[162:165], v[178:181], v[96:99]
	v_mfma_f32_16x16x32_bf16 v[84:87], v[154:157], v[186:189], v[84:87]
	v_mfma_f32_16x16x32_bf16 v[80:83], v[162:165], v[186:189], v[80:83]
	v_mfma_f32_16x16x32_bf16 v[68:71], v[154:157], v[194:197], v[68:71]
	v_mfma_f32_16x16x32_bf16 v[64:67], v[162:165], v[194:197], v[64:67]
	v_mfma_f32_16x16x32_bf16 v[116:119], v[158:161], v[174:177], v[116:119]
	v_mfma_f32_16x16x32_bf16 v[112:115], v[166:169], v[174:177], v[112:115]
	v_mfma_f32_16x16x32_bf16 v[100:103], v[158:161], v[182:185], v[100:103]
	v_mfma_f32_16x16x32_bf16 v[96:99], v[166:169], v[182:185], v[96:99]
	v_mfma_f32_16x16x32_bf16 v[84:87], v[158:161], v[190:193], v[84:87]
	v_mfma_f32_16x16x32_bf16 v[80:83], v[166:169], v[190:193], v[80:83]
	v_mfma_f32_16x16x32_bf16 v[68:71], v[158:161], v[198:201], v[68:71]
	v_mfma_f32_16x16x32_bf16 v[64:67], v[166:169], v[198:201], v[64:67]
	s_waitcnt vmcnt(8)
	s_barrier
	s_mov_b32 m0, s83
	ds_read_b128 v[170:173], v140 offset:16384
	ds_read_b128 v[174:177], v140 offset:17408
	ds_read_b128 v[178:181], v140 offset:18432
	ds_read_b128 v[182:185], v140 offset:19456
	ds_read_b128 v[186:189], v140 offset:20480
	ds_read_b128 v[190:193], v140 offset:21504
	ds_read_b128 v[194:197], v140 offset:22528
	ds_read_b128 v[198:201], v140 offset:23552
	global_load_lds_dwordx4 v244, s[62:63]
	s_mov_b32 m0, s84
	s_cselect_b32 s83, s49, s64
	s_cselect_b32 s82, s48, s55
	s_add_i32 s81, s76, s20
	global_load_lds_dwordx4 v246, s[62:63]
	s_mov_b32 m0, s81
	v_mov_b32_e32 v203, v129
	global_load_lds_dwordx4 v244, s[82:83]
	s_add_i32 m0, s81, 0x2000
	v_mov_b32_e32 v207, v129
	global_load_lds_dwordx4 v246, s[82:83]
	s_mov_b32 m0, s67
	v_lshl_add_u64 v[208:209], s[62:63], 0, v[244:245]
	global_load_lds_dwordx4 v240, s[60:61]
	s_mov_b32 m0, s68
	v_lshl_add_u64 v[210:211], s[62:63], 0, v[246:247]
	global_load_lds_dwordx4 v242, s[60:61]
	s_waitcnt lgkmcnt(0)
	v_lshl_add_u64 v[202:203], s[82:83], 0, v[244:245]
	v_lshl_add_u64 v[206:207], s[82:83], 0, v[246:247]
	v_lshl_add_u64 v[212:213], s[60:61], 0, v[240:241]
	v_lshl_add_u64 v[214:215], s[60:61], 0, v[242:243]
	s_waitcnt vmcnt(8)
	s_barrier
; #define G_STAGE(bufoff, gbase, voff) do { _Pragma("unroll") for (int _i = 0; _i < 2; ++_i) \
;         __builtin_amdgcn_global_load_lds((const unsigned*)((const char*)(gbase) + (voff)[_i]), (LAS unsigned*)(lds + (bufoff) + ldsw + _i * 8192), 16, 0, 0); } while (0)
; #define G_LDA(dst, b, h) do { _Pragma("unroll") for (int m = 0; m < 4; ++m) G_LD8(dst[m], lds + G_SA(b, h) + aoff + m * 2048); } while (0)
; #define G_LDB(dst, b, h) do { _Pragma("unroll") for (int n = 0; n < 2; ++n) G_LD8(dst[n], lds + G_SB(b, h) + boff + n * 2048); } while (0)
; #define G_WAIT_V(n) asm volatile("s_waitcnt vmcnt(" #n ")" ::: "memory")
; #define G_WAIT_L(n) asm volatile("s_waitcnt lgkmcnt(" #n ")" ::: "memory")
; #define G_BAR __builtin_amdgcn_s_barrier()
; #define G_SCHED __builtin_amdgcn_sched_barrier(0)
;     __device__ __forceinline__ unsigned row_off(const Unit& u, int r, LAS unsigned char* lds) const { return (unsigned)((const LAS int*)(lds + LDS_STAGE + u.q * 4096))[r] * (unsigned)rowbytes; }
;     ...
;             G_LDB(B0, 0, 0); G_LDB(B1, 0, 1); G_SCHED; G_LDA(At, 0, 0); G_STAGE(G_SA(1, 1), a11, vA1);
;             if constexpr (GATHER) { if (last) { int tz = tid; asm volatile("" : "+v"(tz));
; #pragma unroll
;                 for (int i = 0; i < 2; ++i) { int R, C; stage_rc(tz * 16 + i * 8192, R, C); gc0[i] = S.row_off(nxt, R, lds) + (unsigned)C * 2u; gc1[i] = S.row_off(nxt, 128 + R, lds) + (unsigned)C * 2u; } } }
;             G_WAIT_L(0); G_BAR; G_MMA(0, 0, At, B0); G_MMA(0, 1, At, B1); G_WAIT_V(8); G_BAR; G_SCHED;
;             G_LDA(At, 0, 1); G_STAGE(G_SB(0, 0), b02, voffB); G_STAGE(G_SB(0, 1), b12, voffB); G_STAGE(G_SA(0, 0), a02, vA0);
;             G_WAIT_L(0); G_BAR; G_MMA(1, 0, At, B0); G_MMA(1, 1, At, B1); G_WAIT_V(8); G_BAR; G_SCHED;
;             G_LDB(B0, 1, 0); G_LDB(B1, 1, 1); G_SCHED; G_LDA(At, 1, 0); G_STAGE(G_SA(0, 1), a12, vA1);
;             G_WAIT_L(0); G_BAR; G_MMA(0, 0, At, B0); G_MMA(0, 1, At, B1); G_WAIT_V(8); G_BAR; G_SCHED;
;             G_LDA(At, 1, 1); G_STAGE(G_SB(1, 0), b02 + kstep, voffB); G_STAGE(G_SB(1, 1), b12 + kstep, voffB); G_STAGE(G_SA(1, 0), a02 + kstep, vA0);
;             G_WAIT_L(0); G_BAR; G_MMA(1, 0, At, B0); G_MMA(1, 1, At, B1); G_WAIT_V(8); G_BAR; G_SCHED;
	s_waitcnt lgkmcnt(0)
	v_mfma_f32_16x16x32_bf16 v[60:63], v[130:133], v[170:173], v[60:63]
	v_mfma_f32_16x16x32_bf16 v[56:59], v[146:149], v[170:173], v[56:59]
	v_mfma_f32_16x16x32_bf16 v[44:47], v[130:133], v[178:181], v[44:47]
	v_mfma_f32_16x16x32_bf16 v[40:43], v[146:149], v[178:181], v[40:43]
	v_mfma_f32_16x16x32_bf16 v[28:31], v[130:133], v[186:189], v[28:31]
	v_mfma_f32_16x16x32_bf16 v[24:27], v[146:149], v[186:189], v[24:27]
	v_mfma_f32_16x16x32_bf16 v[12:15], v[130:133], v[194:197], v[12:15]
	v_mfma_f32_16x16x32_bf16 v[8:11], v[146:149], v[194:197], v[8:11]
	v_mfma_f32_16x16x32_bf16 v[60:63], v[142:145], v[174:177], v[60:63]
	v_mfma_f32_16x16x32_bf16 v[56:59], v[150:153], v[174:177], v[56:59]
	v_mfma_f32_16x16x32_bf16 v[44:47], v[142:145], v[182:185], v[44:47]
	v_mfma_f32_16x16x32_bf16 v[40:43], v[150:153], v[182:185], v[40:43]
	v_mfma_f32_16x16x32_bf16 v[28:31], v[142:145], v[190:193], v[28:31]
	v_mfma_f32_16x16x32_bf16 v[24:27], v[150:153], v[190:193], v[24:27]
	v_mfma_f32_16x16x32_bf16 v[12:15], v[142:145], v[198:201], v[12:15]
	v_mfma_f32_16x16x32_bf16 v[8:11], v[150:153], v[198:201], v[8:11]
	v_mfma_f32_16x16x32_bf16 v[52:55], v[154:157], v[170:173], v[52:55]
	v_mfma_f32_16x16x32_bf16 v[48:51], v[162:165], v[170:173], v[48:51]
	v_mfma_f32_16x16x32_bf16 v[36:39], v[154:157], v[178:181], v[36:39]
	v_mfma_f32_16x16x32_bf16 v[32:35], v[162:165], v[178:181], v[32:35]
	v_mfma_f32_16x16x32_bf16 v[20:23], v[154:157], v[186:189], v[20:23]
	v_mfma_f32_16x16x32_bf16 v[16:19], v[162:165], v[186:189], v[16:19]
	v_mfma_f32_16x16x32_bf16 v[4:7], v[154:157], v[194:197], v[4:7]
	v_mfma_f32_16x16x32_bf16 v[0:3], v[162:165], v[194:197], v[0:3]
	v_mfma_f32_16x16x32_bf16 v[52:55], v[158:161], v[174:177], v[52:55]
	v_mfma_f32_16x16x32_bf16 v[48:51], v[166:169], v[174:177], v[48:51]
	v_mfma_f32_16x16x32_bf16 v[36:39], v[158:161], v[182:185], v[36:39]
	v_mfma_f32_16x16x32_bf16 v[32:35], v[166:169], v[182:185], v[32:35]
	v_mfma_f32_16x16x32_bf16 v[20:23], v[158:161], v[190:193], v[20:23]
	v_mfma_f32_16x16x32_bf16 v[16:19], v[166:169], v[190:193], v[16:19]
	v_mfma_f32_16x16x32_bf16 v[4:7], v[158:161], v[198:201], v[4:7]
	v_mfma_f32_16x16x32_bf16 v[0:3], v[166:169], v[198:201], v[0:3]
	s_waitcnt vmcnt(8)
	s_barrier
	s_add_i32 s60, 0, 0x18000
	v_add_u32_e32 v141, s60, v137
	s_add_i32 s61, 0, 0x1c000
	ds_read_b128 v[130:133], v141
	ds_read_b128 v[142:145], v141 offset:1024
	ds_read_b128 v[146:149], v141 offset:2048
	ds_read_b128 v[150:153], v141 offset:3072
	v_add_u32_e32 v141, s61, v137
	ds_read_b128 v[154:157], v141
	ds_read_b128 v[158:161], v141 offset:1024
	ds_read_b128 v[162:165], v141 offset:2048
	ds_read_b128 v[166:169], v141 offset:3072
	s_mov_b32 m0, s69
	ds_read_b128 v[170:173], v140 offset:32768
	ds_read_b128 v[174:177], v140 offset:33792
	ds_read_b128 v[178:181], v140 offset:34816
	ds_read_b128 v[182:185], v140 offset:35840
	ds_read_b128 v[186:189], v140 offset:36864
	ds_read_b128 v[190:193], v140 offset:37888
	ds_read_b128 v[194:197], v140 offset:38912
	ds_read_b128 v[198:201], v140 offset:39936
	global_load_lds_dwordx4 v240, s[58:59]
	s_mov_b32 m0, s70
	s_nop 0
	global_load_lds_dwordx4 v242, s[58:59]
	s_waitcnt lgkmcnt(0)
	s_waitcnt vmcnt(8)
	s_barrier
	s_waitcnt lgkmcnt(0)
	v_mfma_f32_16x16x32_bf16 v[124:127], v[130:133], v[170:173], v[124:127]
	v_mfma_f32_16x16x32_bf16 v[120:123], v[146:149], v[170:173], v[120:123]
	v_mfma_f32_16x16x32_bf16 v[108:111], v[130:133], v[178:181], v[108:111]
	v_mfma_f32_16x16x32_bf16 v[104:107], v[146:149], v[178:181], v[104:107]
	v_mfma_f32_16x16x32_bf16 v[92:95], v[130:133], v[186:189], v[92:95]
	v_mfma_f32_16x16x32_bf16 v[88:91], v[146:149], v[186:189], v[88:91]
	v_mfma_f32_16x16x32_bf16 v[76:79], v[130:133], v[194:197], v[76:79]
	v_mfma_f32_16x16x32_bf16 v[72:75], v[146:149], v[194:197], v[72:75]
	v_mfma_f32_16x16x32_bf16 v[124:127], v[142:145], v[174:177], v[124:127]
	v_mfma_f32_16x16x32_bf16 v[120:123], v[150:153], v[174:177], v[120:123]
	v_mfma_f32_16x16x32_bf16 v[108:111], v[142:145], v[182:185], v[108:111]
	v_mfma_f32_16x16x32_bf16 v[104:107], v[150:153], v[182:185], v[104:107]
	v_mfma_f32_16x16x32_bf16 v[92:95], v[142:145], v[190:193], v[92:95]
	v_mfma_f32_16x16x32_bf16 v[88:91], v[150:153], v[190:193], v[88:91]
	v_mfma_f32_16x16x32_bf16 v[76:79], v[142:145], v[198:201], v[76:79]
	v_mfma_f32_16x16x32_bf16 v[72:75], v[150:153], v[198:201], v[72:75]
	v_mfma_f32_16x16x32_bf16 v[116:119], v[154:157], v[170:173], v[116:119]
	v_mfma_f32_16x16x32_bf16 v[112:115], v[162:165], v[170:173], v[112:115]
	v_mfma_f32_16x16x32_bf16 v[100:103], v[154:157], v[178:181], v[100:103]
	v_mfma_f32_16x16x32_bf16 v[96:99], v[162:165], v[178:181], v[96:99]
	v_mfma_f32_16x16x32_bf16 v[84:87], v[154:157], v[186:189], v[84:87]
	v_mfma_f32_16x16x32_bf16 v[80:83], v[162:165], v[186:189], v[80:83]
	v_mfma_f32_16x16x32_bf16 v[68:71], v[154:157], v[194:197], v[68:71]
	v_mfma_f32_16x16x32_bf16 v[64:67], v[162:165], v[194:197], v[64:67]
	v_mfma_f32_16x16x32_bf16 v[116:119], v[158:161], v[174:177], v[116:119]
	v_mfma_f32_16x16x32_bf16 v[112:115], v[166:169], v[174:177], v[112:115]
	v_mfma_f32_16x16x32_bf16 v[100:103], v[158:161], v[182:185], v[100:103]
	v_mfma_f32_16x16x32_bf16 v[96:99], v[166:169], v[182:185], v[96:99]
	v_mfma_f32_16x16x32_bf16 v[84:87], v[158:161], v[190:193], v[84:87]
	v_mfma_f32_16x16x32_bf16 v[80:83], v[166:169], v[190:193], v[80:83]
	v_mfma_f32_16x16x32_bf16 v[68:71], v[158:161], v[198:201], v[68:71]
	v_mfma_f32_16x16x32_bf16 v[64:67], v[166:169], v[198:201], v[64:67]
	s_waitcnt vmcnt(8)
	s_barrier
; #define G_STAGE(bufoff, gbase, voff) do { _Pragma("unroll") for (int _i = 0; _i < 2; ++_i) \
;         __builtin_amdgcn_global_load_lds((const unsigned*)((const char*)(gbase) + (voff)[_i]), (LAS unsigned*)(lds + (bufoff) + ldsw + _i * 8192), 16, 0, 0); } while (0)
; #define G_LDA(dst, b, h) do { _Pragma("unroll") for (int m = 0; m < 4; ++m) G_LD8(dst[m], lds + G_SA(b, h) + aoff + m * 2048); } while (0)
; #define G_LDB(dst, b, h) do { _Pragma("unroll") for (int n = 0; n < 2; ++n) G_LD8(dst[n], lds + G_SB(b, h) + boff + n * 2048); } while (0)
; #define G_WAIT_V(n) asm volatile("s_waitcnt vmcnt(" #n ")" ::: "memory")
; #define G_WAIT_L(n) asm volatile("s_waitcnt lgkmcnt(" #n ")" ::: "memory")
; #define G_BAR __builtin_amdgcn_s_barrier()
; #define G_SCHED __builtin_amdgcn_sched_barrier(0)
;     ...
;             G_LDA(At, 0, 1); G_STAGE(G_SB(0, 0), b02, voffB); G_STAGE(G_SB(0, 1), b12, voffB); G_STAGE(G_SA(0, 0), a02, vA0);
;             G_WAIT_L(0); G_BAR; G_MMA(1, 0, At, B0); G_MMA(1, 1, At, B1); G_WAIT_V(8); G_BAR; G_SCHED;
;             G_LDB(B0, 1, 0); G_LDB(B1, 1, 1); G_SCHED; G_LDA(At, 1, 0); G_STAGE(G_SA(0, 1), a12, vA1);
;             G_WAIT_L(0); G_BAR; G_MMA(0, 0, At, B0); G_MMA(0, 1, At, B1); G_WAIT_V(8); G_BAR; G_SCHED;
;             G_LDA(At, 1, 1); G_STAGE(G_SB(1, 0), b02 + kstep, voffB); G_STAGE(G_SB(1, 1), b12 + kstep, voffB); G_STAGE(G_SA(1, 0), a02 + kstep, vA0);
;             G_WAIT_L(0); G_BAR; G_MMA(1, 0, At, B0); G_MMA(1, 1, At, B1); G_WAIT_V(8); G_BAR; G_SCHED;
	s_add_i32 s58, s60, s20
	v_lshl_add_u64 v[204:205], v[208:209], 0, s[8:9]
	s_mov_b32 m0, s58
	ds_read_b128 v[170:173], v140 offset:49152
	ds_read_b128 v[174:177], v140 offset:50176
	ds_read_b128 v[178:181], v140 offset:51200
	ds_read_b128 v[182:185], v140 offset:52224
	ds_read_b128 v[186:189], v140 offset:53248
	ds_read_b128 v[190:193], v140 offset:54272
	ds_read_b128 v[194:197], v140 offset:55296
	ds_read_b128 v[198:201], v140 offset:56320
	global_load_lds_dwordx4 v[204:205], off
	v_lshl_add_u64 v[204:205], v[210:211], 0, s[8:9]
	s_add_i32 m0, s58, 0x2000
	s_add_i32 s58, s61, s20
	global_load_lds_dwordx4 v[204:205], off
	v_lshl_add_u64 v[202:203], v[202:203], 0, s[8:9]
	s_mov_b32 m0, s58
	s_nop 0
	global_load_lds_dwordx4 v[202:203], off
	v_lshl_add_u64 v[202:203], v[206:207], 0, s[8:9]
	s_add_i32 m0, s58, 0x2000
	s_nop 0
	global_load_lds_dwordx4 v[202:203], off
	v_lshl_add_u64 v[202:203], v[212:213], 0, s[8:9]
	s_mov_b32 m0, s72
	s_nop 0
	global_load_lds_dwordx4 v[202:203], off
	v_lshl_add_u64 v[202:203], v[214:215], 0, s[8:9]
	s_mov_b32 m0, s73
	s_nop 0
	global_load_lds_dwordx4 v[202:203], off
	s_waitcnt lgkmcnt(0)
	s_waitcnt vmcnt(8)
	s_barrier
	s_waitcnt lgkmcnt(0)
	v_mfma_f32_16x16x32_bf16 v[60:63], v[130:133], v[170:173], v[60:63]
	v_mfma_f32_16x16x32_bf16 v[56:59], v[146:149], v[170:173], v[56:59]
	v_mfma_f32_16x16x32_bf16 v[44:47], v[130:133], v[178:181], v[44:47]
	v_mfma_f32_16x16x32_bf16 v[40:43], v[146:149], v[178:181], v[40:43]
	v_mfma_f32_16x16x32_bf16 v[28:31], v[130:133], v[186:189], v[28:31]
	v_mfma_f32_16x16x32_bf16 v[24:27], v[146:149], v[186:189], v[24:27]
	v_mfma_f32_16x16x32_bf16 v[12:15], v[130:133], v[194:197], v[12:15]
	v_mfma_f32_16x16x32_bf16 v[8:11], v[146:149], v[194:197], v[8:11]
	v_mfma_f32_16x16x32_bf16 v[60:63], v[142:145], v[174:177], v[60:63]
	v_mfma_f32_16x16x32_bf16 v[56:59], v[150:153], v[174:177], v[56:59]
	v_mfma_f32_16x16x32_bf16 v[44:47], v[142:145], v[182:185], v[44:47]
	v_mfma_f32_16x16x32_bf16 v[40:43], v[150:153], v[182:185], v[40:43]
	v_mfma_f32_16x16x32_bf16 v[28:31], v[142:145], v[190:193], v[28:31]
	v_mfma_f32_16x16x32_bf16 v[24:27], v[150:153], v[190:193], v[24:27]
	v_mfma_f32_16x16x32_bf16 v[12:15], v[142:145], v[198:201], v[12:15]
	v_mfma_f32_16x16x32_bf16 v[8:11], v[150:153], v[198:201], v[8:11]
	v_mfma_f32_16x16x32_bf16 v[52:55], v[154:157], v[170:173], v[52:55]
	v_mfma_f32_16x16x32_bf16 v[48:51], v[162:165], v[170:173], v[48:51]
	v_mfma_f32_16x16x32_bf16 v[36:39], v[154:157], v[178:181], v[36:39]
	v_mfma_f32_16x16x32_bf16 v[32:35], v[162:165], v[178:181], v[32:35]
	v_mfma_f32_16x16x32_bf16 v[20:23], v[154:157], v[186:189], v[20:23]
	v_mfma_f32_16x16x32_bf16 v[16:19], v[162:165], v[186:189], v[16:19]
	v_mfma_f32_16x16x32_bf16 v[4:7], v[154:157], v[194:197], v[4:7]
	v_mfma_f32_16x16x32_bf16 v[0:3], v[162:165], v[194:197], v[0:3]
	v_mfma_f32_16x16x32_bf16 v[52:55], v[158:161], v[174:177], v[52:55]
	v_mfma_f32_16x16x32_bf16 v[48:51], v[166:169], v[174:177], v[48:51]
	v_mfma_f32_16x16x32_bf16 v[36:39], v[158:161], v[182:185], v[36:39]
	v_mfma_f32_16x16x32_bf16 v[32:35], v[166:169], v[182:185], v[32:35]
	v_mfma_f32_16x16x32_bf16 v[20:23], v[158:161], v[190:193], v[20:23]
	v_mfma_f32_16x16x32_bf16 v[16:19], v[166:169], v[190:193], v[16:19]
	v_mfma_f32_16x16x32_bf16 v[4:7], v[158:161], v[198:201], v[4:7]
	v_mfma_f32_16x16x32_bf16 v[0:3], v[166:169], v[198:201], v[0:3]
	s_waitcnt vmcnt(8)
	s_barrier
	s_add_u32 s41, s41, 0x100
	s_addc_u32 s53, s53, 0
	s_add_u32 s55, s55, 0x100
	s_addc_u32 s64, s64, 0
	s_add_u32 s65, s65, 0x100
	s_addc_u32 s79, s79, 0
	s_add_u32 s56, s56, 0x100
	s_addc_u32 s57, s57, 0
	s_cmp_ge_i32 s80, s0
	s_mov_b32 s58, s80
	s_cbranch_scc0 .LBB0_549
	v_readlane_b32 s79, v255, 13
	s_and_b64 vcc, exec, s[38:39]
	s_cbranch_vccz .LBB0_552

; #define G_STAGE(bufoff, gbase, voff) do { _Pragma("unroll") for (int _i = 0; _i < 2; ++_i) \
;         __builtin_amdgcn_global_load_lds((const unsigned*)((const char*)(gbase) + (voff)[_i]), (LAS unsigned*)(lds + (bufoff) + ldsw + _i * 8192), 16, 0, 0); } while (0)
; #define G_LDA(dst, b, h) do { _Pragma("unroll") for (int m = 0; m < 4; ++m) G_LD8(dst[m], lds + G_SA(b, h) + aoff + m * 2048); } while (0)
; #define G_LDB(dst, b, h) do { _Pragma("unroll") for (int n = 0; n < 2; ++n) G_LD8(dst[n], lds + G_SB(b, h) + boff + n * 2048); } while (0)
; #define G_WAIT_V(n) asm volatile("s_waitcnt vmcnt(" #n ")" ::: "memory")
; #define G_WAIT_L(n) asm volatile("s_waitcnt lgkmcnt(" #n ")" ::: "memory")
; #define G_BAR __builtin_amdgcn_s_barrier()
; #define G_SCHED __builtin_amdgcn_sched_barrier(0)
;     ...
;             const char* a11 = cur.a1 + (size_t)(t + 1) * kstep;
;             const char* a02 = last ? nxt.a0 : cur.a0 + (size_t)(t + 2) * kstep; const char* a12 = last ? nxt.a1 : cur.a1 + (size_t)(t + 2) * kstep;
;             const char* b02 = last ? nxt.b0 : cur.b0 + (size_t)(t + 2) * kstep; const char* b12 = last ? nxt.b1 : cur.b1 + (size_t)(t + 2) * kstep;
;             G_LDB(B0, 0, 0); G_LDB(B1, 0, 1); G_SCHED; G_LDA(At, 0, 0); G_STAGE(G_SA(1, 1), a11, vA1);
;             if constexpr (GATHER) { if (last) { int tz = tid; asm volatile("" : "+v"(tz));
; #pragma unroll
;                 for (int i = 0; i < 2; ++i) { int R, C; stage_rc(tz * 16 + i * 8192, R, C); gc0[i] = S.row_off(nxt, R, lds) + (unsigned)C * 2u; gc1[i] = S.row_off(nxt, 128 + R, lds) + (unsigned)C * 2u; } } }
;             G_WAIT_L(0); G_BAR; G_MMA(0, 0, At, B0); G_MMA(0, 1, At, B1); G_WAIT_V(8); G_BAR; G_SCHED;
;             G_LDA(At, 0, 1); G_STAGE(G_SB(0, 0), b02, voffB); G_STAGE(G_SB(0, 1), b12, voffB); G_STAGE(G_SA(0, 0), a02, vA0);
;             G_WAIT_L(0); G_BAR; G_MMA(1, 0, At, B0); G_MMA(1, 1, At, B1); G_WAIT_V(8); G_BAR; G_SCHED;
;             G_LDB(B0, 1, 0); G_LDB(B1, 1, 1); G_SCHED; G_LDA(At, 1, 0); G_STAGE(G_SA(0, 1), a12, vA1);
;             G_WAIT_L(0); G_BAR; G_MMA(0, 0, At, B0); G_MMA(0, 1, At, B1); G_WAIT_V(8); G_BAR; G_SCHED;
;             G_LDA(At, 1, 1); G_STAGE(G_SB(1, 0), b02 + kstep, voffB); G_STAGE(G_SB(1, 1), b12 + kstep, voffB); G_STAGE(G_SA(1, 0), a02 + kstep, vA0);
;             G_WAIT_L(0); G_BAR; G_MMA(1, 0, At, B0); G_MMA(1, 1, At, B1); G_WAIT_V(8); G_BAR; G_SCHED;
.LBB0_576:
	s_add_i32 s71, s52, 2
	ds_read_b128 v[138:141], v134
	ds_read_b128 v[142:145], v134 offset:1024
	ds_read_b128 v[146:149], v134 offset:2048
	ds_read_b128 v[150:153], v134 offset:3072
	ds_read_b128 v[154:157], v135
	ds_read_b128 v[158:161], v135 offset:1024
	ds_read_b128 v[162:165], v135 offset:2048
	ds_read_b128 v[166:169], v135 offset:3072
	s_add_u32 s72, s50, 0x80
	s_addc_u32 s53, s51, 0
	s_add_i32 s75, s22, s20
	s_add_i32 m0, s62, 0xc000
	s_add_i32 s74, s62, 0xe000
	s_add_i32 s76, s75, 0x2000
	s_cmp_eq_u32 s23, s52
	s_cselect_b32 s52, s38, s72
	s_cselect_b32 s55, s37, s70
	s_cselect_b32 s54, s36, s59
	s_cselect_b32 s57, s41, s45
	s_cselect_b32 s56, s40, s35
	s_cselect_b32 s53, s39, s53
	ds_read_b128 v[170:173], v136
	ds_read_b128 v[174:177], v136 offset:1024
	ds_read_b128 v[178:181], v136 offset:2048
	ds_read_b128 v[182:185], v136 offset:3072
	ds_read_b128 v[186:189], v136 offset:4096
	ds_read_b128 v[190:193], v136 offset:5120
	ds_read_b128 v[194:197], v136 offset:6144
	ds_read_b128 v[198:201], v136 offset:7168
	global_load_lds_dwordx4 v240, s[50:51]
	s_mov_b32 m0, s74
	v_mov_b32_e32 v205, v129
	global_load_lds_dwordx4 v242, s[50:51]
	s_waitcnt lgkmcnt(0)
	s_waitcnt vmcnt(8)
	s_barrier
	s_waitcnt lgkmcnt(0)
	v_mfma_f32_16x16x32_bf16 v[124:127], v[138:141], v[170:173], v[124:127]
	v_mfma_f32_16x16x32_bf16 v[120:123], v[146:149], v[170:173], v[120:123]
	v_mfma_f32_16x16x32_bf16 v[108:111], v[138:141], v[178:181], v[108:111]
	v_mfma_f32_16x16x32_bf16 v[104:107], v[146:149], v[178:181], v[104:107]
	v_mfma_f32_16x16x32_bf16 v[92:95], v[138:141], v[186:189], v[92:95]
	v_mfma_f32_16x16x32_bf16 v[88:91], v[146:149], v[186:189], v[88:91]
	v_mfma_f32_16x16x32_bf16 v[76:79], v[138:141], v[194:197], v[76:79]
	v_mfma_f32_16x16x32_bf16 v[72:75], v[146:149], v[194:197], v[72:75]
	v_mfma_f32_16x16x32_bf16 v[124:127], v[142:145], v[174:177], v[124:127]
	v_mfma_f32_16x16x32_bf16 v[120:123], v[150:153], v[174:177], v[120:123]
	v_mfma_f32_16x16x32_bf16 v[108:111], v[142:145], v[182:185], v[108:111]
	v_mfma_f32_16x16x32_bf16 v[104:107], v[150:153], v[182:185], v[104:107]
	v_mfma_f32_16x16x32_bf16 v[92:95], v[142:145], v[190:193], v[92:95]
	v_mfma_f32_16x16x32_bf16 v[88:91], v[150:153], v[190:193], v[88:91]
	v_mfma_f32_16x16x32_bf16 v[76:79], v[142:145], v[198:201], v[76:79]
	v_mfma_f32_16x16x32_bf16 v[72:75], v[150:153], v[198:201], v[72:75]
	v_mfma_f32_16x16x32_bf16 v[116:119], v[154:157], v[170:173], v[116:119]
	v_mfma_f32_16x16x32_bf16 v[112:115], v[162:165], v[170:173], v[112:115]
	v_mfma_f32_16x16x32_bf16 v[100:103], v[154:157], v[178:181], v[100:103]
	v_mfma_f32_16x16x32_bf16 v[96:99], v[162:165], v[178:181], v[96:99]
	v_mfma_f32_16x16x32_bf16 v[84:87], v[154:157], v[186:189], v[84:87]
	v_mfma_f32_16x16x32_bf16 v[80:83], v[162:165], v[186:189], v[80:83]
	v_mfma_f32_16x16x32_bf16 v[68:71], v[154:157], v[194:197], v[68:71]
	v_mfma_f32_16x16x32_bf16 v[64:67], v[162:165], v[194:197], v[64:67]
	v_mfma_f32_16x16x32_bf16 v[116:119], v[158:161], v[174:177], v[116:119]
	v_mfma_f32_16x16x32_bf16 v[112:115], v[166:169], v[174:177], v[112:115]
	v_mfma_f32_16x16x32_bf16 v[100:103], v[158:161], v[182:185], v[100:103]
	v_mfma_f32_16x16x32_bf16 v[96:99], v[166:169], v[182:185], v[96:99]
	v_mfma_f32_16x16x32_bf16 v[84:87], v[158:161], v[190:193], v[84:87]
	v_mfma_f32_16x16x32_bf16 v[80:83], v[166:169], v[190:193], v[80:83]
	v_mfma_f32_16x16x32_bf16 v[68:71], v[158:161], v[198:201], v[68:71]
	v_mfma_f32_16x16x32_bf16 v[64:67], v[166:169], v[198:201], v[64:67]
	s_waitcnt vmcnt(8)
	s_barrier
	s_mov_b32 m0, s75
	ds_read_b128 v[170:173], v136 offset:16384
	ds_read_b128 v[174:177], v136 offset:17408
	ds_read_b128 v[178:181], v136 offset:18432
	ds_read_b128 v[182:185], v136 offset:19456
	ds_read_b128 v[186:189], v136 offset:20480
	ds_read_b128 v[190:193], v136 offset:21504
	ds_read_b128 v[194:197], v136 offset:22528
	ds_read_b128 v[198:201], v136 offset:23552
	global_load_lds_dwordx4 v244, s[56:57]
	s_mov_b32 m0, s76
	s_cselect_b32 s73, s43, s58
	s_cselect_b32 s72, s42, s49
	s_add_i32 s74, s24, s20
	global_load_lds_dwordx4 v246, s[56:57]
	s_mov_b32 m0, s74
	v_mov_b32_e32 v203, v129
	global_load_lds_dwordx4 v244, s[72:73]
	s_add_i32 m0, s74, 0x2000
	v_mov_b32_e32 v207, v129
	global_load_lds_dwordx4 v246, s[72:73]
	s_mov_b32 m0, s62
	v_lshl_add_u64 v[208:209], s[56:57], 0, v[244:245]
	global_load_lds_dwordx4 v240, s[54:55]
	s_mov_b32 m0, s63
	v_lshl_add_u64 v[210:211], s[56:57], 0, v[246:247]
	global_load_lds_dwordx4 v242, s[54:55]
	s_waitcnt lgkmcnt(0)
	v_lshl_add_u64 v[202:203], s[72:73], 0, v[244:245]
	v_lshl_add_u64 v[206:207], s[72:73], 0, v[246:247]
	v_lshl_add_u64 v[212:213], s[54:55], 0, v[240:241]
	v_lshl_add_u64 v[214:215], s[54:55], 0, v[242:243]
	s_waitcnt vmcnt(8)
	s_barrier
; #define G_STAGE(bufoff, gbase, voff) do { _Pragma("unroll") for (int _i = 0; _i < 2; ++_i) \
;         __builtin_amdgcn_global_load_lds((const unsigned*)((const char*)(gbase) + (voff)[_i]), (LAS unsigned*)(lds + (bufoff) + ldsw + _i * 8192), 16, 0, 0); } while (0)
; #define G_LDA(dst, b, h) do { _Pragma("unroll") for (int m = 0; m < 4; ++m) G_LD8(dst[m], lds + G_SA(b, h) + aoff + m * 2048); } while (0)
; #define G_LDB(dst, b, h) do { _Pragma("unroll") for (int n = 0; n < 2; ++n) G_LD8(dst[n], lds + G_SB(b, h) + boff + n * 2048); } while (0)
; #define G_WAIT_V(n) asm volatile("s_waitcnt vmcnt(" #n ")" ::: "memory")
; #define G_WAIT_L(n) asm volatile("s_waitcnt lgkmcnt(" #n ")" ::: "memory")
; #define G_BAR __builtin_amdgcn_s_barrier()
; #define G_SCHED __builtin_amdgcn_sched_barrier(0)
;     __device__ __forceinline__ unsigned row_off(const Unit& u, int r, LAS unsigned char* lds) const { return (unsigned)((const LAS int*)(lds + LDS_STAGE + u.q * 4096))[r] * (unsigned)rowbytes; }
;     ...
;             G_LDB(B0, 0, 0); G_LDB(B1, 0, 1); G_SCHED; G_LDA(At, 0, 0); G_STAGE(G_SA(1, 1), a11, vA1);
;             if constexpr (GATHER) { if (last) { int tz = tid; asm volatile("" : "+v"(tz));
; #pragma unroll
;                 for (int i = 0; i < 2; ++i) { int R, C; stage_rc(tz * 16 + i * 8192, R, C); gc0[i] = S.row_off(nxt, R, lds) + (unsigned)C * 2u; gc1[i] = S.row_off(nxt, 128 + R, lds) + (unsigned)C * 2u; } } }
;             G_WAIT_L(0); G_BAR; G_MMA(0, 0, At, B0); G_MMA(0, 1, At, B1); G_WAIT_V(8); G_BAR; G_SCHED;
;             G_LDA(At, 0, 1); G_STAGE(G_SB(0, 0), b02, voffB); G_STAGE(G_SB(0, 1), b12, voffB); G_STAGE(G_SA(0, 0), a02, vA0);
;             G_WAIT_L(0); G_BAR; G_MMA(1, 0, At, B0); G_MMA(1, 1, At, B1); G_WAIT_V(8); G_BAR; G_SCHED;
;             G_LDB(B0, 1, 0); G_LDB(B1, 1, 1); G_SCHED; G_LDA(At, 1, 0); G_STAGE(G_SA(0, 1), a12, vA1);
;             G_WAIT_L(0); G_BAR; G_MMA(0, 0, At, B0); G_MMA(0, 1, At, B1); G_WAIT_V(8); G_BAR; G_SCHED;
;             G_LDA(At, 1, 1); G_STAGE(G_SB(1, 0), b02 + kstep, voffB); G_STAGE(G_SB(1, 1), b12 + kstep, voffB); G_STAGE(G_SA(1, 0), a02 + kstep, vA0);
;             G_WAIT_L(0); G_BAR; G_MMA(1, 0, At, B0); G_MMA(1, 1, At, B1); G_WAIT_V(8); G_BAR; G_SCHED;
	s_waitcnt lgkmcnt(0)
	v_mfma_f32_16x16x32_bf16 v[60:63], v[138:141], v[170:173], v[60:63]
	v_mfma_f32_16x16x32_bf16 v[56:59], v[146:149], v[170:173], v[56:59]
	v_mfma_f32_16x16x32_bf16 v[44:47], v[138:141], v[178:181], v[44:47]
	v_mfma_f32_16x16x32_bf16 v[40:43], v[146:149], v[178:181], v[40:43]
	v_mfma_f32_16x16x32_bf16 v[28:31], v[138:141], v[186:189], v[28:31]
	v_mfma_f32_16x16x32_bf16 v[24:27], v[146:149], v[186:189], v[24:27]
	v_mfma_f32_16x16x32_bf16 v[12:15], v[138:141], v[194:197], v[12:15]
	v_mfma_f32_16x16x32_bf16 v[8:11], v[146:149], v[194:197], v[8:11]
	v_mfma_f32_16x16x32_bf16 v[60:63], v[142:145], v[174:177], v[60:63]
	v_mfma_f32_16x16x32_bf16 v[56:59], v[150:153], v[174:177], v[56:59]
	v_mfma_f32_16x16x32_bf16 v[44:47], v[142:145], v[182:185], v[44:47]
	v_mfma_f32_16x16x32_bf16 v[40:43], v[150:153], v[182:185], v[40:43]
	v_mfma_f32_16x16x32_bf16 v[28:31], v[142:145], v[190:193], v[28:31]
	v_mfma_f32_16x16x32_bf16 v[24:27], v[150:153], v[190:193], v[24:27]
	v_mfma_f32_16x16x32_bf16 v[12:15], v[142:145], v[198:201], v[12:15]
	v_mfma_f32_16x16x32_bf16 v[8:11], v[150:153], v[198:201], v[8:11]
	v_mfma_f32_16x16x32_bf16 v[52:55], v[154:157], v[170:173], v[52:55]
	v_mfma_f32_16x16x32_bf16 v[48:51], v[162:165], v[170:173], v[48:51]
	v_mfma_f32_16x16x32_bf16 v[36:39], v[154:157], v[178:181], v[36:39]
	v_mfma_f32_16x16x32_bf16 v[32:35], v[162:165], v[178:181], v[32:35]
	v_mfma_f32_16x16x32_bf16 v[20:23], v[154:157], v[186:189], v[20:23]
	v_mfma_f32_16x16x32_bf16 v[16:19], v[162:165], v[186:189], v[16:19]
	v_mfma_f32_16x16x32_bf16 v[4:7], v[154:157], v[194:197], v[4:7]
	v_mfma_f32_16x16x32_bf16 v[0:3], v[162:165], v[194:197], v[0:3]
	v_mfma_f32_16x16x32_bf16 v[52:55], v[158:161], v[174:177], v[52:55]
	v_mfma_f32_16x16x32_bf16 v[48:51], v[166:169], v[174:177], v[48:51]
	v_mfma_f32_16x16x32_bf16 v[36:39], v[158:161], v[182:185], v[36:39]
	v_mfma_f32_16x16x32_bf16 v[32:35], v[166:169], v[182:185], v[32:35]
	v_mfma_f32_16x16x32_bf16 v[20:23], v[158:161], v[190:193], v[20:23]
	v_mfma_f32_16x16x32_bf16 v[16:19], v[166:169], v[190:193], v[16:19]
	v_mfma_f32_16x16x32_bf16 v[4:7], v[158:161], v[198:201], v[4:7]
	v_mfma_f32_16x16x32_bf16 v[0:3], v[166:169], v[198:201], v[0:3]
	s_waitcnt vmcnt(8)
	s_barrier
	s_add_i32 s54, 0, 0x18000
	v_add_u32_e32 v137, s54, v133
	s_add_i32 s55, 0, 0x1c000
	ds_read_b128 v[138:141], v137
	ds_read_b128 v[142:145], v137 offset:1024
	ds_read_b128 v[146:149], v137 offset:2048
	ds_read_b128 v[150:153], v137 offset:3072
	v_add_u32_e32 v137, s55, v133
	ds_read_b128 v[154:157], v137
	ds_read_b128 v[158:161], v137 offset:1024
	ds_read_b128 v[162:165], v137 offset:2048
	ds_read_b128 v[166:169], v137 offset:3072
	s_mov_b32 m0, s64
	ds_read_b128 v[170:173], v136 offset:32768
	ds_read_b128 v[174:177], v136 offset:33792
	ds_read_b128 v[178:181], v136 offset:34816
	ds_read_b128 v[182:185], v136 offset:35840
	ds_read_b128 v[186:189], v136 offset:36864
	ds_read_b128 v[190:193], v136 offset:37888
	ds_read_b128 v[194:197], v136 offset:38912
	ds_read_b128 v[198:201], v136 offset:39936
	global_load_lds_dwordx4 v240, s[52:53]
	s_mov_b32 m0, s65
	s_nop 0
	global_load_lds_dwordx4 v242, s[52:53]
	s_waitcnt lgkmcnt(0)
	s_waitcnt vmcnt(8)
	s_barrier
	s_waitcnt lgkmcnt(0)
	v_mfma_f32_16x16x32_bf16 v[124:127], v[138:141], v[170:173], v[124:127]
	v_mfma_f32_16x16x32_bf16 v[120:123], v[146:149], v[170:173], v[120:123]
	v_mfma_f32_16x16x32_bf16 v[108:111], v[138:141], v[178:181], v[108:111]
	v_mfma_f32_16x16x32_bf16 v[104:107], v[146:149], v[178:181], v[104:107]
	v_mfma_f32_16x16x32_bf16 v[92:95], v[138:141], v[186:189], v[92:95]
	v_mfma_f32_16x16x32_bf16 v[88:91], v[146:149], v[186:189], v[88:91]
	v_mfma_f32_16x16x32_bf16 v[76:79], v[138:141], v[194:197], v[76:79]
	v_mfma_f32_16x16x32_bf16 v[72:75], v[146:149], v[194:197], v[72:75]
	v_mfma_f32_16x16x32_bf16 v[124:127], v[142:145], v[174:177], v[124:127]
	v_mfma_f32_16x16x32_bf16 v[120:123], v[150:153], v[174:177], v[120:123]
	v_mfma_f32_16x16x32_bf16 v[108:111], v[142:145], v[182:185], v[108:111]
	v_mfma_f32_16x16x32_bf16 v[104:107], v[150:153], v[182:185], v[104:107]
	v_mfma_f32_16x16x32_bf16 v[92:95], v[142:145], v[190:193], v[92:95]
	v_mfma_f32_16x16x32_bf16 v[88:91], v[150:153], v[190:193], v[88:91]
	v_mfma_f32_16x16x32_bf16 v[76:79], v[142:145], v[198:201], v[76:79]
	v_mfma_f32_16x16x32_bf16 v[72:75], v[150:153], v[198:201], v[72:75]
	v_mfma_f32_16x16x32_bf16 v[116:119], v[154:157], v[170:173], v[116:119]
	v_mfma_f32_16x16x32_bf16 v[112:115], v[162:165], v[170:173], v[112:115]
	v_mfma_f32_16x16x32_bf16 v[100:103], v[154:157], v[178:181], v[100:103]
	v_mfma_f32_16x16x32_bf16 v[96:99], v[162:165], v[178:181], v[96:99]
	v_mfma_f32_16x16x32_bf16 v[84:87], v[154:157], v[186:189], v[84:87]
	v_mfma_f32_16x16x32_bf16 v[80:83], v[162:165], v[186:189], v[80:83]
	v_mfma_f32_16x16x32_bf16 v[68:71], v[154:157], v[194:197], v[68:71]
	v_mfma_f32_16x16x32_bf16 v[64:67], v[162:165], v[194:197], v[64:67]
	v_mfma_f32_16x16x32_bf16 v[116:119], v[158:161], v[174:177], v[116:119]
	v_mfma_f32_16x16x32_bf16 v[112:115], v[166:169], v[174:177], v[112:115]
	v_mfma_f32_16x16x32_bf16 v[100:103], v[158:161], v[182:185], v[100:103]
	v_mfma_f32_16x16x32_bf16 v[96:99], v[166:169], v[182:185], v[96:99]
	v_mfma_f32_16x16x32_bf16 v[84:87], v[158:161], v[190:193], v[84:87]
	v_mfma_f32_16x16x32_bf16 v[80:83], v[166:169], v[190:193], v[80:83]
	v_mfma_f32_16x16x32_bf16 v[68:71], v[158:161], v[198:201], v[68:71]
	v_mfma_f32_16x16x32_bf16 v[64:67], v[166:169], v[198:201], v[64:67]
	s_waitcnt vmcnt(8)
	s_barrier
; #define G_STAGE(bufoff, gbase, voff) do { _Pragma("unroll") for (int _i = 0; _i < 2; ++_i) \
;         __builtin_amdgcn_global_load_lds((const unsigned*)((const char*)(gbase) + (voff)[_i]), (LAS unsigned*)(lds + (bufoff) + ldsw + _i * 8192), 16, 0, 0); } while (0)
; #define G_LDA(dst, b, h) do { _Pragma("unroll") for (int m = 0; m < 4; ++m) G_LD8(dst[m], lds + G_SA(b, h) + aoff + m * 2048); } while (0)
; #define G_LDB(dst, b, h) do { _Pragma("unroll") for (int n = 0; n < 2; ++n) G_LD8(dst[n], lds + G_SB(b, h) + boff + n * 2048); } while (0)
; #define G_WAIT_V(n) asm volatile("s_waitcnt vmcnt(" #n ")" ::: "memory")
; #define G_WAIT_L(n) asm volatile("s_waitcnt lgkmcnt(" #n ")" ::: "memory")
; #define G_BAR __builtin_amdgcn_s_barrier()
; #define G_SCHED __builtin_amdgcn_sched_barrier(0)
;     ...
;             G_LDA(At, 0, 1); G_STAGE(G_SB(0, 0), b02, voffB); G_STAGE(G_SB(0, 1), b12, voffB); G_STAGE(G_SA(0, 0), a02, vA0);
;             G_WAIT_L(0); G_BAR; G_MMA(1, 0, At, B0); G_MMA(1, 1, At, B1); G_WAIT_V(8); G_BAR; G_SCHED;
;             G_LDB(B0, 1, 0); G_LDB(B1, 1, 1); G_SCHED; G_LDA(At, 1, 0); G_STAGE(G_SA(0, 1), a12, vA1);
;             G_WAIT_L(0); G_BAR; G_MMA(0, 0, At, B0); G_MMA(0, 1, At, B1); G_WAIT_V(8); G_BAR; G_SCHED;
;             G_LDA(At, 1, 1); G_STAGE(G_SB(1, 0), b02 + kstep, voffB); G_STAGE(G_SB(1, 1), b12 + kstep, voffB); G_STAGE(G_SA(1, 0), a02 + kstep, vA0);
;             G_WAIT_L(0); G_BAR; G_MMA(1, 0, At, B0); G_MMA(1, 1, At, B1); G_WAIT_V(8); G_BAR; G_SCHED;
	s_add_i32 s52, s54, s20
	v_lshl_add_u64 v[204:205], v[208:209], 0, s[6:7]
	s_mov_b32 m0, s52
	ds_read_b128 v[170:173], v136 offset:49152
	ds_read_b128 v[174:177], v136 offset:50176
	ds_read_b128 v[178:181], v136 offset:51200
	ds_read_b128 v[182:185], v136 offset:52224
	ds_read_b128 v[186:189], v136 offset:53248
	ds_read_b128 v[190:193], v136 offset:54272
	ds_read_b128 v[194:197], v136 offset:55296
	ds_read_b128 v[198:201], v136 offset:56320
	global_load_lds_dwordx4 v[204:205], off
	v_lshl_add_u64 v[204:205], v[210:211], 0, s[6:7]
	s_add_i32 m0, s52, 0x2000
	s_add_i32 s52, s55, s20
	global_load_lds_dwordx4 v[204:205], off
	v_lshl_add_u64 v[202:203], v[202:203], 0, s[6:7]
	s_mov_b32 m0, s52
	s_nop 0
	global_load_lds_dwordx4 v[202:203], off
	v_lshl_add_u64 v[202:203], v[206:207], 0, s[6:7]
	s_add_i32 m0, s52, 0x2000
	s_nop 0
	global_load_lds_dwordx4 v[202:203], off
	v_lshl_add_u64 v[202:203], v[212:213], 0, s[6:7]
	s_mov_b32 m0, s25
	s_nop 0
	global_load_lds_dwordx4 v[202:203], off
	v_lshl_add_u64 v[202:203], v[214:215], 0, s[6:7]
	s_mov_b32 m0, s67
	s_nop 0
	global_load_lds_dwordx4 v[202:203], off
	s_waitcnt lgkmcnt(0)
	s_waitcnt vmcnt(8)
	s_barrier
	s_waitcnt lgkmcnt(0)
	v_mfma_f32_16x16x32_bf16 v[60:63], v[138:141], v[170:173], v[60:63]
	v_mfma_f32_16x16x32_bf16 v[56:59], v[146:149], v[170:173], v[56:59]
	v_mfma_f32_16x16x32_bf16 v[44:47], v[138:141], v[178:181], v[44:47]
	v_mfma_f32_16x16x32_bf16 v[40:43], v[146:149], v[178:181], v[40:43]
	v_mfma_f32_16x16x32_bf16 v[28:31], v[138:141], v[186:189], v[28:31]
	v_mfma_f32_16x16x32_bf16 v[24:27], v[146:149], v[186:189], v[24:27]
	v_mfma_f32_16x16x32_bf16 v[12:15], v[138:141], v[194:197], v[12:15]
	v_mfma_f32_16x16x32_bf16 v[8:11], v[146:149], v[194:197], v[8:11]
	v_mfma_f32_16x16x32_bf16 v[60:63], v[142:145], v[174:177], v[60:63]
	v_mfma_f32_16x16x32_bf16 v[56:59], v[150:153], v[174:177], v[56:59]
	v_mfma_f32_16x16x32_bf16 v[44:47], v[142:145], v[182:185], v[44:47]
	v_mfma_f32_16x16x32_bf16 v[40:43], v[150:153], v[182:185], v[40:43]
	v_mfma_f32_16x16x32_bf16 v[28:31], v[142:145], v[190:193], v[28:31]
	v_mfma_f32_16x16x32_bf16 v[24:27], v[150:153], v[190:193], v[24:27]
	v_mfma_f32_16x16x32_bf16 v[12:15], v[142:145], v[198:201], v[12:15]
	v_mfma_f32_16x16x32_bf16 v[8:11], v[150:153], v[198:201], v[8:11]
	v_mfma_f32_16x16x32_bf16 v[52:55], v[154:157], v[170:173], v[52:55]
	v_mfma_f32_16x16x32_bf16 v[48:51], v[162:165], v[170:173], v[48:51]
	v_mfma_f32_16x16x32_bf16 v[36:39], v[154:157], v[178:181], v[36:39]
	v_mfma_f32_16x16x32_bf16 v[32:35], v[162:165], v[178:181], v[32:35]
	v_mfma_f32_16x16x32_bf16 v[20:23], v[154:157], v[186:189], v[20:23]
	v_mfma_f32_16x16x32_bf16 v[16:19], v[162:165], v[186:189], v[16:19]
	v_mfma_f32_16x16x32_bf16 v[4:7], v[154:157], v[194:197], v[4:7]
	v_mfma_f32_16x16x32_bf16 v[0:3], v[162:165], v[194:197], v[0:3]
	v_mfma_f32_16x16x32_bf16 v[52:55], v[158:161], v[174:177], v[52:55]
	v_mfma_f32_16x16x32_bf16 v[48:51], v[166:169], v[174:177], v[48:51]
	v_mfma_f32_16x16x32_bf16 v[36:39], v[158:161], v[182:185], v[36:39]
	v_mfma_f32_16x16x32_bf16 v[32:35], v[166:169], v[182:185], v[32:35]
	v_mfma_f32_16x16x32_bf16 v[20:23], v[158:161], v[190:193], v[20:23]
	v_mfma_f32_16x16x32_bf16 v[16:19], v[166:169], v[190:193], v[16:19]
	v_mfma_f32_16x16x32_bf16 v[4:7], v[158:161], v[198:201], v[4:7]
	v_mfma_f32_16x16x32_bf16 v[0:3], v[166:169], v[198:201], v[0:3]
	s_waitcnt vmcnt(8)
	s_barrier
	s_add_u32 s35, s35, 0x100
	s_addc_u32 s45, s45, 0
	s_add_u32 s49, s49, 0x100
	s_addc_u32 s58, s58, 0
	s_add_u32 s59, s59, 0x100
	s_addc_u32 s70, s70, 0
	s_add_u32 s50, s50, 0x100
	s_addc_u32 s51, s51, 0
	s_cmp_ge_i32 s71, s2
	s_mov_b32 s52, s71
	s_cbranch_scc0 .LBB0_576
	s_and_b64 vcc, exec, s[14:15]
	s_cbranch_vccz .LBB0_579

; #define G_STAGE(bufoff, gbase, voff) do { _Pragma("unroll") for (int _i = 0; _i < 2; ++_i) \
;         __builtin_amdgcn_global_load_lds((const unsigned*)((const char*)(gbase) + (voff)[_i]), (LAS unsigned*)(lds + (bufoff) + ldsw + _i * 8192), 16, 0, 0); } while (0)
; #define G_LDA(dst, b, h) do { _Pragma("unroll") for (int m = 0; m < 4; ++m) G_LD8(dst[m], lds + G_SA(b, h) + aoff + m * 2048); } while (0)
; #define G_LDB(dst, b, h) do { _Pragma("unroll") for (int n = 0; n < 2; ++n) G_LD8(dst[n], lds + G_SB(b, h) + boff + n * 2048); } while (0)
; #define G_WAIT_V(n) asm volatile("s_waitcnt vmcnt(" #n ")" ::: "memory")
; #define G_WAIT_L(n) asm volatile("s_waitcnt lgkmcnt(" #n ")" ::: "memory")
; #define G_BAR __builtin_amdgcn_s_barrier()
; #define G_SCHED __builtin_amdgcn_sched_barrier(0)
;     ...
;             const char* a11 = cur.a1 + (size_t)(t + 1) * kstep;
;             const char* a02 = last ? nxt.a0 : cur.a0 + (size_t)(t + 2) * kstep; const char* a12 = last ? nxt.a1 : cur.a1 + (size_t)(t + 2) * kstep;
;             const char* b02 = last ? nxt.b0 : cur.b0 + (size_t)(t + 2) * kstep; const char* b12 = last ? nxt.b1 : cur.b1 + (size_t)(t + 2) * kstep;
;             G_LDB(B0, 0, 0); G_LDB(B1, 0, 1); G_SCHED; G_LDA(At, 0, 0); G_STAGE(G_SA(1, 1), a11, vA1);
;             if constexpr (GATHER) { if (last) { int tz = tid; asm volatile("" : "+v"(tz));
; #pragma unroll
;                 for (int i = 0; i < 2; ++i) { int R, C; stage_rc(tz * 16 + i * 8192, R, C); gc0[i] = S.row_off(nxt, R, lds) + (unsigned)C * 2u; gc1[i] = S.row_off(nxt, 128 + R, lds) + (unsigned)C * 2u; } } }
;             G_WAIT_L(0); G_BAR; G_MMA(0, 0, At, B0); G_MMA(0, 1, At, B1); G_WAIT_V(8); G_BAR; G_SCHED;
;             G_LDA(At, 0, 1); G_STAGE(G_SB(0, 0), b02, voffB); G_STAGE(G_SB(0, 1), b12, voffB); G_STAGE(G_SA(0, 0), a02, vA0);
;             G_WAIT_L(0); G_BAR; G_MMA(1, 0, At, B0); G_MMA(1, 1, At, B1); G_WAIT_V(8); G_BAR; G_SCHED;
;             G_LDB(B0, 1, 0); G_LDB(B1, 1, 1); G_SCHED; G_LDA(At, 1, 0); G_STAGE(G_SA(0, 1), a12, vA1);
;             G_WAIT_L(0); G_BAR; G_MMA(0, 0, At, B0); G_MMA(0, 1, At, B1); G_WAIT_V(8); G_BAR; G_SCHED;
;             G_LDA(At, 1, 1); G_STAGE(G_SB(1, 0), b02 + kstep, voffB); G_STAGE(G_SB(1, 1), b12 + kstep, voffB); G_STAGE(G_SA(1, 0), a02 + kstep, vA0);
;             G_WAIT_L(0); G_BAR; G_MMA(1, 0, At, B0); G_MMA(1, 1, At, B1); G_WAIT_V(8); G_BAR; G_SCHED;
.LBB0_812:
	s_add_i32 s74, s54, 2
	ds_read_b128 v[138:141], v134
	ds_read_b128 v[142:145], v134 offset:1024
	ds_read_b128 v[146:149], v134 offset:2048
	ds_read_b128 v[150:153], v134 offset:3072
	ds_read_b128 v[154:157], v135
	ds_read_b128 v[158:161], v135 offset:1024
	ds_read_b128 v[162:165], v135 offset:2048
	ds_read_b128 v[166:169], v135 offset:3072
	s_add_u32 s75, s52, 0x80
	s_addc_u32 s55, s53, 0
	s_add_i32 s78, s68, s20
	s_add_i32 m0, s22, 0xc000
	s_add_i32 s77, s22, 0xe000
	s_add_i32 s79, s78, 0x2000
	s_cmp_eq_u32 s67, s54
	s_cselect_b32 s54, s46, s75
	s_cselect_b32 s57, s49, s73
	s_cselect_b32 s56, s48, s72
	s_cselect_b32 s59, s43, s61
	s_cselect_b32 s58, s42, s60
	s_cselect_b32 s55, s47, s55
	ds_read_b128 v[170:173], v136
	ds_read_b128 v[174:177], v136 offset:1024
	ds_read_b128 v[178:181], v136 offset:2048
	ds_read_b128 v[182:185], v136 offset:3072
	ds_read_b128 v[186:189], v136 offset:4096
	ds_read_b128 v[190:193], v136 offset:5120
	ds_read_b128 v[194:197], v136 offset:6144
	ds_read_b128 v[198:201], v136 offset:7168
	global_load_lds_dwordx4 v240, s[52:53]
	s_mov_b32 m0, s77
	v_mov_b32_e32 v205, v129
	global_load_lds_dwordx4 v242, s[52:53]
	s_waitcnt lgkmcnt(0)
	s_waitcnt vmcnt(8)
	s_barrier
	s_waitcnt lgkmcnt(0)
	v_mfma_f32_16x16x32_bf16 v[124:127], v[138:141], v[170:173], v[124:127]
	v_mfma_f32_16x16x32_bf16 v[120:123], v[146:149], v[170:173], v[120:123]
	v_mfma_f32_16x16x32_bf16 v[108:111], v[138:141], v[178:181], v[108:111]
	v_mfma_f32_16x16x32_bf16 v[104:107], v[146:149], v[178:181], v[104:107]
	v_mfma_f32_16x16x32_bf16 v[92:95], v[138:141], v[186:189], v[92:95]
	v_mfma_f32_16x16x32_bf16 v[88:91], v[146:149], v[186:189], v[88:91]
	v_mfma_f32_16x16x32_bf16 v[76:79], v[138:141], v[194:197], v[76:79]
	v_mfma_f32_16x16x32_bf16 v[72:75], v[146:149], v[194:197], v[72:75]
	v_mfma_f32_16x16x32_bf16 v[124:127], v[142:145], v[174:177], v[124:127]
	v_mfma_f32_16x16x32_bf16 v[120:123], v[150:153], v[174:177], v[120:123]
	v_mfma_f32_16x16x32_bf16 v[108:111], v[142:145], v[182:185], v[108:111]
	v_mfma_f32_16x16x32_bf16 v[104:107], v[150:153], v[182:185], v[104:107]
	v_mfma_f32_16x16x32_bf16 v[92:95], v[142:145], v[190:193], v[92:95]
	v_mfma_f32_16x16x32_bf16 v[88:91], v[150:153], v[190:193], v[88:91]
	v_mfma_f32_16x16x32_bf16 v[76:79], v[142:145], v[198:201], v[76:79]
	v_mfma_f32_16x16x32_bf16 v[72:75], v[150:153], v[198:201], v[72:75]
	v_mfma_f32_16x16x32_bf16 v[116:119], v[154:157], v[170:173], v[116:119]
	v_mfma_f32_16x16x32_bf16 v[112:115], v[162:165], v[170:173], v[112:115]
	v_mfma_f32_16x16x32_bf16 v[100:103], v[154:157], v[178:181], v[100:103]
	v_mfma_f32_16x16x32_bf16 v[96:99], v[162:165], v[178:181], v[96:99]
	v_mfma_f32_16x16x32_bf16 v[84:87], v[154:157], v[186:189], v[84:87]
	v_mfma_f32_16x16x32_bf16 v[80:83], v[162:165], v[186:189], v[80:83]
	v_mfma_f32_16x16x32_bf16 v[68:71], v[154:157], v[194:197], v[68:71]
	v_mfma_f32_16x16x32_bf16 v[64:67], v[162:165], v[194:197], v[64:67]
	v_mfma_f32_16x16x32_bf16 v[116:119], v[158:161], v[174:177], v[116:119]
	v_mfma_f32_16x16x32_bf16 v[112:115], v[166:169], v[174:177], v[112:115]
	v_mfma_f32_16x16x32_bf16 v[100:103], v[158:161], v[182:185], v[100:103]
	v_mfma_f32_16x16x32_bf16 v[96:99], v[166:169], v[182:185], v[96:99]
	v_mfma_f32_16x16x32_bf16 v[84:87], v[158:161], v[190:193], v[84:87]
	v_mfma_f32_16x16x32_bf16 v[80:83], v[166:169], v[190:193], v[80:83]
	v_mfma_f32_16x16x32_bf16 v[68:71], v[158:161], v[198:201], v[68:71]
	v_mfma_f32_16x16x32_bf16 v[64:67], v[166:169], v[198:201], v[64:67]
	s_waitcnt vmcnt(8)
	s_barrier
	s_mov_b32 m0, s78
	ds_read_b128 v[170:173], v136 offset:16384
	ds_read_b128 v[174:177], v136 offset:17408
	ds_read_b128 v[178:181], v136 offset:18432
	ds_read_b128 v[182:185], v136 offset:19456
	ds_read_b128 v[186:189], v136 offset:20480
	ds_read_b128 v[190:193], v136 offset:21504
	ds_read_b128 v[194:197], v136 offset:22528
	ds_read_b128 v[198:201], v136 offset:23552
	global_load_lds_dwordx4 v244, s[58:59]
	s_mov_b32 m0, s79
	s_cselect_b32 s79, s45, s71
	s_cselect_b32 s78, s44, s62
	s_add_i32 s75, s69, s20
	global_load_lds_dwordx4 v246, s[58:59]
	s_mov_b32 m0, s75
	v_mov_b32_e32 v203, v129
	global_load_lds_dwordx4 v244, s[78:79]
	s_add_i32 m0, s75, 0x2000
	v_mov_b32_e32 v207, v129
	global_load_lds_dwordx4 v246, s[78:79]
	s_mov_b32 m0, s22
	v_lshl_add_u64 v[208:209], s[58:59], 0, v[244:245]
	global_load_lds_dwordx4 v240, s[56:57]
	s_mov_b32 m0, s23
	v_lshl_add_u64 v[210:211], s[58:59], 0, v[246:247]
	global_load_lds_dwordx4 v242, s[56:57]
	s_waitcnt lgkmcnt(0)
	v_lshl_add_u64 v[202:203], s[78:79], 0, v[244:245]
	v_lshl_add_u64 v[206:207], s[78:79], 0, v[246:247]
	v_lshl_add_u64 v[212:213], s[56:57], 0, v[240:241]
	v_lshl_add_u64 v[214:215], s[56:57], 0, v[242:243]
	s_waitcnt vmcnt(8)
	s_barrier
; #define G_STAGE(bufoff, gbase, voff) do { _Pragma("unroll") for (int _i = 0; _i < 2; ++_i) \
;         __builtin_amdgcn_global_load_lds((const unsigned*)((const char*)(gbase) + (voff)[_i]), (LAS unsigned*)(lds + (bufoff) + ldsw + _i * 8192), 16, 0, 0); } while (0)
; #define G_LDA(dst, b, h) do { _Pragma("unroll") for (int m = 0; m < 4; ++m) G_LD8(dst[m], lds + G_SA(b, h) + aoff + m * 2048); } while (0)
; #define G_LDB(dst, b, h) do { _Pragma("unroll") for (int n = 0; n < 2; ++n) G_LD8(dst[n], lds + G_SB(b, h) + boff + n * 2048); } while (0)
; #define G_WAIT_V(n) asm volatile("s_waitcnt vmcnt(" #n ")" ::: "memory")
; #define G_WAIT_L(n) asm volatile("s_waitcnt lgkmcnt(" #n ")" ::: "memory")
; #define G_BAR __builtin_amdgcn_s_barrier()
; #define G_SCHED __builtin_amdgcn_sched_barrier(0)
;     __device__ __forceinline__ unsigned row_off(const Unit& u, int r, LAS unsigned char* lds) const { return (unsigned)((const LAS int*)(lds + LDS_STAGE + u.q * 4096))[r] * (unsigned)rowbytes; }
;     ...
;             G_LDB(B0, 0, 0); G_LDB(B1, 0, 1); G_SCHED; G_LDA(At, 0, 0); G_STAGE(G_SA(1, 1), a11, vA1);
;             if constexpr (GATHER) { if (last) { int tz = tid; asm volatile("" : "+v"(tz));
; #pragma unroll
;                 for (int i = 0; i < 2; ++i) { int R, C; stage_rc(tz * 16 + i * 8192, R, C); gc0[i] = S.row_off(nxt, R, lds) + (unsigned)C * 2u; gc1[i] = S.row_off(nxt, 128 + R, lds) + (unsigned)C * 2u; } } }
;             G_WAIT_L(0); G_BAR; G_MMA(0, 0, At, B0); G_MMA(0, 1, At, B1); G_WAIT_V(8); G_BAR; G_SCHED;
;             G_LDA(At, 0, 1); G_STAGE(G_SB(0, 0), b02, voffB); G_STAGE(G_SB(0, 1), b12, voffB); G_STAGE(G_SA(0, 0), a02, vA0);
;             G_WAIT_L(0); G_BAR; G_MMA(1, 0, At, B0); G_MMA(1, 1, At, B1); G_WAIT_V(8); G_BAR; G_SCHED;
;             G_LDB(B0, 1, 0); G_LDB(B1, 1, 1); G_SCHED; G_LDA(At, 1, 0); G_STAGE(G_SA(0, 1), a12, vA1);
;             G_WAIT_L(0); G_BAR; G_MMA(0, 0, At, B0); G_MMA(0, 1, At, B1); G_WAIT_V(8); G_BAR; G_SCHED;
;             G_LDA(At, 1, 1); G_STAGE(G_SB(1, 0), b02 + kstep, voffB); G_STAGE(G_SB(1, 1), b12 + kstep, voffB); G_STAGE(G_SA(1, 0), a02 + kstep, vA0);
;             G_WAIT_L(0); G_BAR; G_MMA(1, 0, At, B0); G_MMA(1, 1, At, B1); G_WAIT_V(8); G_BAR; G_SCHED;
	s_waitcnt lgkmcnt(0)
	v_mfma_f32_16x16x32_bf16 v[60:63], v[138:141], v[170:173], v[60:63]
	v_mfma_f32_16x16x32_bf16 v[56:59], v[146:149], v[170:173], v[56:59]
	v_mfma_f32_16x16x32_bf16 v[44:47], v[138:141], v[178:181], v[44:47]
	v_mfma_f32_16x16x32_bf16 v[40:43], v[146:149], v[178:181], v[40:43]
	v_mfma_f32_16x16x32_bf16 v[28:31], v[138:141], v[186:189], v[28:31]
	v_mfma_f32_16x16x32_bf16 v[24:27], v[146:149], v[186:189], v[24:27]
	v_mfma_f32_16x16x32_bf16 v[12:15], v[138:141], v[194:197], v[12:15]
	v_mfma_f32_16x16x32_bf16 v[8:11], v[146:149], v[194:197], v[8:11]
	v_mfma_f32_16x16x32_bf16 v[60:63], v[142:145], v[174:177], v[60:63]
	v_mfma_f32_16x16x32_bf16 v[56:59], v[150:153], v[174:177], v[56:59]
	v_mfma_f32_16x16x32_bf16 v[44:47], v[142:145], v[182:185], v[44:47]
	v_mfma_f32_16x16x32_bf16 v[40:43], v[150:153], v[182:185], v[40:43]
	v_mfma_f32_16x16x32_bf16 v[28:31], v[142:145], v[190:193], v[28:31]
	v_mfma_f32_16x16x32_bf16 v[24:27], v[150:153], v[190:193], v[24:27]
	v_mfma_f32_16x16x32_bf16 v[12:15], v[142:145], v[198:201], v[12:15]
	v_mfma_f32_16x16x32_bf16 v[8:11], v[150:153], v[198:201], v[8:11]
	v_mfma_f32_16x16x32_bf16 v[52:55], v[154:157], v[170:173], v[52:55]
	v_mfma_f32_16x16x32_bf16 v[48:51], v[162:165], v[170:173], v[48:51]
	v_mfma_f32_16x16x32_bf16 v[36:39], v[154:157], v[178:181], v[36:39]
	v_mfma_f32_16x16x32_bf16 v[32:35], v[162:165], v[178:181], v[32:35]
	v_mfma_f32_16x16x32_bf16 v[20:23], v[154:157], v[186:189], v[20:23]
	v_mfma_f32_16x16x32_bf16 v[16:19], v[162:165], v[186:189], v[16:19]
	v_mfma_f32_16x16x32_bf16 v[4:7], v[154:157], v[194:197], v[4:7]
	v_mfma_f32_16x16x32_bf16 v[0:3], v[162:165], v[194:197], v[0:3]
	v_mfma_f32_16x16x32_bf16 v[52:55], v[158:161], v[174:177], v[52:55]
	v_mfma_f32_16x16x32_bf16 v[48:51], v[166:169], v[174:177], v[48:51]
	v_mfma_f32_16x16x32_bf16 v[36:39], v[158:161], v[182:185], v[36:39]
	v_mfma_f32_16x16x32_bf16 v[32:35], v[166:169], v[182:185], v[32:35]
	v_mfma_f32_16x16x32_bf16 v[20:23], v[158:161], v[190:193], v[20:23]
	v_mfma_f32_16x16x32_bf16 v[16:19], v[166:169], v[190:193], v[16:19]
	v_mfma_f32_16x16x32_bf16 v[4:7], v[158:161], v[198:201], v[4:7]
	v_mfma_f32_16x16x32_bf16 v[0:3], v[166:169], v[198:201], v[0:3]
	s_waitcnt vmcnt(8)
	s_barrier
	s_add_i32 s56, 0, 0x18000
	v_add_u32_e32 v137, s56, v133
	s_add_i32 s57, 0, 0x1c000
	ds_read_b128 v[138:141], v137
	ds_read_b128 v[142:145], v137 offset:1024
	ds_read_b128 v[146:149], v137 offset:2048
	ds_read_b128 v[150:153], v137 offset:3072
	v_add_u32_e32 v137, s57, v133
	ds_read_b128 v[154:157], v137
	ds_read_b128 v[158:161], v137 offset:1024
	ds_read_b128 v[162:165], v137 offset:2048
	ds_read_b128 v[166:169], v137 offset:3072
	s_mov_b32 m0, s24
	ds_read_b128 v[170:173], v136 offset:32768
	ds_read_b128 v[174:177], v136 offset:33792
	ds_read_b128 v[178:181], v136 offset:34816
	ds_read_b128 v[182:185], v136 offset:35840
	ds_read_b128 v[186:189], v136 offset:36864
	ds_read_b128 v[190:193], v136 offset:37888
	ds_read_b128 v[194:197], v136 offset:38912
	ds_read_b128 v[198:201], v136 offset:39936
	global_load_lds_dwordx4 v240, s[54:55]
	s_mov_b32 m0, s25
	s_nop 0
	global_load_lds_dwordx4 v242, s[54:55]
	s_waitcnt lgkmcnt(0)
	s_waitcnt vmcnt(8)
	s_barrier
	s_waitcnt lgkmcnt(0)
	v_mfma_f32_16x16x32_bf16 v[124:127], v[138:141], v[170:173], v[124:127]
	v_mfma_f32_16x16x32_bf16 v[120:123], v[146:149], v[170:173], v[120:123]
	v_mfma_f32_16x16x32_bf16 v[108:111], v[138:141], v[178:181], v[108:111]
	v_mfma_f32_16x16x32_bf16 v[104:107], v[146:149], v[178:181], v[104:107]
	v_mfma_f32_16x16x32_bf16 v[92:95], v[138:141], v[186:189], v[92:95]
	v_mfma_f32_16x16x32_bf16 v[88:91], v[146:149], v[186:189], v[88:91]
	v_mfma_f32_16x16x32_bf16 v[76:79], v[138:141], v[194:197], v[76:79]
	v_mfma_f32_16x16x32_bf16 v[72:75], v[146:149], v[194:197], v[72:75]
	v_mfma_f32_16x16x32_bf16 v[124:127], v[142:145], v[174:177], v[124:127]
	v_mfma_f32_16x16x32_bf16 v[120:123], v[150:153], v[174:177], v[120:123]
	v_mfma_f32_16x16x32_bf16 v[108:111], v[142:145], v[182:185], v[108:111]
	v_mfma_f32_16x16x32_bf16 v[104:107], v[150:153], v[182:185], v[104:107]
	v_mfma_f32_16x16x32_bf16 v[92:95], v[142:145], v[190:193], v[92:95]
	v_mfma_f32_16x16x32_bf16 v[88:91], v[150:153], v[190:193], v[88:91]
	v_mfma_f32_16x16x32_bf16 v[76:79], v[142:145], v[198:201], v[76:79]
	v_mfma_f32_16x16x32_bf16 v[72:75], v[150:153], v[198:201], v[72:75]
	v_mfma_f32_16x16x32_bf16 v[116:119], v[154:157], v[170:173], v[116:119]
	v_mfma_f32_16x16x32_bf16 v[112:115], v[162:165], v[170:173], v[112:115]
	v_mfma_f32_16x16x32_bf16 v[100:103], v[154:157], v[178:181], v[100:103]
	v_mfma_f32_16x16x32_bf16 v[96:99], v[162:165], v[178:181], v[96:99]
	v_mfma_f32_16x16x32_bf16 v[84:87], v[154:157], v[186:189], v[84:87]
	v_mfma_f32_16x16x32_bf16 v[80:83], v[162:165], v[186:189], v[80:83]
	v_mfma_f32_16x16x32_bf16 v[68:71], v[154:157], v[194:197], v[68:71]
	v_mfma_f32_16x16x32_bf16 v[64:67], v[162:165], v[194:197], v[64:67]
	v_mfma_f32_16x16x32_bf16 v[116:119], v[158:161], v[174:177], v[116:119]
	v_mfma_f32_16x16x32_bf16 v[112:115], v[166:169], v[174:177], v[112:115]
	v_mfma_f32_16x16x32_bf16 v[100:103], v[158:161], v[182:185], v[100:103]
	v_mfma_f32_16x16x32_bf16 v[96:99], v[166:169], v[182:185], v[96:99]
	v_mfma_f32_16x16x32_bf16 v[84:87], v[158:161], v[190:193], v[84:87]
	v_mfma_f32_16x16x32_bf16 v[80:83], v[166:169], v[190:193], v[80:83]
	v_mfma_f32_16x16x32_bf16 v[68:71], v[158:161], v[198:201], v[68:71]
	v_mfma_f32_16x16x32_bf16 v[64:67], v[166:169], v[198:201], v[64:67]
	s_waitcnt vmcnt(8)
	s_barrier
; #define G_STAGE(bufoff, gbase, voff) do { _Pragma("unroll") for (int _i = 0; _i < 2; ++_i) \
;         __builtin_amdgcn_global_load_lds((const unsigned*)((const char*)(gbase) + (voff)[_i]), (LAS unsigned*)(lds + (bufoff) + ldsw + _i * 8192), 16, 0, 0); } while (0)
; #define G_LDA(dst, b, h) do { _Pragma("unroll") for (int m = 0; m < 4; ++m) G_LD8(dst[m], lds + G_SA(b, h) + aoff + m * 2048); } while (0)
; #define G_LDB(dst, b, h) do { _Pragma("unroll") for (int n = 0; n < 2; ++n) G_LD8(dst[n], lds + G_SB(b, h) + boff + n * 2048); } while (0)
; #define G_WAIT_V(n) asm volatile("s_waitcnt vmcnt(" #n ")" ::: "memory")
; #define G_WAIT_L(n) asm volatile("s_waitcnt lgkmcnt(" #n ")" ::: "memory")
; #define G_BAR __builtin_amdgcn_s_barrier()
; #define G_SCHED __builtin_amdgcn_sched_barrier(0)
;     ...
;             G_LDA(At, 0, 1); G_STAGE(G_SB(0, 0), b02, voffB); G_STAGE(G_SB(0, 1), b12, voffB); G_STAGE(G_SA(0, 0), a02, vA0);
;             G_WAIT_L(0); G_BAR; G_MMA(1, 0, At, B0); G_MMA(1, 1, At, B1); G_WAIT_V(8); G_BAR; G_SCHED;
;             G_LDB(B0, 1, 0); G_LDB(B1, 1, 1); G_SCHED; G_LDA(At, 1, 0); G_STAGE(G_SA(0, 1), a12, vA1);
;             G_WAIT_L(0); G_BAR; G_MMA(0, 0, At, B0); G_MMA(0, 1, At, B1); G_WAIT_V(8); G_BAR; G_SCHED;
;             G_LDA(At, 1, 1); G_STAGE(G_SB(1, 0), b02 + kstep, voffB); G_STAGE(G_SB(1, 1), b12 + kstep, voffB); G_STAGE(G_SA(1, 0), a02 + kstep, vA0);
;             G_WAIT_L(0); G_BAR; G_MMA(1, 0, At, B0); G_MMA(1, 1, At, B1); G_WAIT_V(8); G_BAR; G_SCHED;
	s_add_i32 s54, s56, s20
	v_lshl_add_u64 v[204:205], v[208:209], 0, s[36:37]
	s_mov_b32 m0, s54
	ds_read_b128 v[170:173], v136 offset:49152
	ds_read_b128 v[174:177], v136 offset:50176
	ds_read_b128 v[178:181], v136 offset:51200
	ds_read_b128 v[182:185], v136 offset:52224
	ds_read_b128 v[186:189], v136 offset:53248
	ds_read_b128 v[190:193], v136 offset:54272
	ds_read_b128 v[194:197], v136 offset:55296
	ds_read_b128 v[198:201], v136 offset:56320
	global_load_lds_dwordx4 v[204:205], off
	v_lshl_add_u64 v[204:205], v[210:211], 0, s[36:37]
	s_add_i32 m0, s54, 0x2000
	s_add_i32 s54, s57, s20
	global_load_lds_dwordx4 v[204:205], off
	v_lshl_add_u64 v[202:203], v[202:203], 0, s[36:37]
	s_mov_b32 m0, s54
	s_nop 0
	global_load_lds_dwordx4 v[202:203], off
	v_lshl_add_u64 v[202:203], v[206:207], 0, s[36:37]
	s_add_i32 m0, s54, 0x2000
	s_nop 0
	global_load_lds_dwordx4 v[202:203], off
	v_lshl_add_u64 v[202:203], v[212:213], 0, s[36:37]
	s_mov_b32 m0, s65
	s_nop 0
	global_load_lds_dwordx4 v[202:203], off
	v_lshl_add_u64 v[202:203], v[214:215], 0, s[36:37]
	s_mov_b32 m0, s66
	s_nop 0
	global_load_lds_dwordx4 v[202:203], off
	s_waitcnt lgkmcnt(0)
	s_waitcnt vmcnt(8)
	s_barrier
	s_waitcnt lgkmcnt(0)
	v_mfma_f32_16x16x32_bf16 v[60:63], v[138:141], v[170:173], v[60:63]
	v_mfma_f32_16x16x32_bf16 v[56:59], v[146:149], v[170:173], v[56:59]
	v_mfma_f32_16x16x32_bf16 v[44:47], v[138:141], v[178:181], v[44:47]
	v_mfma_f32_16x16x32_bf16 v[40:43], v[146:149], v[178:181], v[40:43]
	v_mfma_f32_16x16x32_bf16 v[28:31], v[138:141], v[186:189], v[28:31]
	v_mfma_f32_16x16x32_bf16 v[24:27], v[146:149], v[186:189], v[24:27]
	v_mfma_f32_16x16x32_bf16 v[12:15], v[138:141], v[194:197], v[12:15]
	v_mfma_f32_16x16x32_bf16 v[8:11], v[146:149], v[194:197], v[8:11]
	v_mfma_f32_16x16x32_bf16 v[60:63], v[142:145], v[174:177], v[60:63]
	v_mfma_f32_16x16x32_bf16 v[56:59], v[150:153], v[174:177], v[56:59]
	v_mfma_f32_16x16x32_bf16 v[44:47], v[142:145], v[182:185], v[44:47]
	v_mfma_f32_16x16x32_bf16 v[40:43], v[150:153], v[182:185], v[40:43]
	v_mfma_f32_16x16x32_bf16 v[28:31], v[142:145], v[190:193], v[28:31]
	v_mfma_f32_16x16x32_bf16 v[24:27], v[150:153], v[190:193], v[24:27]
	v_mfma_f32_16x16x32_bf16 v[12:15], v[142:145], v[198:201], v[12:15]
	v_mfma_f32_16x16x32_bf16 v[8:11], v[150:153], v[198:201], v[8:11]
	v_mfma_f32_16x16x32_bf16 v[52:55], v[154:157], v[170:173], v[52:55]
	v_mfma_f32_16x16x32_bf16 v[48:51], v[162:165], v[170:173], v[48:51]
	v_mfma_f32_16x16x32_bf16 v[36:39], v[154:157], v[178:181], v[36:39]
	v_mfma_f32_16x16x32_bf16 v[32:35], v[162:165], v[178:181], v[32:35]
	v_mfma_f32_16x16x32_bf16 v[20:23], v[154:157], v[186:189], v[20:23]
	v_mfma_f32_16x16x32_bf16 v[16:19], v[162:165], v[186:189], v[16:19]
	v_mfma_f32_16x16x32_bf16 v[4:7], v[154:157], v[194:197], v[4:7]
	v_mfma_f32_16x16x32_bf16 v[0:3], v[162:165], v[194:197], v[0:3]
	v_mfma_f32_16x16x32_bf16 v[52:55], v[158:161], v[174:177], v[52:55]
	v_mfma_f32_16x16x32_bf16 v[48:51], v[166:169], v[174:177], v[48:51]
	v_mfma_f32_16x16x32_bf16 v[36:39], v[158:161], v[182:185], v[36:39]
	v_mfma_f32_16x16x32_bf16 v[32:35], v[166:169], v[182:185], v[32:35]
	v_mfma_f32_16x16x32_bf16 v[20:23], v[158:161], v[190:193], v[20:23]
	v_mfma_f32_16x16x32_bf16 v[16:19], v[166:169], v[190:193], v[16:19]
	v_mfma_f32_16x16x32_bf16 v[4:7], v[158:161], v[198:201], v[4:7]
	v_mfma_f32_16x16x32_bf16 v[0:3], v[166:169], v[198:201], v[0:3]
	s_waitcnt vmcnt(8)
	s_barrier
	s_add_u32 s60, s60, 0x100
	s_addc_u32 s61, s61, 0
	s_add_u32 s62, s62, 0x100
	s_addc_u32 s71, s71, 0
	s_add_u32 s72, s72, 0x100
	s_addc_u32 s73, s73, 0
	s_add_u32 s52, s52, 0x100
	s_addc_u32 s53, s53, 0
	s_cmp_ge_i32 s74, s0
	s_mov_b32 s54, s74
	s_cbranch_scc0 .LBB0_812
	v_readlane_b32 s78, v255, 11
	v_readlane_b32 s79, v255, 13
	s_and_b64 vcc, exec, s[40:41]
	s_cbranch_vccz .LBB0_815

; #define G_STAGE(bufoff, gbase, voff) do { _Pragma("unroll") for (int _i = 0; _i < 2; ++_i) \
;         __builtin_amdgcn_global_load_lds((const unsigned*)((const char*)(gbase) + (voff)[_i]), (LAS unsigned*)(lds + (bufoff) + ldsw + _i * 8192), 16, 0, 0); } while (0)
; #define G_LDA(dst, b, h) do { _Pragma("unroll") for (int m = 0; m < 4; ++m) G_LD8(dst[m], lds + G_SA(b, h) + aoff + m * 2048); } while (0)
; #define G_LDB(dst, b, h) do { _Pragma("unroll") for (int n = 0; n < 2; ++n) G_LD8(dst[n], lds + G_SB(b, h) + boff + n * 2048); } while (0)
; #define G_WAIT_V(n) asm volatile("s_waitcnt vmcnt(" #n ")" ::: "memory")
; #define G_WAIT_L(n) asm volatile("s_waitcnt lgkmcnt(" #n ")" ::: "memory")
; #define G_BAR __builtin_amdgcn_s_barrier()
; #define G_SCHED __builtin_amdgcn_sched_barrier(0)
;     __device__ __forceinline__ unsigned row_off(const Unit& u, int r, LAS unsigned char* lds) const { return (unsigned)((const LAS int*)(lds + LDS_STAGE + u.q * 4096))[r] * (unsigned)rowbytes; }
;     ...
;             G_LDB(B0, 0, 0); G_LDB(B1, 0, 1); G_SCHED; G_LDA(At, 0, 0); G_STAGE(G_SA(1, 1), a11, vA1);
;             if constexpr (GATHER) { if (last) { int tz = tid; asm volatile("" : "+v"(tz));
; #pragma unroll
;                 for (int i = 0; i < 2; ++i) { int R, C; stage_rc(tz * 16 + i * 8192, R, C); gc0[i] = S.row_off(nxt, R, lds) + (unsigned)C * 2u; gc1[i] = S.row_off(nxt, 128 + R, lds) + (unsigned)C * 2u; } } }
;             G_WAIT_L(0); G_BAR; G_MMA(0, 0, At, B0); G_MMA(0, 1, At, B1); G_WAIT_V(8); G_BAR; G_SCHED;
;             G_LDA(At, 0, 1); G_STAGE(G_SB(0, 0), b02, voffB); G_STAGE(G_SB(0, 1), b12, voffB); G_STAGE(G_SA(0, 0), a02, vA0);
;             G_WAIT_L(0); G_BAR; G_MMA(1, 0, At, B0); G_MMA(1, 1, At, B1); G_WAIT_V(8); G_BAR; G_SCHED;
;             G_LDB(B0, 1, 0); G_LDB(B1, 1, 1); G_SCHED; G_LDA(At, 1, 0); G_STAGE(G_SA(0, 1), a12, vA1);
;             G_WAIT_L(0); G_BAR; G_MMA(0, 0, At, B0); G_MMA(0, 1, At, B1); G_WAIT_V(8); G_BAR; G_SCHED;
;             G_LDA(At, 1, 1); G_STAGE(G_SB(1, 0), b02 + kstep, voffB); G_STAGE(G_SB(1, 1), b12 + kstep, voffB); G_STAGE(G_SA(1, 0), a02 + kstep, vA0);
;             G_WAIT_L(0); G_BAR; G_MMA(1, 0, At, B0); G_MMA(1, 1, At, B1); G_WAIT_V(8); G_BAR; G_SCHED;
.LBB0_1023:
	s_add_i32 s78, s54, 2
	ds_read_b128 v[72:75], v70
	ds_read_b128 v[76:79], v70 offset:1024
	ds_read_b128 v[80:83], v70 offset:2048
	ds_read_b128 v[84:87], v70 offset:3072
	s_add_u32 s79, s52, 0x80
	s_addc_u32 s55, s53, 0
	s_add_i32 s81, s73, s20
	s_add_i32 m0, s23, 0xc000
	s_add_i32 s80, s23, 0xe000
	s_add_i32 s82, s81, 0x2000
	s_cmp_eq_u32 s72, s54
	s_cselect_b32 s54, s44, s79
	s_cselect_b32 s57, s43, s77
	s_cselect_b32 s56, s42, s75
	s_cselect_b32 s59, s49, s61
	s_cselect_b32 s58, s48, s60
	s_cselect_b32 s55, s45, s55
	ds_read_b128 v[88:91], v71
	ds_read_b128 v[92:95], v71 offset:1024
	ds_read_b128 v[96:99], v71 offset:2048
	ds_read_b128 v[100:103], v71 offset:3072
	ds_read_b128 v[104:107], v71 offset:4096
	ds_read_b128 v[108:111], v71 offset:5120
	ds_read_b128 v[112:115], v71 offset:6144
	ds_read_b128 v[116:119], v71 offset:7168
	global_load_lds_dwordx4 v240, s[52:53]
	s_mov_b32 m0, s80
	v_mov_b32_e32 v123, v65
	global_load_lds_dwordx4 v242, s[52:53]
	s_waitcnt lgkmcnt(0)
	s_waitcnt vmcnt(8)
	s_barrier
	s_waitcnt lgkmcnt(0)
	v_mfma_f32_16x16x32_bf16 v[60:63], v[72:75], v[88:91], v[60:63]
	v_mfma_f32_16x16x32_bf16 v[56:59], v[80:83], v[88:91], v[56:59]
	v_mfma_f32_16x16x32_bf16 v[52:55], v[72:75], v[96:99], v[52:55]
	v_mfma_f32_16x16x32_bf16 v[48:51], v[80:83], v[96:99], v[48:51]
	v_mfma_f32_16x16x32_bf16 v[44:47], v[72:75], v[104:107], v[44:47]
	v_mfma_f32_16x16x32_bf16 v[40:43], v[80:83], v[104:107], v[40:43]
	v_mfma_f32_16x16x32_bf16 v[36:39], v[72:75], v[112:115], v[36:39]
	v_mfma_f32_16x16x32_bf16 v[32:35], v[80:83], v[112:115], v[32:35]
	v_mfma_f32_16x16x32_bf16 v[60:63], v[76:79], v[92:95], v[60:63]
	v_mfma_f32_16x16x32_bf16 v[56:59], v[84:87], v[92:95], v[56:59]
	v_mfma_f32_16x16x32_bf16 v[52:55], v[76:79], v[100:103], v[52:55]
	v_mfma_f32_16x16x32_bf16 v[48:51], v[84:87], v[100:103], v[48:51]
	v_mfma_f32_16x16x32_bf16 v[44:47], v[76:79], v[108:111], v[44:47]
	v_mfma_f32_16x16x32_bf16 v[40:43], v[84:87], v[108:111], v[40:43]
	v_mfma_f32_16x16x32_bf16 v[36:39], v[76:79], v[116:119], v[36:39]
	v_mfma_f32_16x16x32_bf16 v[32:35], v[84:87], v[116:119], v[32:35]
	s_waitcnt vmcnt(8)
	s_barrier
	s_mov_b32 m0, s81
	ds_read_b128 v[88:91], v71 offset:16384
	ds_read_b128 v[92:95], v71 offset:17408
	ds_read_b128 v[96:99], v71 offset:18432
	ds_read_b128 v[100:103], v71 offset:19456
	ds_read_b128 v[104:107], v71 offset:20480
	ds_read_b128 v[108:111], v71 offset:21504
	ds_read_b128 v[112:115], v71 offset:22528
	ds_read_b128 v[116:119], v71 offset:23552
	global_load_lds_dwordx4 v244, s[58:59]
	s_mov_b32 m0, s82
	s_cselect_b32 s81, s47, s74
	global_load_lds_dwordx4 v246, s[58:59]
	s_cselect_b32 s80, s46, s62
	s_mov_b32 m0, s24
	v_mov_b32_e32 v121, v65
	global_load_lds_dwordx4 v244, s[80:81]
	s_mov_b32 m0, s25
	v_mov_b32_e32 v125, v65
	global_load_lds_dwordx4 v246, s[80:81]
	s_mov_b32 m0, s23
	v_lshl_add_u64 v[126:127], s[58:59], 0, v[244:245]
	global_load_lds_dwordx4 v240, s[56:57]
	s_mov_b32 m0, s27
	v_lshl_add_u64 v[128:129], s[58:59], 0, v[246:247]
	global_load_lds_dwordx4 v242, s[56:57]
	s_waitcnt lgkmcnt(0)
	v_lshl_add_u64 v[120:121], s[80:81], 0, v[244:245]
	v_lshl_add_u64 v[124:125], s[80:81], 0, v[246:247]
	v_lshl_add_u64 v[130:131], s[56:57], 0, v[240:241]
	v_lshl_add_u64 v[132:133], s[56:57], 0, v[242:243]
	s_waitcnt vmcnt(8)
	s_barrier
	s_waitcnt lgkmcnt(0)
	v_mfma_f32_16x16x32_bf16 v[28:31], v[72:75], v[88:91], v[28:31]
	v_mfma_f32_16x16x32_bf16 v[24:27], v[80:83], v[88:91], v[24:27]
	v_mfma_f32_16x16x32_bf16 v[20:23], v[72:75], v[96:99], v[20:23]
	v_mfma_f32_16x16x32_bf16 v[16:19], v[80:83], v[96:99], v[16:19]
	v_mfma_f32_16x16x32_bf16 v[12:15], v[72:75], v[104:107], v[12:15]
	v_mfma_f32_16x16x32_bf16 v[8:11], v[80:83], v[104:107], v[8:11]
	v_mfma_f32_16x16x32_bf16 v[4:7], v[72:75], v[112:115], v[4:7]
	v_mfma_f32_16x16x32_bf16 v[0:3], v[80:83], v[112:115], v[0:3]
	v_mfma_f32_16x16x32_bf16 v[28:31], v[76:79], v[92:95], v[28:31]
	v_mfma_f32_16x16x32_bf16 v[24:27], v[84:87], v[92:95], v[24:27]
	v_mfma_f32_16x16x32_bf16 v[20:23], v[76:79], v[100:103], v[20:23]
	v_mfma_f32_16x16x32_bf16 v[16:19], v[84:87], v[100:103], v[16:19]
	v_mfma_f32_16x16x32_bf16 v[12:15], v[76:79], v[108:111], v[12:15]
	v_mfma_f32_16x16x32_bf16 v[8:11], v[84:87], v[108:111], v[8:11]
	v_mfma_f32_16x16x32_bf16 v[4:7], v[76:79], v[116:119], v[4:7]
	v_mfma_f32_16x16x32_bf16 v[0:3], v[84:87], v[116:119], v[0:3]
	s_waitcnt vmcnt(8)
	s_barrier
	s_add_i32 s56, 0, 0x18000
	v_add_u32_e32 v84, s56, v69
	ds_read_b128 v[72:75], v84
	ds_read_b128 v[76:79], v84 offset:1024
	ds_read_b128 v[80:83], v84 offset:2048
	ds_read_b128 v[84:87], v84 offset:3072
	s_mov_b32 m0, s33
	ds_read_b128 v[88:91], v71 offset:32768
	ds_read_b128 v[92:95], v71 offset:33792
	ds_read_b128 v[96:99], v71 offset:34816
	ds_read_b128 v[100:103], v71 offset:35840
	ds_read_b128 v[104:107], v71 offset:36864
	ds_read_b128 v[108:111], v71 offset:37888
	ds_read_b128 v[112:115], v71 offset:38912
	ds_read_b128 v[116:119], v71 offset:39936
	global_load_lds_dwordx4 v240, s[54:55]
	s_mov_b32 m0, s41
	s_nop 0
	global_load_lds_dwordx4 v242, s[54:55]
	s_waitcnt lgkmcnt(0)
	s_waitcnt vmcnt(8)
	s_barrier
; #define G_STAGE(bufoff, gbase, voff) do { _Pragma("unroll") for (int _i = 0; _i < 2; ++_i) \
;         __builtin_amdgcn_global_load_lds((const unsigned*)((const char*)(gbase) + (voff)[_i]), (LAS unsigned*)(lds + (bufoff) + ldsw + _i * 8192), 16, 0, 0); } while (0)
; #define G_LDA(dst, b, h) do { _Pragma("unroll") for (int m = 0; m < 4; ++m) G_LD8(dst[m], lds + G_SA(b, h) + aoff + m * 2048); } while (0)
; #define G_LDB(dst, b, h) do { _Pragma("unroll") for (int n = 0; n < 2; ++n) G_LD8(dst[n], lds + G_SB(b, h) + boff + n * 2048); } while (0)
; #define G_WAIT_V(n) asm volatile("s_waitcnt vmcnt(" #n ")" ::: "memory")
; #define G_WAIT_L(n) asm volatile("s_waitcnt lgkmcnt(" #n ")" ::: "memory")
; #define G_BAR __builtin_amdgcn_s_barrier()
; #define G_SCHED __builtin_amdgcn_sched_barrier(0)
;     __device__ __forceinline__ unsigned row_off(const Unit& u, int r, LAS unsigned char* lds) const { return (unsigned)((const LAS int*)(lds + LDS_STAGE + u.q * 4096))[r] * (unsigned)rowbytes; }
;     ...
;             G_LDB(B0, 0, 0); G_LDB(B1, 0, 1); G_SCHED; G_LDA(At, 0, 0); G_STAGE(G_SA(1, 1), a11, vA1);
;             if constexpr (GATHER) { if (last) { int tz = tid; asm volatile("" : "+v"(tz));
; #pragma unroll
;                 for (int i = 0; i < 2; ++i) { int R, C; stage_rc(tz * 16 + i * 8192, R, C); gc0[i] = S.row_off(nxt, R, lds) + (unsigned)C * 2u; gc1[i] = S.row_off(nxt, 128 + R, lds) + (unsigned)C * 2u; } } }
;             G_WAIT_L(0); G_BAR; G_MMA(0, 0, At, B0); G_MMA(0, 1, At, B1); G_WAIT_V(8); G_BAR; G_SCHED;
;             G_LDA(At, 0, 1); G_STAGE(G_SB(0, 0), b02, voffB); G_STAGE(G_SB(0, 1), b12, voffB); G_STAGE(G_SA(0, 0), a02, vA0);
;             G_WAIT_L(0); G_BAR; G_MMA(1, 0, At, B0); G_MMA(1, 1, At, B1); G_WAIT_V(8); G_BAR; G_SCHED;
;             G_LDB(B0, 1, 0); G_LDB(B1, 1, 1); G_SCHED; G_LDA(At, 1, 0); G_STAGE(G_SA(0, 1), a12, vA1);
;             G_WAIT_L(0); G_BAR; G_MMA(0, 0, At, B0); G_MMA(0, 1, At, B1); G_WAIT_V(8); G_BAR; G_SCHED;
;             G_LDA(At, 1, 1); G_STAGE(G_SB(1, 0), b02 + kstep, voffB); G_STAGE(G_SB(1, 1), b12 + kstep, voffB); G_STAGE(G_SA(1, 0), a02 + kstep, vA0);
;             G_WAIT_L(0); G_BAR; G_MMA(1, 0, At, B0); G_MMA(1, 1, At, B1); G_WAIT_V(8); G_BAR; G_SCHED;
	s_waitcnt lgkmcnt(0)
	v_mfma_f32_16x16x32_bf16 v[60:63], v[72:75], v[88:91], v[60:63]
	v_mfma_f32_16x16x32_bf16 v[56:59], v[80:83], v[88:91], v[56:59]
	v_mfma_f32_16x16x32_bf16 v[52:55], v[72:75], v[96:99], v[52:55]
	v_mfma_f32_16x16x32_bf16 v[48:51], v[80:83], v[96:99], v[48:51]
	v_mfma_f32_16x16x32_bf16 v[44:47], v[72:75], v[104:107], v[44:47]
	v_mfma_f32_16x16x32_bf16 v[40:43], v[80:83], v[104:107], v[40:43]
	v_mfma_f32_16x16x32_bf16 v[36:39], v[72:75], v[112:115], v[36:39]
	v_mfma_f32_16x16x32_bf16 v[32:35], v[80:83], v[112:115], v[32:35]
	v_mfma_f32_16x16x32_bf16 v[60:63], v[76:79], v[92:95], v[60:63]
	v_mfma_f32_16x16x32_bf16 v[56:59], v[84:87], v[92:95], v[56:59]
	v_mfma_f32_16x16x32_bf16 v[52:55], v[76:79], v[100:103], v[52:55]
	v_mfma_f32_16x16x32_bf16 v[48:51], v[84:87], v[100:103], v[48:51]
	v_mfma_f32_16x16x32_bf16 v[44:47], v[76:79], v[108:111], v[44:47]
	v_mfma_f32_16x16x32_bf16 v[40:43], v[84:87], v[108:111], v[40:43]
	v_mfma_f32_16x16x32_bf16 v[36:39], v[76:79], v[116:119], v[36:39]
	v_mfma_f32_16x16x32_bf16 v[32:35], v[84:87], v[116:119], v[32:35]
	s_waitcnt vmcnt(8)
	s_barrier
	s_add_i32 s54, s56, s20
	v_lshl_add_u64 v[122:123], v[126:127], 0, s[36:37]
	s_mov_b32 m0, s54
	ds_read_b128 v[88:91], v71 offset:49152
	ds_read_b128 v[92:95], v71 offset:50176
	ds_read_b128 v[96:99], v71 offset:51200
	ds_read_b128 v[100:103], v71 offset:52224
	ds_read_b128 v[104:107], v71 offset:53248
	ds_read_b128 v[108:111], v71 offset:54272
	ds_read_b128 v[112:115], v71 offset:55296
	ds_read_b128 v[116:119], v71 offset:56320
	global_load_lds_dwordx4 v[122:123], off
	v_lshl_add_u64 v[122:123], v[128:129], 0, s[36:37]
	s_add_i32 m0, s54, 0x2000
	v_lshl_add_u64 v[120:121], v[120:121], 0, s[36:37]
	global_load_lds_dwordx4 v[122:123], off
	s_mov_b32 m0, s69
	s_nop 0
	global_load_lds_dwordx4 v[120:121], off
	v_lshl_add_u64 v[120:121], v[124:125], 0, s[36:37]
	s_mov_b32 m0, s71
	s_nop 0
	global_load_lds_dwordx4 v[120:121], off
	v_lshl_add_u64 v[120:121], v[130:131], 0, s[36:37]
	s_mov_b32 m0, s66
	s_nop 0
	global_load_lds_dwordx4 v[120:121], off
	v_lshl_add_u64 v[120:121], v[132:133], 0, s[36:37]
	s_mov_b32 m0, s67
	s_nop 0
	global_load_lds_dwordx4 v[120:121], off
	s_waitcnt lgkmcnt(0)
	s_waitcnt vmcnt(8)
	s_barrier
	s_waitcnt lgkmcnt(0)
	v_mfma_f32_16x16x32_bf16 v[28:31], v[72:75], v[88:91], v[28:31]
	v_mfma_f32_16x16x32_bf16 v[24:27], v[80:83], v[88:91], v[24:27]
	v_mfma_f32_16x16x32_bf16 v[20:23], v[72:75], v[96:99], v[20:23]
	v_mfma_f32_16x16x32_bf16 v[16:19], v[80:83], v[96:99], v[16:19]
	v_mfma_f32_16x16x32_bf16 v[12:15], v[72:75], v[104:107], v[12:15]
	v_mfma_f32_16x16x32_bf16 v[8:11], v[80:83], v[104:107], v[8:11]
	v_mfma_f32_16x16x32_bf16 v[4:7], v[72:75], v[112:115], v[4:7]
	v_mfma_f32_16x16x32_bf16 v[0:3], v[80:83], v[112:115], v[0:3]
	v_mfma_f32_16x16x32_bf16 v[28:31], v[76:79], v[92:95], v[28:31]
	v_mfma_f32_16x16x32_bf16 v[24:27], v[84:87], v[92:95], v[24:27]
	v_mfma_f32_16x16x32_bf16 v[20:23], v[76:79], v[100:103], v[20:23]
	v_mfma_f32_16x16x32_bf16 v[16:19], v[84:87], v[100:103], v[16:19]
	v_mfma_f32_16x16x32_bf16 v[12:15], v[76:79], v[108:111], v[12:15]
	v_mfma_f32_16x16x32_bf16 v[8:11], v[84:87], v[108:111], v[8:11]
	v_mfma_f32_16x16x32_bf16 v[4:7], v[76:79], v[116:119], v[4:7]
	v_mfma_f32_16x16x32_bf16 v[0:3], v[84:87], v[116:119], v[0:3]
	s_waitcnt vmcnt(8)
	s_barrier
	s_add_u32 s60, s60, 0x100
	s_addc_u32 s61, s61, 0
	s_add_u32 s62, s62, 0x100
	s_addc_u32 s74, s74, 0
	s_add_u32 s75, s75, 0x100
	s_addc_u32 s77, s77, 0
	s_add_u32 s52, s52, 0x100
	s_addc_u32 s53, s53, 0
	s_cmp_ge_i32 s78, s0
	s_mov_b32 s54, s78
	s_cbranch_scc0 .LBB0_1023
	v_pk_mul_f32 v[62:63], v[62:63], s[40:41] op_sel_hi:[1,0]
	v_pk_mul_f32 v[60:61], v[60:61], s[40:41] op_sel_hi:[1,0]
	v_pk_mul_f32 v[58:59], v[58:59], s[40:41] op_sel_hi:[1,0]
	v_pk_mul_f32 v[56:57], v[56:57], s[40:41] op_sel_hi:[1,0]
	v_pk_mul_f32 v[54:55], v[54:55], s[40:41] op_sel_hi:[1,0]
	v_pk_mul_f32 v[52:53], v[52:53], s[40:41] op_sel_hi:[1,0]
	v_pk_mul_f32 v[50:51], v[50:51], s[40:41] op_sel_hi:[1,0]
	v_pk_mul_f32 v[48:49], v[48:49], s[40:41] op_sel_hi:[1,0]
	v_pk_mul_f32 v[46:47], v[46:47], s[40:41] op_sel_hi:[1,0]
	v_pk_mul_f32 v[44:45], v[44:45], s[40:41] op_sel_hi:[1,0]
	v_pk_mul_f32 v[42:43], v[42:43], s[40:41] op_sel_hi:[1,0]
	v_pk_mul_f32 v[40:41], v[40:41], s[40:41] op_sel_hi:[1,0]
	v_pk_mul_f32 v[38:39], v[38:39], s[40:41] op_sel_hi:[1,0]
	v_pk_mul_f32 v[36:37], v[36:37], s[40:41] op_sel_hi:[1,0]
	v_pk_mul_f32 v[34:35], v[34:35], s[40:41] op_sel_hi:[1,0]
	v_pk_mul_f32 v[32:33], v[32:33], s[40:41] op_sel_hi:[1,0]
	v_pk_mul_f32 v[30:31], v[30:31], s[40:41] op_sel_hi:[1,0]
	v_pk_mul_f32 v[28:29], v[28:29], s[40:41] op_sel_hi:[1,0]
	v_pk_mul_f32 v[26:27], v[26:27], s[40:41] op_sel_hi:[1,0]
	v_pk_mul_f32 v[24:25], v[24:25], s[40:41] op_sel_hi:[1,0]
	v_pk_mul_f32 v[22:23], v[22:23], s[40:41] op_sel_hi:[1,0]
	v_pk_mul_f32 v[20:21], v[20:21], s[40:41] op_sel_hi:[1,0]
	v_pk_mul_f32 v[18:19], v[18:19], s[40:41] op_sel_hi:[1,0]
	v_pk_mul_f32 v[16:17], v[16:17], s[40:41] op_sel_hi:[1,0]
	v_pk_mul_f32 v[14:15], v[14:15], s[40:41] op_sel_hi:[1,0]
	v_pk_mul_f32 v[12:13], v[12:13], s[40:41] op_sel_hi:[1,0]
	v_pk_mul_f32 v[10:11], v[10:11], s[40:41] op_sel_hi:[1,0]
	v_pk_mul_f32 v[8:9], v[8:9], s[40:41] op_sel_hi:[1,0]
	v_pk_mul_f32 v[6:7], v[6:7], s[40:41] op_sel_hi:[1,0]
	v_pk_mul_f32 v[4:5], v[4:5], s[40:41] op_sel_hi:[1,0]
	v_pk_mul_f32 v[2:3], v[2:3], s[40:41] op_sel_hi:[1,0]
	v_pk_mul_f32 v[0:1], v[0:1], s[40:41] op_sel_hi:[1,0]
	v_readlane_b32 s78, v255, 11
	v_readlane_b32 s79, v255, 13
	s_and_b64 vcc, exec, s[38:39]
	s_cbranch_vccz .LBB0_1026

; #define G_STAGE(bufoff, gbase, voff) do { _Pragma("unroll") for (int _i = 0; _i < 2; ++_i) \
;         __builtin_amdgcn_global_load_lds((const unsigned*)((const char*)(gbase) + (voff)[_i]), (LAS unsigned*)(lds + (bufoff) + ldsw + _i * 8192), 16, 0, 0); } while (0)
; #define G_LDA(dst, b, h) do { _Pragma("unroll") for (int m = 0; m < 4; ++m) G_LD8(dst[m], lds + G_SA(b, h) + aoff + m * 2048); } while (0)
; #define G_LDB(dst, b, h) do { _Pragma("unroll") for (int n = 0; n < 2; ++n) G_LD8(dst[n], lds + G_SB(b, h) + boff + n * 2048); } while (0)
; #define G_WAIT_V(n) asm volatile("s_waitcnt vmcnt(" #n ")" ::: "memory")
; #define G_WAIT_L(n) asm volatile("s_waitcnt lgkmcnt(" #n ")" ::: "memory")
; #define G_BAR __builtin_amdgcn_s_barrier()
; #define G_SCHED __builtin_amdgcn_sched_barrier(0)
;     ...
;             const char* a11 = cur.a1 + (size_t)(t + 1) * kstep;
;             const char* a02 = last ? nxt.a0 : cur.a0 + (size_t)(t + 2) * kstep; const char* a12 = last ? nxt.a1 : cur.a1 + (size_t)(t + 2) * kstep;
;             const char* b02 = last ? nxt.b0 : cur.b0 + (size_t)(t + 2) * kstep; const char* b12 = last ? nxt.b1 : cur.b1 + (size_t)(t + 2) * kstep;
;             G_LDB(B0, 0, 0); G_LDB(B1, 0, 1); G_SCHED; G_LDA(At, 0, 0); G_STAGE(G_SA(1, 1), a11, vA1);
;             if constexpr (GATHER) { if (last) { int tz = tid; asm volatile("" : "+v"(tz));
; #pragma unroll
;                 for (int i = 0; i < 2; ++i) { int R, C; stage_rc(tz * 16 + i * 8192, R, C); gc0[i] = S.row_off(nxt, R, lds) + (unsigned)C * 2u; gc1[i] = S.row_off(nxt, 128 + R, lds) + (unsigned)C * 2u; } } }
;             G_WAIT_L(0); G_BAR; G_MMA(0, 0, At, B0); G_MMA(0, 1, At, B1); G_WAIT_V(8); G_BAR; G_SCHED;
;             G_LDA(At, 0, 1); G_STAGE(G_SB(0, 0), b02, voffB); G_STAGE(G_SB(0, 1), b12, voffB); G_STAGE(G_SA(0, 0), a02, vA0);
;             G_WAIT_L(0); G_BAR; G_MMA(1, 0, At, B0); G_MMA(1, 1, At, B1); G_WAIT_V(8); G_BAR; G_SCHED;
;             G_LDB(B0, 1, 0); G_LDB(B1, 1, 1); G_SCHED; G_LDA(At, 1, 0); G_STAGE(G_SA(0, 1), a12, vA1);
;             G_WAIT_L(0); G_BAR; G_MMA(0, 0, At, B0); G_MMA(0, 1, At, B1); G_WAIT_V(8); G_BAR; G_SCHED;
;             G_LDA(At, 1, 1); G_STAGE(G_SB(1, 0), b02 + kstep, voffB); G_STAGE(G_SB(1, 1), b12 + kstep, voffB); G_STAGE(G_SA(1, 0), a02 + kstep, vA0);
;             G_WAIT_L(0); G_BAR; G_MMA(1, 0, At, B0); G_MMA(1, 1, At, B1); G_WAIT_V(8); G_BAR; G_SCHED;
.LBB0_1058:
	s_add_i32 s79, s54, 2
	ds_read_b128 v[130:133], v138
	ds_read_b128 v[144:147], v138 offset:1024
	ds_read_b128 v[148:151], v138 offset:2048
	ds_read_b128 v[152:155], v138 offset:3072
	ds_read_b128 v[156:159], v139
	ds_read_b128 v[160:163], v139 offset:1024
	ds_read_b128 v[164:167], v139 offset:2048
	ds_read_b128 v[168:171], v139 offset:3072
	s_add_u32 s80, s52, 0x80
	s_addc_u32 s55, s53, 0
	s_add_i32 s83, s71, s20
	s_add_i32 m0, s33, 0xc000
	s_add_i32 s82, s33, 0xe000
	s_add_i32 s84, s83, 0x2000
	s_cmp_eq_u32 s69, s54
	s_cselect_b32 s54, s44, s80
	s_cselect_b32 s57, s43, s78
	s_cselect_b32 s56, s42, s77
	s_cselect_b32 s59, s47, s41
	s_cselect_b32 s58, s46, s5
	s_cselect_b32 s55, s45, s55
	ds_read_b128 v[172:175], v140
	ds_read_b128 v[176:179], v140 offset:1024
	ds_read_b128 v[180:183], v140 offset:2048
	ds_read_b128 v[184:187], v140 offset:3072
	ds_read_b128 v[188:191], v140 offset:4096
	ds_read_b128 v[192:195], v140 offset:5120
	ds_read_b128 v[196:199], v140 offset:6144
	ds_read_b128 v[200:203], v140 offset:7168
	global_load_lds_dwordx4 v240, s[52:53]
	s_mov_b32 m0, s82
	v_mov_b32_e32 v207, v129
	global_load_lds_dwordx4 v242, s[52:53]
	s_waitcnt lgkmcnt(0)
	s_waitcnt vmcnt(8)
	s_barrier
	s_waitcnt lgkmcnt(0)
	v_mfma_f32_16x16x32_bf16 v[124:127], v[130:133], v[172:175], v[124:127]
	v_mfma_f32_16x16x32_bf16 v[120:123], v[148:151], v[172:175], v[120:123]
	v_mfma_f32_16x16x32_bf16 v[108:111], v[130:133], v[180:183], v[108:111]
	v_mfma_f32_16x16x32_bf16 v[104:107], v[148:151], v[180:183], v[104:107]
	v_mfma_f32_16x16x32_bf16 v[92:95], v[130:133], v[188:191], v[92:95]
	v_mfma_f32_16x16x32_bf16 v[88:91], v[148:151], v[188:191], v[88:91]
	v_mfma_f32_16x16x32_bf16 v[76:79], v[130:133], v[196:199], v[76:79]
	v_mfma_f32_16x16x32_bf16 v[72:75], v[148:151], v[196:199], v[72:75]
	v_mfma_f32_16x16x32_bf16 v[124:127], v[144:147], v[176:179], v[124:127]
	v_mfma_f32_16x16x32_bf16 v[120:123], v[152:155], v[176:179], v[120:123]
	v_mfma_f32_16x16x32_bf16 v[108:111], v[144:147], v[184:187], v[108:111]
	v_mfma_f32_16x16x32_bf16 v[104:107], v[152:155], v[184:187], v[104:107]
	v_mfma_f32_16x16x32_bf16 v[92:95], v[144:147], v[192:195], v[92:95]
	v_mfma_f32_16x16x32_bf16 v[88:91], v[152:155], v[192:195], v[88:91]
	v_mfma_f32_16x16x32_bf16 v[76:79], v[144:147], v[200:203], v[76:79]
	v_mfma_f32_16x16x32_bf16 v[72:75], v[152:155], v[200:203], v[72:75]
	v_mfma_f32_16x16x32_bf16 v[116:119], v[156:159], v[172:175], v[116:119]
	v_mfma_f32_16x16x32_bf16 v[112:115], v[164:167], v[172:175], v[112:115]
	v_mfma_f32_16x16x32_bf16 v[100:103], v[156:159], v[180:183], v[100:103]
	v_mfma_f32_16x16x32_bf16 v[96:99], v[164:167], v[180:183], v[96:99]
	v_mfma_f32_16x16x32_bf16 v[84:87], v[156:159], v[188:191], v[84:87]
	v_mfma_f32_16x16x32_bf16 v[80:83], v[164:167], v[188:191], v[80:83]
	v_mfma_f32_16x16x32_bf16 v[68:71], v[156:159], v[196:199], v[68:71]
	v_mfma_f32_16x16x32_bf16 v[64:67], v[164:167], v[196:199], v[64:67]
	v_mfma_f32_16x16x32_bf16 v[116:119], v[160:163], v[176:179], v[116:119]
	v_mfma_f32_16x16x32_bf16 v[112:115], v[168:171], v[176:179], v[112:115]
	v_mfma_f32_16x16x32_bf16 v[100:103], v[160:163], v[184:187], v[100:103]
	v_mfma_f32_16x16x32_bf16 v[96:99], v[168:171], v[184:187], v[96:99]
	v_mfma_f32_16x16x32_bf16 v[84:87], v[160:163], v[192:195], v[84:87]
	v_mfma_f32_16x16x32_bf16 v[80:83], v[168:171], v[192:195], v[80:83]
	v_mfma_f32_16x16x32_bf16 v[68:71], v[160:163], v[200:203], v[68:71]
	v_mfma_f32_16x16x32_bf16 v[64:67], v[168:171], v[200:203], v[64:67]
	s_waitcnt vmcnt(8)
	s_barrier
	s_mov_b32 m0, s83
	ds_read_b128 v[172:175], v140 offset:16384
	ds_read_b128 v[176:179], v140 offset:17408
	ds_read_b128 v[180:183], v140 offset:18432
	ds_read_b128 v[184:187], v140 offset:19456
	ds_read_b128 v[188:191], v140 offset:20480
	ds_read_b128 v[192:195], v140 offset:21504
	ds_read_b128 v[196:199], v140 offset:22528
	ds_read_b128 v[200:203], v140 offset:23552
	global_load_lds_dwordx4 v244, s[58:59]
	s_mov_b32 m0, s84
	s_cselect_b32 s81, s49, s61
	s_cselect_b32 s80, s48, s60
	s_add_i32 s82, s72, s20
	global_load_lds_dwordx4 v246, s[58:59]
	s_mov_b32 m0, s82
	v_mov_b32_e32 v205, v129
	global_load_lds_dwordx4 v244, s[80:81]
	s_add_i32 m0, s82, 0x2000
	v_mov_b32_e32 v209, v129
	global_load_lds_dwordx4 v246, s[80:81]
	s_mov_b32 m0, s33
	v_lshl_add_u64 v[210:211], s[58:59], 0, v[244:245]
	global_load_lds_dwordx4 v240, s[56:57]
	s_mov_b32 m0, s62
	v_lshl_add_u64 v[212:213], s[58:59], 0, v[246:247]
	global_load_lds_dwordx4 v242, s[56:57]
	s_waitcnt lgkmcnt(0)
	v_lshl_add_u64 v[204:205], s[80:81], 0, v[244:245]
	v_lshl_add_u64 v[208:209], s[80:81], 0, v[246:247]
	v_lshl_add_u64 v[214:215], s[56:57], 0, v[240:241]
	v_lshl_add_u64 v[216:217], s[56:57], 0, v[242:243]
	s_waitcnt vmcnt(8)
	s_barrier
; #define G_STAGE(bufoff, gbase, voff) do { _Pragma("unroll") for (int _i = 0; _i < 2; ++_i) \
;         __builtin_amdgcn_global_load_lds((const unsigned*)((const char*)(gbase) + (voff)[_i]), (LAS unsigned*)(lds + (bufoff) + ldsw + _i * 8192), 16, 0, 0); } while (0)
; #define G_LDA(dst, b, h) do { _Pragma("unroll") for (int m = 0; m < 4; ++m) G_LD8(dst[m], lds + G_SA(b, h) + aoff + m * 2048); } while (0)
; #define G_LDB(dst, b, h) do { _Pragma("unroll") for (int n = 0; n < 2; ++n) G_LD8(dst[n], lds + G_SB(b, h) + boff + n * 2048); } while (0)
; #define G_WAIT_V(n) asm volatile("s_waitcnt vmcnt(" #n ")" ::: "memory")
; #define G_WAIT_L(n) asm volatile("s_waitcnt lgkmcnt(" #n ")" ::: "memory")
; #define G_BAR __builtin_amdgcn_s_barrier()
; #define G_SCHED __builtin_amdgcn_sched_barrier(0)
;     ...
;             G_WAIT_L(0); G_BAR; G_MMA(1, 0, At, B0); G_MMA(1, 1, At, B1); G_WAIT_V(8); G_BAR; G_SCHED;
;             G_LDB(B0, 1, 0); G_LDB(B1, 1, 1); G_SCHED; G_LDA(At, 1, 0); G_STAGE(G_SA(0, 1), a12, vA1);
;             G_WAIT_L(0); G_BAR; G_MMA(0, 0, At, B0); G_MMA(0, 1, At, B1); G_WAIT_V(8); G_BAR; G_SCHED;
	s_waitcnt lgkmcnt(0)
	v_mfma_f32_16x16x32_bf16 v[60:63], v[130:133], v[172:175], v[60:63]
	v_mfma_f32_16x16x32_bf16 v[56:59], v[148:151], v[172:175], v[56:59]
	v_mfma_f32_16x16x32_bf16 v[44:47], v[130:133], v[180:183], v[44:47]
	v_mfma_f32_16x16x32_bf16 v[40:43], v[148:151], v[180:183], v[40:43]
	v_mfma_f32_16x16x32_bf16 v[28:31], v[130:133], v[188:191], v[28:31]
	v_mfma_f32_16x16x32_bf16 v[24:27], v[148:151], v[188:191], v[24:27]
	v_mfma_f32_16x16x32_bf16 v[12:15], v[130:133], v[196:199], v[12:15]
	v_mfma_f32_16x16x32_bf16 v[8:11], v[148:151], v[196:199], v[8:11]
	v_mfma_f32_16x16x32_bf16 v[60:63], v[144:147], v[176:179], v[60:63]
	v_mfma_f32_16x16x32_bf16 v[56:59], v[152:155], v[176:179], v[56:59]
	v_mfma_f32_16x16x32_bf16 v[44:47], v[144:147], v[184:187], v[44:47]
	v_mfma_f32_16x16x32_bf16 v[40:43], v[152:155], v[184:187], v[40:43]
	v_mfma_f32_16x16x32_bf16 v[28:31], v[144:147], v[192:195], v[28:31]
	v_mfma_f32_16x16x32_bf16 v[24:27], v[152:155], v[192:195], v[24:27]
	v_mfma_f32_16x16x32_bf16 v[12:15], v[144:147], v[200:203], v[12:15]
	v_mfma_f32_16x16x32_bf16 v[8:11], v[152:155], v[200:203], v[8:11]
	v_mfma_f32_16x16x32_bf16 v[52:55], v[156:159], v[172:175], v[52:55]
	v_mfma_f32_16x16x32_bf16 v[48:51], v[164:167], v[172:175], v[48:51]
	v_mfma_f32_16x16x32_bf16 v[36:39], v[156:159], v[180:183], v[36:39]
	v_mfma_f32_16x16x32_bf16 v[32:35], v[164:167], v[180:183], v[32:35]
	v_mfma_f32_16x16x32_bf16 v[20:23], v[156:159], v[188:191], v[20:23]
	v_mfma_f32_16x16x32_bf16 v[16:19], v[164:167], v[188:191], v[16:19]
	v_mfma_f32_16x16x32_bf16 v[4:7], v[156:159], v[196:199], v[4:7]
	v_mfma_f32_16x16x32_bf16 v[0:3], v[164:167], v[196:199], v[0:3]
	v_mfma_f32_16x16x32_bf16 v[52:55], v[160:163], v[176:179], v[52:55]
	v_mfma_f32_16x16x32_bf16 v[48:51], v[168:171], v[176:179], v[48:51]
	v_mfma_f32_16x16x32_bf16 v[36:39], v[160:163], v[184:187], v[36:39]
	v_mfma_f32_16x16x32_bf16 v[32:35], v[168:171], v[184:187], v[32:35]
	v_mfma_f32_16x16x32_bf16 v[20:23], v[160:163], v[192:195], v[20:23]
	v_mfma_f32_16x16x32_bf16 v[16:19], v[168:171], v[192:195], v[16:19]
	v_mfma_f32_16x16x32_bf16 v[4:7], v[160:163], v[200:203], v[4:7]
	v_mfma_f32_16x16x32_bf16 v[0:3], v[168:171], v[200:203], v[0:3]
	s_waitcnt vmcnt(8)
	s_barrier
	s_add_i32 s56, 0, 0x18000
	s_add_i32 s57, 0, 0x1c000
	v_add_u32_e32 v152, s56, v137
	v_add_u32_e32 v168, s57, v137
	ds_read_b128 v[130:133], v152
	ds_read_b128 v[144:147], v152 offset:1024
	ds_read_b128 v[148:151], v152 offset:2048
	ds_read_b128 v[152:155], v152 offset:3072
	ds_read_b128 v[156:159], v168
	ds_read_b128 v[160:163], v168 offset:1024
	ds_read_b128 v[164:167], v168 offset:2048
	ds_read_b128 v[168:171], v168 offset:3072
	s_mov_b32 m0, s63
	ds_read_b128 v[172:175], v140 offset:32768
	ds_read_b128 v[176:179], v140 offset:33792
	ds_read_b128 v[180:183], v140 offset:34816
	ds_read_b128 v[184:187], v140 offset:35840
	ds_read_b128 v[188:191], v140 offset:36864
	ds_read_b128 v[192:195], v140 offset:37888
	ds_read_b128 v[196:199], v140 offset:38912
	ds_read_b128 v[200:203], v140 offset:39936
	global_load_lds_dwordx4 v240, s[54:55]
	s_mov_b32 m0, s64
	s_nop 0
	global_load_lds_dwordx4 v242, s[54:55]
	s_waitcnt lgkmcnt(0)
	s_waitcnt vmcnt(8)
	s_barrier
	s_waitcnt lgkmcnt(0)
	v_mfma_f32_16x16x32_bf16 v[124:127], v[130:133], v[172:175], v[124:127]
	v_mfma_f32_16x16x32_bf16 v[120:123], v[148:151], v[172:175], v[120:123]
	v_mfma_f32_16x16x32_bf16 v[108:111], v[130:133], v[180:183], v[108:111]
	v_mfma_f32_16x16x32_bf16 v[104:107], v[148:151], v[180:183], v[104:107]
	v_mfma_f32_16x16x32_bf16 v[92:95], v[130:133], v[188:191], v[92:95]
	v_mfma_f32_16x16x32_bf16 v[88:91], v[148:151], v[188:191], v[88:91]
	v_mfma_f32_16x16x32_bf16 v[76:79], v[130:133], v[196:199], v[76:79]
	v_mfma_f32_16x16x32_bf16 v[72:75], v[148:151], v[196:199], v[72:75]
	v_mfma_f32_16x16x32_bf16 v[124:127], v[144:147], v[176:179], v[124:127]
	v_mfma_f32_16x16x32_bf16 v[120:123], v[152:155], v[176:179], v[120:123]
	v_mfma_f32_16x16x32_bf16 v[108:111], v[144:147], v[184:187], v[108:111]
	v_mfma_f32_16x16x32_bf16 v[104:107], v[152:155], v[184:187], v[104:107]
	v_mfma_f32_16x16x32_bf16 v[92:95], v[144:147], v[192:195], v[92:95]
	v_mfma_f32_16x16x32_bf16 v[88:91], v[152:155], v[192:195], v[88:91]
	v_mfma_f32_16x16x32_bf16 v[76:79], v[144:147], v[200:203], v[76:79]
	v_mfma_f32_16x16x32_bf16 v[72:75], v[152:155], v[200:203], v[72:75]
	v_mfma_f32_16x16x32_bf16 v[116:119], v[156:159], v[172:175], v[116:119]
	v_mfma_f32_16x16x32_bf16 v[112:115], v[164:167], v[172:175], v[112:115]
	v_mfma_f32_16x16x32_bf16 v[100:103], v[156:159], v[180:183], v[100:103]
	v_mfma_f32_16x16x32_bf16 v[96:99], v[164:167], v[180:183], v[96:99]
	v_mfma_f32_16x16x32_bf16 v[84:87], v[156:159], v[188:191], v[84:87]
	v_mfma_f32_16x16x32_bf16 v[80:83], v[164:167], v[188:191], v[80:83]
	v_mfma_f32_16x16x32_bf16 v[68:71], v[156:159], v[196:199], v[68:71]
	v_mfma_f32_16x16x32_bf16 v[64:67], v[164:167], v[196:199], v[64:67]
	v_mfma_f32_16x16x32_bf16 v[116:119], v[160:163], v[176:179], v[116:119]
	v_mfma_f32_16x16x32_bf16 v[112:115], v[168:171], v[176:179], v[112:115]
	v_mfma_f32_16x16x32_bf16 v[100:103], v[160:163], v[184:187], v[100:103]
	v_mfma_f32_16x16x32_bf16 v[96:99], v[168:171], v[184:187], v[96:99]
	v_mfma_f32_16x16x32_bf16 v[84:87], v[160:163], v[192:195], v[84:87]
	v_mfma_f32_16x16x32_bf16 v[80:83], v[168:171], v[192:195], v[80:83]
	v_mfma_f32_16x16x32_bf16 v[68:71], v[160:163], v[200:203], v[68:71]
	v_mfma_f32_16x16x32_bf16 v[64:67], v[168:171], v[200:203], v[64:67]
	s_waitcnt vmcnt(8)
	s_barrier
; #define G_STAGE(bufoff, gbase, voff) do { _Pragma("unroll") for (int _i = 0; _i < 2; ++_i) \
;         __builtin_amdgcn_global_load_lds((const unsigned*)((const char*)(gbase) + (voff)[_i]), (LAS unsigned*)(lds + (bufoff) + ldsw + _i * 8192), 16, 0, 0); } while (0)
; #define G_LDA(dst, b, h) do { _Pragma("unroll") for (int m = 0; m < 4; ++m) G_LD8(dst[m], lds + G_SA(b, h) + aoff + m * 2048); } while (0)
; #define G_WAIT_V(n) asm volatile("s_waitcnt vmcnt(" #n ")" ::: "memory")
; #define G_WAIT_L(n) asm volatile("s_waitcnt lgkmcnt(" #n ")" ::: "memory")
; #define G_BAR __builtin_amdgcn_s_barrier()
; #define G_SCHED __builtin_amdgcn_sched_barrier(0)
;     ...
;             G_LDA(At, 1, 1); G_STAGE(G_SB(1, 0), b02 + kstep, voffB); G_STAGE(G_SB(1, 1), b12 + kstep, voffB); G_STAGE(G_SA(1, 0), a02 + kstep, vA0);
;             G_WAIT_L(0); G_BAR; G_MMA(1, 0, At, B0); G_MMA(1, 1, At, B1); G_WAIT_V(8); G_BAR; G_SCHED;
;         }
	s_add_i32 s54, s56, s20
	v_lshl_add_u64 v[206:207], v[210:211], 0, s[34:35]
	s_mov_b32 m0, s54
	ds_read_b128 v[172:175], v140 offset:49152
	ds_read_b128 v[176:179], v140 offset:50176
	ds_read_b128 v[180:183], v140 offset:51200
	ds_read_b128 v[184:187], v140 offset:52224
	ds_read_b128 v[188:191], v140 offset:53248
	ds_read_b128 v[192:195], v140 offset:54272
	ds_read_b128 v[196:199], v140 offset:55296
	ds_read_b128 v[200:203], v140 offset:56320
	global_load_lds_dwordx4 v[206:207], off
	v_lshl_add_u64 v[206:207], v[212:213], 0, s[34:35]
	s_add_i32 m0, s54, 0x2000
	s_add_i32 s54, s57, s20
	global_load_lds_dwordx4 v[206:207], off
	v_lshl_add_u64 v[204:205], v[204:205], 0, s[34:35]
	s_mov_b32 m0, s54
	s_nop 0
	global_load_lds_dwordx4 v[204:205], off
	v_lshl_add_u64 v[204:205], v[208:209], 0, s[34:35]
	s_add_i32 m0, s54, 0x2000
	s_nop 0
	global_load_lds_dwordx4 v[204:205], off
	v_lshl_add_u64 v[204:205], v[214:215], 0, s[34:35]
	s_mov_b32 m0, s66
	s_nop 0
	global_load_lds_dwordx4 v[204:205], off
	v_lshl_add_u64 v[204:205], v[216:217], 0, s[34:35]
	s_mov_b32 m0, s67
	s_nop 0
	global_load_lds_dwordx4 v[204:205], off
	s_waitcnt lgkmcnt(0)
	s_waitcnt vmcnt(8)
	s_barrier
	s_waitcnt lgkmcnt(0)
	v_mfma_f32_16x16x32_bf16 v[60:63], v[130:133], v[172:175], v[60:63]
	v_mfma_f32_16x16x32_bf16 v[56:59], v[148:151], v[172:175], v[56:59]
	v_mfma_f32_16x16x32_bf16 v[44:47], v[130:133], v[180:183], v[44:47]
	v_mfma_f32_16x16x32_bf16 v[40:43], v[148:151], v[180:183], v[40:43]
	v_mfma_f32_16x16x32_bf16 v[28:31], v[130:133], v[188:191], v[28:31]
	v_mfma_f32_16x16x32_bf16 v[24:27], v[148:151], v[188:191], v[24:27]
	v_mfma_f32_16x16x32_bf16 v[12:15], v[130:133], v[196:199], v[12:15]
	v_mfma_f32_16x16x32_bf16 v[8:11], v[148:151], v[196:199], v[8:11]
	v_mfma_f32_16x16x32_bf16 v[60:63], v[144:147], v[176:179], v[60:63]
	v_mfma_f32_16x16x32_bf16 v[56:59], v[152:155], v[176:179], v[56:59]
	v_mfma_f32_16x16x32_bf16 v[44:47], v[144:147], v[184:187], v[44:47]
	v_mfma_f32_16x16x32_bf16 v[40:43], v[152:155], v[184:187], v[40:43]
	v_mfma_f32_16x16x32_bf16 v[28:31], v[144:147], v[192:195], v[28:31]
	v_mfma_f32_16x16x32_bf16 v[24:27], v[152:155], v[192:195], v[24:27]
	v_mfma_f32_16x16x32_bf16 v[12:15], v[144:147], v[200:203], v[12:15]
	v_mfma_f32_16x16x32_bf16 v[8:11], v[152:155], v[200:203], v[8:11]
	v_mfma_f32_16x16x32_bf16 v[52:55], v[156:159], v[172:175], v[52:55]
	v_mfma_f32_16x16x32_bf16 v[48:51], v[164:167], v[172:175], v[48:51]
	v_mfma_f32_16x16x32_bf16 v[36:39], v[156:159], v[180:183], v[36:39]
	v_mfma_f32_16x16x32_bf16 v[32:35], v[164:167], v[180:183], v[32:35]
	v_mfma_f32_16x16x32_bf16 v[20:23], v[156:159], v[188:191], v[20:23]
	v_mfma_f32_16x16x32_bf16 v[16:19], v[164:167], v[188:191], v[16:19]
	v_mfma_f32_16x16x32_bf16 v[4:7], v[156:159], v[196:199], v[4:7]
	v_mfma_f32_16x16x32_bf16 v[0:3], v[164:167], v[196:199], v[0:3]
	v_mfma_f32_16x16x32_bf16 v[52:55], v[160:163], v[176:179], v[52:55]
	v_mfma_f32_16x16x32_bf16 v[48:51], v[168:171], v[176:179], v[48:51]
	v_mfma_f32_16x16x32_bf16 v[36:39], v[160:163], v[184:187], v[36:39]
	v_mfma_f32_16x16x32_bf16 v[32:35], v[168:171], v[184:187], v[32:35]
	v_mfma_f32_16x16x32_bf16 v[20:23], v[160:163], v[192:195], v[20:23]
	v_mfma_f32_16x16x32_bf16 v[16:19], v[168:171], v[192:195], v[16:19]
	v_mfma_f32_16x16x32_bf16 v[4:7], v[160:163], v[200:203], v[4:7]
	v_mfma_f32_16x16x32_bf16 v[0:3], v[168:171], v[200:203], v[0:3]
	s_waitcnt vmcnt(8)
	s_barrier
	s_add_u32 s5, s5, 0x100
	s_addc_u32 s41, s41, 0
	s_add_u32 s60, s60, 0x100
	s_addc_u32 s61, s61, 0
	s_add_u32 s77, s77, 0x100
	s_addc_u32 s78, s78, 0
	s_add_u32 s52, s52, 0x100
	s_addc_u32 s53, s53, 0
	s_cmp_ge_i32 s79, s24
	s_mov_b32 s54, s79
	s_cbranch_scc0 .LBB0_1058
	v_readlane_b32 s78, v255, 11
	v_readlane_b32 s79, v255, 13
	s_and_b64 vcc, exec, s[38:39]
	s_cbranch_vccz .LBB0_1061

; #define G_STAGE(bufoff, gbase, voff) do { _Pragma("unroll") for (int _i = 0; _i < 2; ++_i) \
;         __builtin_amdgcn_global_load_lds((const unsigned*)((const char*)(gbase) + (voff)[_i]), (LAS unsigned*)(lds + (bufoff) + ldsw + _i * 8192), 16, 0, 0); } while (0)
; #define G_LDA(dst, b, h) do { _Pragma("unroll") for (int m = 0; m < 4; ++m) G_LD8(dst[m], lds + G_SA(b, h) + aoff + m * 2048); } while (0)
; #define G_LDB(dst, b, h) do { _Pragma("unroll") for (int n = 0; n < 2; ++n) G_LD8(dst[n], lds + G_SB(b, h) + boff + n * 2048); } while (0)
; #define G_WAIT_V(n) asm volatile("s_waitcnt vmcnt(" #n ")" ::: "memory")
; #define G_WAIT_L(n) asm volatile("s_waitcnt lgkmcnt(" #n ")" ::: "memory")
; #define G_BAR __builtin_amdgcn_s_barrier()
; #define G_SCHED __builtin_amdgcn_sched_barrier(0)
;     __device__ __forceinline__ unsigned row_off(const Unit& u, int r, LAS unsigned char* lds) const { return (unsigned)((const LAS int*)(lds + LDS_STAGE + u.q * 4096))[r] * (unsigned)rowbytes; }
;     ...
;             const char* a11 = cur.a1 + (size_t)(t + 1) * kstep;
;             const char* a02 = last ? nxt.a0 : cur.a0 + (size_t)(t + 2) * kstep; const char* a12 = last ? nxt.a1 : cur.a1 + (size_t)(t + 2) * kstep;
;             const char* b02 = last ? nxt.b0 : cur.b0 + (size_t)(t + 2) * kstep; const char* b12 = last ? nxt.b1 : cur.b1 + (size_t)(t + 2) * kstep;
;             G_LDB(B0, 0, 0); G_LDB(B1, 0, 1); G_SCHED; G_LDA(At, 0, 0); G_STAGE(G_SA(1, 1), a11, vA1);
;             if constexpr (GATHER) { if (last) { int tz = tid; asm volatile("" : "+v"(tz));
; #pragma unroll
;                 for (int i = 0; i < 2; ++i) { int R, C; stage_rc(tz * 16 + i * 8192, R, C); gc0[i] = S.row_off(nxt, R, lds) + (unsigned)C * 2u; gc1[i] = S.row_off(nxt, 128 + R, lds) + (unsigned)C * 2u; } } }
;             G_WAIT_L(0); G_BAR; G_MMA(0, 0, At, B0); G_MMA(0, 1, At, B1); G_WAIT_V(8); G_BAR; G_SCHED;
;             G_LDA(At, 0, 1); G_STAGE(G_SB(0, 0), b02, voffB); G_STAGE(G_SB(0, 1), b12, voffB); G_STAGE(G_SA(0, 0), a02, vA0);
.LBB0_1322:
	s_add_i32 vcc_lo, s66, 2
	s_add_u32 vcc_hi, s64, 0x80
	s_addc_u32 s67, s65, 0
	s_add_i32 s68, 0, 0x10000
	s_add_i32 s1, 0, 0x14000
	v_add_u32_e32 v146, s68, v172
	v_add_u32_e32 v162, s1, v172
	ds_read_b128 v[130:133], v146
	ds_read_b128 v[134:137], v146 offset:1024
	ds_read_b128 v[138:141], v146 offset:2048
	ds_read_b128 v[146:149], v146 offset:3072
	ds_read_b128 v[150:153], v162
	ds_read_b128 v[154:157], v162 offset:1024
	ds_read_b128 v[158:161], v162 offset:2048
	ds_read_b128 v[162:165], v162 offset:3072
	s_add_i32 s11, s68, s77
	s_add_i32 m0, s10, 0xc000
	s_add_i32 s33, s10, 0xe000
	s_add_i32 s21, s11, 0x2000
	s_cmp_eq_u32 s89, s66
	s_cselect_b32 s66, s54, vcc_hi
	s_cselect_b32 s69, s53, s97
	s_cselect_b32 s68, s52, s96
	s_cselect_b32 s71, s57, s93
	s_cselect_b32 s70, s56, s9
	s_cselect_b32 s67, s55, s67
	ds_read_b128 v[174:177], v173
	ds_read_b128 v[178:181], v173 offset:1024
	ds_read_b128 v[182:185], v173 offset:2048
	ds_read_b128 v[186:189], v173 offset:3072
	ds_read_b128 v[190:193], v173 offset:4096
	ds_read_b128 v[194:197], v173 offset:5120
	ds_read_b128 v[198:201], v173 offset:6144
	ds_read_b128 v[202:205], v173 offset:7168
	global_load_lds_dwordx4 v240, s[64:65]
	s_mov_b32 m0, s33
	s_nop 0
	global_load_lds_dwordx4 v242, s[64:65]
	s_waitcnt lgkmcnt(0)
	v_mov_b32_e32 v129, v145
	s_waitcnt vmcnt(8)
	s_barrier
	s_waitcnt lgkmcnt(0)
	v_mfma_f32_16x16x32_bf16 v[124:127], v[130:133], v[174:177], v[124:127]
	v_mfma_f32_16x16x32_bf16 v[120:123], v[138:141], v[174:177], v[120:123]
	v_mfma_f32_16x16x32_bf16 v[116:119], v[130:133], v[182:185], v[116:119]
	v_mfma_f32_16x16x32_bf16 v[112:115], v[138:141], v[182:185], v[112:115]
	v_mfma_f32_16x16x32_bf16 v[108:111], v[130:133], v[190:193], v[108:111]
	v_mfma_f32_16x16x32_bf16 v[104:107], v[138:141], v[190:193], v[104:107]
	v_mfma_f32_16x16x32_bf16 v[100:103], v[130:133], v[198:201], v[100:103]
	v_mfma_f32_16x16x32_bf16 v[96:99], v[138:141], v[198:201], v[96:99]
	v_mfma_f32_16x16x32_bf16 v[124:127], v[134:137], v[178:181], v[124:127]
	v_mfma_f32_16x16x32_bf16 v[120:123], v[146:149], v[178:181], v[120:123]
	v_mfma_f32_16x16x32_bf16 v[116:119], v[134:137], v[186:189], v[116:119]
	v_mfma_f32_16x16x32_bf16 v[112:115], v[146:149], v[186:189], v[112:115]
	v_mfma_f32_16x16x32_bf16 v[108:111], v[134:137], v[194:197], v[108:111]
	v_mfma_f32_16x16x32_bf16 v[104:107], v[146:149], v[194:197], v[104:107]
	v_mfma_f32_16x16x32_bf16 v[100:103], v[134:137], v[202:205], v[100:103]
	v_mfma_f32_16x16x32_bf16 v[96:99], v[146:149], v[202:205], v[96:99]
	v_mfma_f32_16x16x32_bf16 v[68:71], v[150:153], v[174:177], v[68:71]
	v_mfma_f32_16x16x32_bf16 v[60:63], v[158:161], v[174:177], v[60:63]
	v_mfma_f32_16x16x32_bf16 v[52:55], v[150:153], v[182:185], v[52:55]
	v_mfma_f32_16x16x32_bf16 v[48:51], v[158:161], v[182:185], v[48:51]
	v_mfma_f32_16x16x32_bf16 v[44:47], v[150:153], v[190:193], v[44:47]
	v_mfma_f32_16x16x32_bf16 v[40:43], v[158:161], v[190:193], v[40:43]
	v_mfma_f32_16x16x32_bf16 v[36:39], v[150:153], v[198:201], v[36:39]
	v_mfma_f32_16x16x32_bf16 v[32:35], v[158:161], v[198:201], v[32:35]
	v_mfma_f32_16x16x32_bf16 v[68:71], v[154:157], v[178:181], v[68:71]
	v_mfma_f32_16x16x32_bf16 v[60:63], v[162:165], v[178:181], v[60:63]
	v_mfma_f32_16x16x32_bf16 v[52:55], v[154:157], v[186:189], v[52:55]
	v_mfma_f32_16x16x32_bf16 v[48:51], v[162:165], v[186:189], v[48:51]
	v_mfma_f32_16x16x32_bf16 v[44:47], v[154:157], v[194:197], v[44:47]
	v_mfma_f32_16x16x32_bf16 v[40:43], v[162:165], v[194:197], v[40:43]
	v_mfma_f32_16x16x32_bf16 v[36:39], v[154:157], v[202:205], v[36:39]
	v_mfma_f32_16x16x32_bf16 v[32:35], v[162:165], v[202:205], v[32:35]
	s_waitcnt vmcnt(8)
	s_barrier
	s_mov_b32 m0, s11
	ds_read_b128 v[174:177], v173 offset:16384
	ds_read_b128 v[178:181], v173 offset:17408
	ds_read_b128 v[182:185], v173 offset:18432
	ds_read_b128 v[186:189], v173 offset:19456
	ds_read_b128 v[190:193], v173 offset:20480
	ds_read_b128 v[194:197], v173 offset:21504
	ds_read_b128 v[198:201], v173 offset:22528
	ds_read_b128 v[202:205], v173 offset:23552
	v_mov_b32_e32 v143, v145
	global_load_lds_dwordx4 v244, s[70:71]
	v_mov_b32_e32 v207, v145
	s_mov_b32 m0, s21
	v_lshl_add_u64 v[208:209], s[70:71], 0, v[244:245]
	v_lshl_add_u64 v[210:211], s[70:71], 0, v[246:247]
	global_load_lds_dwordx4 v246, s[70:71]
	s_cselect_b32 s71, s59, s95
	s_cselect_b32 s70, s58, s94
	s_add_i32 s1, s1, s77
	s_mov_b32 m0, s1
	v_lshl_add_u64 v[212:213], s[70:71], 0, v[244:245]
	global_load_lds_dwordx4 v244, s[70:71]
	s_add_i32 m0, s1, 0x2000
	v_lshl_add_u64 v[142:143], s[70:71], 0, v[246:247]
	global_load_lds_dwordx4 v246, s[70:71]
	s_mov_b32 m0, s10
	v_lshl_add_u64 v[206:207], s[68:69], 0, v[240:241]
	global_load_lds_dwordx4 v240, s[68:69]
	s_mov_b32 m0, s63
	v_lshl_add_u64 v[214:215], s[68:69], 0, v[242:243]
	global_load_lds_dwordx4 v242, s[68:69]
	s_waitcnt lgkmcnt(0)
	s_waitcnt vmcnt(8)
	s_barrier
; #define G_STAGE(bufoff, gbase, voff) do { _Pragma("unroll") for (int _i = 0; _i < 2; ++_i) \
;         __builtin_amdgcn_global_load_lds((const unsigned*)((const char*)(gbase) + (voff)[_i]), (LAS unsigned*)(lds + (bufoff) + ldsw + _i * 8192), 16, 0, 0); } while (0)
; #define G_LDA(dst, b, h) do { _Pragma("unroll") for (int m = 0; m < 4; ++m) G_LD8(dst[m], lds + G_SA(b, h) + aoff + m * 2048); } while (0)
; #define G_LDB(dst, b, h) do { _Pragma("unroll") for (int n = 0; n < 2; ++n) G_LD8(dst[n], lds + G_SB(b, h) + boff + n * 2048); } while (0)
; #define G_WAIT_V(n) asm volatile("s_waitcnt vmcnt(" #n ")" ::: "memory")
; #define G_WAIT_L(n) asm volatile("s_waitcnt lgkmcnt(" #n ")" ::: "memory")
; #define G_BAR __builtin_amdgcn_s_barrier()
; #define G_SCHED __builtin_amdgcn_sched_barrier(0)
;     ...
;             G_WAIT_L(0); G_BAR; G_MMA(1, 0, At, B0); G_MMA(1, 1, At, B1); G_WAIT_V(8); G_BAR; G_SCHED;
;             G_LDB(B0, 1, 0); G_LDB(B1, 1, 1); G_SCHED; G_LDA(At, 1, 0); G_STAGE(G_SA(0, 1), a12, vA1);
;             G_WAIT_L(0); G_BAR; G_MMA(0, 0, At, B0); G_MMA(0, 1, At, B1); G_WAIT_V(8); G_BAR; G_SCHED;
	s_waitcnt lgkmcnt(0)
	v_mfma_f32_16x16x32_bf16 v[92:95], v[130:133], v[174:177], v[92:95]
	v_mfma_f32_16x16x32_bf16 v[88:91], v[138:141], v[174:177], v[88:91]
	v_mfma_f32_16x16x32_bf16 v[84:87], v[130:133], v[182:185], v[84:87]
	v_mfma_f32_16x16x32_bf16 v[80:83], v[138:141], v[182:185], v[80:83]
	v_mfma_f32_16x16x32_bf16 v[76:79], v[130:133], v[190:193], v[76:79]
	v_mfma_f32_16x16x32_bf16 v[72:75], v[138:141], v[190:193], v[72:75]
	v_mfma_f32_16x16x32_bf16 v[64:67], v[130:133], v[198:201], v[64:67]
	v_mfma_f32_16x16x32_bf16 v[56:59], v[138:141], v[198:201], v[56:59]
	v_mfma_f32_16x16x32_bf16 v[92:95], v[134:137], v[178:181], v[92:95]
	v_mfma_f32_16x16x32_bf16 v[88:91], v[146:149], v[178:181], v[88:91]
	v_mfma_f32_16x16x32_bf16 v[84:87], v[134:137], v[186:189], v[84:87]
	v_mfma_f32_16x16x32_bf16 v[80:83], v[146:149], v[186:189], v[80:83]
	v_mfma_f32_16x16x32_bf16 v[76:79], v[134:137], v[194:197], v[76:79]
	v_mfma_f32_16x16x32_bf16 v[72:75], v[146:149], v[194:197], v[72:75]
	v_mfma_f32_16x16x32_bf16 v[64:67], v[134:137], v[202:205], v[64:67]
	v_mfma_f32_16x16x32_bf16 v[56:59], v[146:149], v[202:205], v[56:59]
	v_mfma_f32_16x16x32_bf16 v[28:31], v[150:153], v[174:177], v[28:31]
	v_mfma_f32_16x16x32_bf16 v[24:27], v[158:161], v[174:177], v[24:27]
	v_mfma_f32_16x16x32_bf16 v[20:23], v[150:153], v[182:185], v[20:23]
	v_mfma_f32_16x16x32_bf16 v[16:19], v[158:161], v[182:185], v[16:19]
	v_mfma_f32_16x16x32_bf16 v[12:15], v[150:153], v[190:193], v[12:15]
	v_mfma_f32_16x16x32_bf16 v[8:11], v[158:161], v[190:193], v[8:11]
	v_mfma_f32_16x16x32_bf16 v[4:7], v[150:153], v[198:201], v[4:7]
	v_mfma_f32_16x16x32_bf16 v[0:3], v[158:161], v[198:201], v[0:3]
	v_mfma_f32_16x16x32_bf16 v[28:31], v[154:157], v[178:181], v[28:31]
	v_mfma_f32_16x16x32_bf16 v[24:27], v[162:165], v[178:181], v[24:27]
	v_mfma_f32_16x16x32_bf16 v[20:23], v[154:157], v[186:189], v[20:23]
	v_mfma_f32_16x16x32_bf16 v[16:19], v[162:165], v[186:189], v[16:19]
	v_mfma_f32_16x16x32_bf16 v[12:15], v[154:157], v[194:197], v[12:15]
	v_mfma_f32_16x16x32_bf16 v[8:11], v[162:165], v[194:197], v[8:11]
	v_mfma_f32_16x16x32_bf16 v[4:7], v[154:157], v[202:205], v[4:7]
	v_mfma_f32_16x16x32_bf16 v[0:3], v[162:165], v[202:205], v[0:3]
	s_waitcnt vmcnt(8)
	s_barrier
	s_add_i32 s1, 0, 0x18000
	v_add_u32_e32 v129, s1, v172
	s_add_i32 s11, 0, 0x1c000
	ds_read_b128 v[130:133], v129
	ds_read_b128 v[134:137], v129 offset:1024
	ds_read_b128 v[138:141], v129 offset:2048
	ds_read_b128 v[146:149], v129 offset:3072
	v_add_u32_e32 v129, s11, v172
	ds_read_b128 v[150:153], v129
	ds_read_b128 v[154:157], v129 offset:1024
	ds_read_b128 v[158:161], v129 offset:2048
	ds_read_b128 v[162:165], v129 offset:3072
	s_mov_b32 m0, s72
	ds_read_b128 v[174:177], v173 offset:32768
	ds_read_b128 v[178:181], v173 offset:33792
	ds_read_b128 v[182:185], v173 offset:34816
	ds_read_b128 v[186:189], v173 offset:35840
	ds_read_b128 v[190:193], v173 offset:36864
	ds_read_b128 v[194:197], v173 offset:37888
	ds_read_b128 v[198:201], v173 offset:38912
	ds_read_b128 v[202:205], v173 offset:39936
	global_load_lds_dwordx4 v240, s[66:67]
	s_mov_b32 m0, s73
	s_nop 0
	global_load_lds_dwordx4 v242, s[66:67]
	s_waitcnt lgkmcnt(0)
	s_waitcnt vmcnt(8)
	s_barrier
	s_waitcnt lgkmcnt(0)
	v_mfma_f32_16x16x32_bf16 v[124:127], v[130:133], v[174:177], v[124:127]
	v_mfma_f32_16x16x32_bf16 v[120:123], v[138:141], v[174:177], v[120:123]
	v_mfma_f32_16x16x32_bf16 v[116:119], v[130:133], v[182:185], v[116:119]
	v_mfma_f32_16x16x32_bf16 v[112:115], v[138:141], v[182:185], v[112:115]
	v_mfma_f32_16x16x32_bf16 v[108:111], v[130:133], v[190:193], v[108:111]
	v_mfma_f32_16x16x32_bf16 v[104:107], v[138:141], v[190:193], v[104:107]
	v_mfma_f32_16x16x32_bf16 v[100:103], v[130:133], v[198:201], v[100:103]
	v_mfma_f32_16x16x32_bf16 v[96:99], v[138:141], v[198:201], v[96:99]
	v_mfma_f32_16x16x32_bf16 v[124:127], v[134:137], v[178:181], v[124:127]
	v_mfma_f32_16x16x32_bf16 v[120:123], v[146:149], v[178:181], v[120:123]
	v_mfma_f32_16x16x32_bf16 v[116:119], v[134:137], v[186:189], v[116:119]
	v_mfma_f32_16x16x32_bf16 v[112:115], v[146:149], v[186:189], v[112:115]
	v_mfma_f32_16x16x32_bf16 v[108:111], v[134:137], v[194:197], v[108:111]
	v_mfma_f32_16x16x32_bf16 v[104:107], v[146:149], v[194:197], v[104:107]
	v_mfma_f32_16x16x32_bf16 v[100:103], v[134:137], v[202:205], v[100:103]
	v_mfma_f32_16x16x32_bf16 v[96:99], v[146:149], v[202:205], v[96:99]
	v_mfma_f32_16x16x32_bf16 v[68:71], v[150:153], v[174:177], v[68:71]
	v_mfma_f32_16x16x32_bf16 v[60:63], v[158:161], v[174:177], v[60:63]
	v_mfma_f32_16x16x32_bf16 v[52:55], v[150:153], v[182:185], v[52:55]
	v_mfma_f32_16x16x32_bf16 v[48:51], v[158:161], v[182:185], v[48:51]
	v_mfma_f32_16x16x32_bf16 v[44:47], v[150:153], v[190:193], v[44:47]
	v_mfma_f32_16x16x32_bf16 v[40:43], v[158:161], v[190:193], v[40:43]
	v_mfma_f32_16x16x32_bf16 v[36:39], v[150:153], v[198:201], v[36:39]
	v_mfma_f32_16x16x32_bf16 v[32:35], v[158:161], v[198:201], v[32:35]
	v_mfma_f32_16x16x32_bf16 v[68:71], v[154:157], v[178:181], v[68:71]
	v_mfma_f32_16x16x32_bf16 v[60:63], v[162:165], v[178:181], v[60:63]
	v_mfma_f32_16x16x32_bf16 v[52:55], v[154:157], v[186:189], v[52:55]
	v_mfma_f32_16x16x32_bf16 v[48:51], v[162:165], v[186:189], v[48:51]
	v_mfma_f32_16x16x32_bf16 v[44:47], v[154:157], v[194:197], v[44:47]
	v_mfma_f32_16x16x32_bf16 v[40:43], v[162:165], v[194:197], v[40:43]
	v_mfma_f32_16x16x32_bf16 v[36:39], v[154:157], v[202:205], v[36:39]
	v_mfma_f32_16x16x32_bf16 v[32:35], v[162:165], v[202:205], v[32:35]
	s_waitcnt vmcnt(8)
	s_barrier
; #define G_STAGE(bufoff, gbase, voff) do { _Pragma("unroll") for (int _i = 0; _i < 2; ++_i) \
;         __builtin_amdgcn_global_load_lds((const unsigned*)((const char*)(gbase) + (voff)[_i]), (LAS unsigned*)(lds + (bufoff) + ldsw + _i * 8192), 16, 0, 0); } while (0)
; #define G_LDA(dst, b, h) do { _Pragma("unroll") for (int m = 0; m < 4; ++m) G_LD8(dst[m], lds + G_SA(b, h) + aoff + m * 2048); } while (0)
; #define G_WAIT_V(n) asm volatile("s_waitcnt vmcnt(" #n ")" ::: "memory")
; #define G_WAIT_L(n) asm volatile("s_waitcnt lgkmcnt(" #n ")" ::: "memory")
; #define G_BAR __builtin_amdgcn_s_barrier()
; #define G_SCHED __builtin_amdgcn_sched_barrier(0)
;     ...
;             G_LDA(At, 1, 1); G_STAGE(G_SB(1, 0), b02 + kstep, voffB); G_STAGE(G_SB(1, 1), b12 + kstep, voffB); G_STAGE(G_SA(1, 0), a02 + kstep, vA0);
;             G_WAIT_L(0); G_BAR; G_MMA(1, 0, At, B0); G_MMA(1, 1, At, B1); G_WAIT_V(8); G_BAR; G_SCHED;
;         }
	s_add_i32 s1, s1, s77
	v_lshl_add_u64 v[128:129], v[208:209], 0, s[48:49]
	s_mov_b32 m0, s1
	ds_read_b128 v[174:177], v173 offset:49152
	ds_read_b128 v[178:181], v173 offset:50176
	ds_read_b128 v[182:185], v173 offset:51200
	ds_read_b128 v[186:189], v173 offset:52224
	ds_read_b128 v[190:193], v173 offset:53248
	ds_read_b128 v[194:197], v173 offset:54272
	ds_read_b128 v[198:201], v173 offset:55296
	ds_read_b128 v[202:205], v173 offset:56320
	global_load_lds_dwordx4 v[128:129], off
	v_lshl_add_u64 v[128:129], v[210:211], 0, s[48:49]
	s_add_i32 m0, s1, 0x2000
	s_add_i32 s1, s11, s77
	global_load_lds_dwordx4 v[128:129], off
	v_lshl_add_u64 v[128:129], v[212:213], 0, s[48:49]
	s_mov_b32 m0, s1
	s_nop 0
	global_load_lds_dwordx4 v[128:129], off
	v_lshl_add_u64 v[128:129], v[142:143], 0, s[48:49]
	s_add_i32 m0, s1, 0x2000
	s_nop 0
	global_load_lds_dwordx4 v[128:129], off
	v_lshl_add_u64 v[128:129], v[206:207], 0, s[48:49]
	s_mov_b32 m0, s75
	s_nop 0
	global_load_lds_dwordx4 v[128:129], off
	v_lshl_add_u64 v[128:129], v[214:215], 0, s[48:49]
	s_mov_b32 m0, s76
	s_nop 0
	global_load_lds_dwordx4 v[128:129], off
	s_waitcnt lgkmcnt(0)
	s_waitcnt vmcnt(8)
	s_barrier
	s_waitcnt lgkmcnt(0)
	v_mfma_f32_16x16x32_bf16 v[92:95], v[130:133], v[174:177], v[92:95]
	v_mfma_f32_16x16x32_bf16 v[88:91], v[138:141], v[174:177], v[88:91]
	v_mfma_f32_16x16x32_bf16 v[84:87], v[130:133], v[182:185], v[84:87]
	v_mfma_f32_16x16x32_bf16 v[80:83], v[138:141], v[182:185], v[80:83]
	v_mfma_f32_16x16x32_bf16 v[76:79], v[130:133], v[190:193], v[76:79]
	v_mfma_f32_16x16x32_bf16 v[72:75], v[138:141], v[190:193], v[72:75]
	v_mfma_f32_16x16x32_bf16 v[64:67], v[130:133], v[198:201], v[64:67]
	v_mfma_f32_16x16x32_bf16 v[56:59], v[138:141], v[198:201], v[56:59]
	v_mfma_f32_16x16x32_bf16 v[92:95], v[134:137], v[178:181], v[92:95]
	v_mfma_f32_16x16x32_bf16 v[88:91], v[146:149], v[178:181], v[88:91]
	v_mfma_f32_16x16x32_bf16 v[84:87], v[134:137], v[186:189], v[84:87]
	v_mfma_f32_16x16x32_bf16 v[80:83], v[146:149], v[186:189], v[80:83]
	v_mfma_f32_16x16x32_bf16 v[76:79], v[134:137], v[194:197], v[76:79]
	v_mfma_f32_16x16x32_bf16 v[72:75], v[146:149], v[194:197], v[72:75]
	v_mfma_f32_16x16x32_bf16 v[64:67], v[134:137], v[202:205], v[64:67]
	v_mfma_f32_16x16x32_bf16 v[56:59], v[146:149], v[202:205], v[56:59]
	v_mfma_f32_16x16x32_bf16 v[28:31], v[150:153], v[174:177], v[28:31]
	v_mfma_f32_16x16x32_bf16 v[24:27], v[158:161], v[174:177], v[24:27]
	v_mfma_f32_16x16x32_bf16 v[20:23], v[150:153], v[182:185], v[20:23]
	v_mfma_f32_16x16x32_bf16 v[16:19], v[158:161], v[182:185], v[16:19]
	v_mfma_f32_16x16x32_bf16 v[12:15], v[150:153], v[190:193], v[12:15]
	v_mfma_f32_16x16x32_bf16 v[8:11], v[158:161], v[190:193], v[8:11]
	v_mfma_f32_16x16x32_bf16 v[4:7], v[150:153], v[198:201], v[4:7]
	v_mfma_f32_16x16x32_bf16 v[0:3], v[158:161], v[198:201], v[0:3]
	v_mfma_f32_16x16x32_bf16 v[28:31], v[154:157], v[178:181], v[28:31]
	v_mfma_f32_16x16x32_bf16 v[24:27], v[162:165], v[178:181], v[24:27]
	v_mfma_f32_16x16x32_bf16 v[20:23], v[154:157], v[186:189], v[20:23]
	v_mfma_f32_16x16x32_bf16 v[16:19], v[162:165], v[186:189], v[16:19]
	v_mfma_f32_16x16x32_bf16 v[12:15], v[154:157], v[194:197], v[12:15]
	v_mfma_f32_16x16x32_bf16 v[8:11], v[162:165], v[194:197], v[8:11]
	v_mfma_f32_16x16x32_bf16 v[4:7], v[154:157], v[202:205], v[4:7]
	v_mfma_f32_16x16x32_bf16 v[0:3], v[162:165], v[202:205], v[0:3]
	s_waitcnt vmcnt(8)
	s_barrier
	s_add_u32 s9, s9, 0x100
	s_addc_u32 s93, s93, 0
	s_add_u32 s94, s94, 0x100
	s_addc_u32 s95, s95, 0
	s_add_u32 s96, s96, 0x100
	s_addc_u32 s97, s97, 0
	s_add_u32 s64, s64, 0x100
	s_addc_u32 s65, s65, 0
	s_cmp_ge_i32 vcc_lo, s2
	s_mov_b32 s66, vcc_lo
	s_cbranch_scc0 .LBB0_1322
	v_readlane_b32 s64, v255, 9
	v_readlane_b32 s65, v255, 10
	s_load_dword s97, s[64:65], 0xa8
	s_and_b64 vcc, exec, s[46:47]
	s_cbranch_vccz .LBB0_1325

; #define G_STAGE(bufoff, gbase, voff) do { _Pragma("unroll") for (int _i = 0; _i < 2; ++_i) \
;         __builtin_amdgcn_global_load_lds((const unsigned*)((const char*)(gbase) + (voff)[_i]), (LAS unsigned*)(lds + (bufoff) + ldsw + _i * 8192), 16, 0, 0); } while (0)
; #define G_LDA(dst, b, h) do { _Pragma("unroll") for (int m = 0; m < 4; ++m) G_LD8(dst[m], lds + G_SA(b, h) + aoff + m * 2048); } while (0)
; #define G_LDB(dst, b, h) do { _Pragma("unroll") for (int n = 0; n < 2; ++n) G_LD8(dst[n], lds + G_SB(b, h) + boff + n * 2048); } while (0)
; #define G_WAIT_V(n) asm volatile("s_waitcnt vmcnt(" #n ")" ::: "memory")
; #define G_WAIT_L(n) asm volatile("s_waitcnt lgkmcnt(" #n ")" ::: "memory")
; #define G_BAR __builtin_amdgcn_s_barrier()
; #define G_SCHED __builtin_amdgcn_sched_barrier(0)
;     __device__ __forceinline__ unsigned row_off(const Unit& u, int r, LAS unsigned char* lds) const { return (unsigned)((const LAS int*)(lds + LDS_STAGE + u.q * 4096))[r] * (unsigned)rowbytes; }
;     ...
;             const char* a11 = cur.a1 + (size_t)(t + 1) * kstep;
;             const char* a02 = last ? nxt.a0 : cur.a0 + (size_t)(t + 2) * kstep; const char* a12 = last ? nxt.a1 : cur.a1 + (size_t)(t + 2) * kstep;
;             const char* b02 = last ? nxt.b0 : cur.b0 + (size_t)(t + 2) * kstep; const char* b12 = last ? nxt.b1 : cur.b1 + (size_t)(t + 2) * kstep;
;             G_LDB(B0, 0, 0); G_LDB(B1, 0, 1); G_SCHED; G_LDA(At, 0, 0); G_STAGE(G_SA(1, 1), a11, vA1);
;             if constexpr (GATHER) { if (last) { int tz = tid; asm volatile("" : "+v"(tz));
; #pragma unroll
;                 for (int i = 0; i < 2; ++i) { int R, C; stage_rc(tz * 16 + i * 8192, R, C); gc0[i] = S.row_off(nxt, R, lds) + (unsigned)C * 2u; gc1[i] = S.row_off(nxt, 128 + R, lds) + (unsigned)C * 2u; } } }
;             G_WAIT_L(0); G_BAR; G_MMA(0, 0, At, B0); G_MMA(0, 1, At, B1); G_WAIT_V(8); G_BAR; G_SCHED;
;             G_LDA(At, 0, 1); G_STAGE(G_SB(0, 0), b02, voffB); G_STAGE(G_SB(0, 1), b12, voffB); G_STAGE(G_SA(0, 0), a02, vA0);
;             G_WAIT_L(0); G_BAR; G_MMA(1, 0, At, B0); G_MMA(1, 1, At, B1); G_WAIT_V(8); G_BAR; G_SCHED;
.LBB0_1626:
	s_add_i32 s31, s31, 2
	s_add_u32 s78, s26, s74
	s_addc_u32 s79, s27, s75
	s_add_u32 s80, s62, s74
	s_addc_u32 s81, s63, s75
	s_add_u32 s82, s80, 0x100
	s_addc_u32 s83, s81, 0
	s_add_u32 s80, s36, s74
	s_addc_u32 s81, s37, s75
	s_add_u32 vcc_lo, s87, s74
	s_waitcnt lgkmcnt(0)
	s_addc_u32 vcc_hi, s90, s75
	s_and_b64 s[76:77], s[76:77], exec
	s_cselect_b32 s79, s57, s79
	s_cselect_b32 s78, s56, s78
	s_cselect_b32 s81, s51, s81
	s_cselect_b32 s80, s50, s80
	s_cselect_b32 s77, s55, s83
	s_cselect_b32 s76, s54, s82
	s_cselect_b32 s83, s53, vcc_hi
	s_cselect_b32 s82, s52, vcc_lo
	s_waitcnt vmcnt(8)
	s_barrier
	s_waitcnt lgkmcnt(0)
	v_mfma_i32_16x16x64_i8 v[156:159], v[88:91], v[184:187], v[156:159]
	v_mfma_i32_16x16x64_i8 v[148:151], v[96:99], v[184:187], v[148:151]
	v_mfma_i32_16x16x64_i8 v[140:143], v[88:91], v[176:179], v[140:143]
	v_mfma_i32_16x16x64_i8 v[132:135], v[96:99], v[176:179], v[132:135]
	v_mfma_i32_16x16x64_i8 v[124:127], v[88:91], v[168:171], v[124:127]
	v_mfma_i32_16x16x64_i8 v[116:119], v[96:99], v[168:171], v[116:119]
	v_mfma_i32_16x16x64_i8 v[108:111], v[88:91], v[160:163], v[108:111]
	v_mfma_i32_16x16x64_i8 v[84:87], v[96:99], v[160:163], v[84:87]
	v_mfma_i32_16x16x64_i8 v[156:159], v[92:95], v[188:191], v[156:159]
	v_mfma_i32_16x16x64_i8 v[148:151], v[100:103], v[188:191], v[148:151]
	v_mfma_i32_16x16x64_i8 v[140:143], v[92:95], v[180:183], v[140:143]
	v_mfma_i32_16x16x64_i8 v[132:135], v[100:103], v[180:183], v[132:135]
	v_mfma_i32_16x16x64_i8 v[124:127], v[92:95], v[172:175], v[124:127]
	v_mfma_i32_16x16x64_i8 v[116:119], v[100:103], v[172:175], v[116:119]
	v_mfma_i32_16x16x64_i8 v[108:111], v[92:95], v[164:167], v[108:111]
	v_mfma_i32_16x16x64_i8 v[84:87], v[100:103], v[164:167], v[84:87]
	v_mfma_i32_16x16x64_i8 v[152:155], v[64:67], v[184:187], v[152:155]
	v_mfma_i32_16x16x64_i8 v[144:147], v[72:75], v[184:187], v[144:147]
	v_mfma_i32_16x16x64_i8 v[136:139], v[64:67], v[176:179], v[136:139]
	v_mfma_i32_16x16x64_i8 v[128:131], v[72:75], v[176:179], v[128:131]
	v_mfma_i32_16x16x64_i8 v[120:123], v[64:67], v[168:171], v[120:123]
	v_mfma_i32_16x16x64_i8 v[112:115], v[72:75], v[168:171], v[112:115]
	v_mfma_i32_16x16x64_i8 v[104:107], v[64:67], v[160:163], v[104:107]
	v_mfma_i32_16x16x64_i8 v[80:83], v[72:75], v[160:163], v[80:83]
	v_mfma_i32_16x16x64_i8 v[152:155], v[68:71], v[188:191], v[152:155]
	v_mfma_i32_16x16x64_i8 v[144:147], v[76:79], v[188:191], v[144:147]
	v_mfma_i32_16x16x64_i8 v[136:139], v[68:71], v[180:183], v[136:139]
	v_mfma_i32_16x16x64_i8 v[128:131], v[76:79], v[180:183], v[128:131]
	v_mfma_i32_16x16x64_i8 v[120:123], v[68:71], v[172:175], v[120:123]
	v_mfma_i32_16x16x64_i8 v[112:115], v[76:79], v[172:175], v[112:115]
	v_mfma_i32_16x16x64_i8 v[104:107], v[68:71], v[164:167], v[104:107]
	v_mfma_i32_16x16x64_i8 v[80:83], v[76:79], v[164:167], v[80:83]
	s_waitcnt vmcnt(8)
	s_barrier
	s_mov_b32 m0, s34
	ds_read_b128 v[160:163], v208 offset:16384
	ds_read_b128 v[164:167], v208 offset:17408
	ds_read_b128 v[168:171], v208 offset:18432
	ds_read_b128 v[172:175], v208 offset:19456
	ds_read_b128 v[176:179], v208 offset:20480
	ds_read_b128 v[180:183], v208 offset:21504
	ds_read_b128 v[184:187], v208 offset:22528
	ds_read_b128 v[188:191], v208 offset:23552
	global_load_lds_dwordx4 v244, s[80:81]
	s_mov_b32 m0, s35
	v_mov_b32_e32 v211, v193
	global_load_lds_dwordx4 v246, s[80:81]
	s_mov_b32 m0, s30
	v_mov_b32_e32 v213, v193
	global_load_lds_dwordx4 v244, s[82:83]
	s_mov_b32 m0, s0
	v_mov_b32_e32 v195, v193
	global_load_lds_dwordx4 v246, s[82:83]
	s_mov_b32 m0, s3
	v_mov_b32_e32 v197, v193
	global_load_lds_dwordx4 v194, s[78:79]
	s_mov_b32 m0, s40
	v_lshl_add_u64 v[214:215], s[80:81], 0, v[244:245]
	global_load_lds_dwordx4 v196, s[78:79]
	s_waitcnt lgkmcnt(0)
	v_lshl_add_u64 v[216:217], s[80:81], 0, v[246:247]
	v_lshl_add_u64 v[210:211], s[82:83], 0, v[244:245]
	v_lshl_add_u64 v[212:213], s[82:83], 0, v[246:247]
	v_lshl_add_u64 v[218:219], s[78:79], 0, v[194:195]
	v_lshl_add_u64 v[220:221], s[78:79], 0, v[196:197]
	s_waitcnt vmcnt(8)
	s_barrier
	s_waitcnt lgkmcnt(0)
	v_mfma_i32_16x16x64_i8 v[60:63], v[88:91], v[160:163], v[60:63]
	v_mfma_i32_16x16x64_i8 v[52:55], v[96:99], v[160:163], v[52:55]
	v_mfma_i32_16x16x64_i8 v[44:47], v[88:91], v[168:171], v[44:47]
	v_mfma_i32_16x16x64_i8 v[36:39], v[96:99], v[168:171], v[36:39]
	v_mfma_i32_16x16x64_i8 v[28:31], v[88:91], v[176:179], v[28:31]
	v_mfma_i32_16x16x64_i8 v[20:23], v[96:99], v[176:179], v[20:23]
	v_mfma_i32_16x16x64_i8 v[12:15], v[88:91], v[184:187], v[12:15]
	v_mfma_i32_16x16x64_i8 v[4:7], v[96:99], v[184:187], v[4:7]
	v_mfma_i32_16x16x64_i8 v[60:63], v[92:95], v[164:167], v[60:63]
	v_mfma_i32_16x16x64_i8 v[52:55], v[100:103], v[164:167], v[52:55]
	v_mfma_i32_16x16x64_i8 v[44:47], v[92:95], v[172:175], v[44:47]
	v_mfma_i32_16x16x64_i8 v[36:39], v[100:103], v[172:175], v[36:39]
	v_mfma_i32_16x16x64_i8 v[28:31], v[92:95], v[180:183], v[28:31]
	v_mfma_i32_16x16x64_i8 v[20:23], v[100:103], v[180:183], v[20:23]
	v_mfma_i32_16x16x64_i8 v[12:15], v[92:95], v[188:191], v[12:15]
	v_mfma_i32_16x16x64_i8 v[4:7], v[100:103], v[188:191], v[4:7]
	v_mfma_i32_16x16x64_i8 v[56:59], v[64:67], v[160:163], v[56:59]
	v_mfma_i32_16x16x64_i8 v[48:51], v[72:75], v[160:163], v[48:51]
	v_mfma_i32_16x16x64_i8 v[40:43], v[64:67], v[168:171], v[40:43]
	v_mfma_i32_16x16x64_i8 v[32:35], v[72:75], v[168:171], v[32:35]
	v_mfma_i32_16x16x64_i8 v[24:27], v[64:67], v[176:179], v[24:27]
	v_mfma_i32_16x16x64_i8 v[16:19], v[72:75], v[176:179], v[16:19]
	v_mfma_i32_16x16x64_i8 v[8:11], v[64:67], v[184:187], v[8:11]
	v_mfma_i32_16x16x64_i8 v[0:3], v[72:75], v[184:187], v[0:3]
	v_mfma_i32_16x16x64_i8 v[56:59], v[68:71], v[164:167], v[56:59]
	v_mfma_i32_16x16x64_i8 v[48:51], v[76:79], v[164:167], v[48:51]
	v_mfma_i32_16x16x64_i8 v[40:43], v[68:71], v[172:175], v[40:43]
	v_mfma_i32_16x16x64_i8 v[32:35], v[76:79], v[172:175], v[32:35]
	v_mfma_i32_16x16x64_i8 v[24:27], v[68:71], v[180:183], v[24:27]
	v_mfma_i32_16x16x64_i8 v[16:19], v[76:79], v[180:183], v[16:19]
	v_mfma_i32_16x16x64_i8 v[8:11], v[68:71], v[188:191], v[8:11]
	v_mfma_i32_16x16x64_i8 v[0:3], v[76:79], v[188:191], v[0:3]
	s_waitcnt vmcnt(8)
	s_barrier
; #define G_STAGE(bufoff, gbase, voff) do { _Pragma("unroll") for (int _i = 0; _i < 2; ++_i) \
;         __builtin_amdgcn_global_load_lds((const unsigned*)((const char*)(gbase) + (voff)[_i]), (LAS unsigned*)(lds + (bufoff) + ldsw + _i * 8192), 16, 0, 0); } while (0)
; #define G_LDA(dst, b, h) do { _Pragma("unroll") for (int m = 0; m < 4; ++m) G_LD8(dst[m], lds + G_SA(b, h) + aoff + m * 2048); } while (0)
; #define G_LDB(dst, b, h) do { _Pragma("unroll") for (int n = 0; n < 2; ++n) G_LD8(dst[n], lds + G_SB(b, h) + boff + n * 2048); } while (0)
; #define G_WAIT_V(n) asm volatile("s_waitcnt vmcnt(" #n ")" ::: "memory")
; #define G_WAIT_L(n) asm volatile("s_waitcnt lgkmcnt(" #n ")" ::: "memory")
; #define G_BAR __builtin_amdgcn_s_barrier()
; #define G_SCHED __builtin_amdgcn_sched_barrier(0)
;     ...
;             G_LDB(B0, 1, 0); G_LDB(B1, 1, 1); G_SCHED; G_LDA(At, 1, 0); G_STAGE(G_SA(0, 1), a12, vA1);
;             G_WAIT_L(0); G_BAR; G_MMA(0, 0, At, B0); G_MMA(0, 1, At, B1); G_WAIT_V(8); G_BAR; G_SCHED;
;             G_LDA(At, 1, 1); G_STAGE(G_SB(1, 0), b02 + kstep, voffB); G_STAGE(G_SB(1, 1), b12 + kstep, voffB); G_STAGE(G_SA(1, 0), a02 + kstep, vA0);
;             G_WAIT_L(0); G_BAR; G_MMA(1, 0, At, B0); G_MMA(1, 1, At, B1); G_WAIT_V(8); G_BAR; G_SCHED;
;         }
	s_add_i32 s78, 0, 0x18000
	s_add_i32 s79, 0, 0x1c000
	v_add_u32_e32 v76, s78, v203
	v_add_u32_e32 v100, s79, v203
	ds_read_b128 v[64:67], v76
	ds_read_b128 v[68:71], v76 offset:1024
	ds_read_b128 v[72:75], v76 offset:2048
	ds_read_b128 v[76:79], v76 offset:3072
	ds_read_b128 v[88:91], v100
	ds_read_b128 v[92:95], v100 offset:1024
	ds_read_b128 v[96:99], v100 offset:2048
	ds_read_b128 v[100:103], v100 offset:3072
	s_mov_b32 m0, s41
	v_lshl_add_u64 v[222:223], s[76:77], 0, v[192:193]
	ds_read_b128 v[160:163], v208 offset:32768
	ds_read_b128 v[164:167], v208 offset:33792
	ds_read_b128 v[168:171], v208 offset:34816
	ds_read_b128 v[172:175], v208 offset:35840
	ds_read_b128 v[176:179], v208 offset:36864
	ds_read_b128 v[180:183], v208 offset:37888
	ds_read_b128 v[184:187], v208 offset:38912
	ds_read_b128 v[188:191], v208 offset:39936
	global_load_lds_dwordx4 v[222:223], off
	v_lshl_add_u64 v[222:223], s[76:77], 0, v[198:199]
	s_mov_b32 m0, s18
	s_nop 0
	global_load_lds_dwordx4 v[222:223], off
	s_waitcnt lgkmcnt(0)
	s_waitcnt vmcnt(8)
	s_barrier
	s_waitcnt lgkmcnt(0)
	v_mfma_i32_16x16x64_i8 v[156:159], v[64:67], v[160:163], v[156:159]
	v_mfma_i32_16x16x64_i8 v[148:151], v[72:75], v[160:163], v[148:151]
	v_mfma_i32_16x16x64_i8 v[140:143], v[64:67], v[168:171], v[140:143]
	v_mfma_i32_16x16x64_i8 v[132:135], v[72:75], v[168:171], v[132:135]
	v_mfma_i32_16x16x64_i8 v[124:127], v[64:67], v[176:179], v[124:127]
	v_mfma_i32_16x16x64_i8 v[116:119], v[72:75], v[176:179], v[116:119]
	v_mfma_i32_16x16x64_i8 v[108:111], v[64:67], v[184:187], v[108:111]
	v_mfma_i32_16x16x64_i8 v[84:87], v[72:75], v[184:187], v[84:87]
	v_mfma_i32_16x16x64_i8 v[156:159], v[68:71], v[164:167], v[156:159]
	v_mfma_i32_16x16x64_i8 v[148:151], v[76:79], v[164:167], v[148:151]
	v_mfma_i32_16x16x64_i8 v[140:143], v[68:71], v[172:175], v[140:143]
	v_mfma_i32_16x16x64_i8 v[132:135], v[76:79], v[172:175], v[132:135]
	v_mfma_i32_16x16x64_i8 v[124:127], v[68:71], v[180:183], v[124:127]
	v_mfma_i32_16x16x64_i8 v[116:119], v[76:79], v[180:183], v[116:119]
	v_mfma_i32_16x16x64_i8 v[108:111], v[68:71], v[188:191], v[108:111]
	v_mfma_i32_16x16x64_i8 v[84:87], v[76:79], v[188:191], v[84:87]
	v_mfma_i32_16x16x64_i8 v[152:155], v[88:91], v[160:163], v[152:155]
	v_mfma_i32_16x16x64_i8 v[144:147], v[96:99], v[160:163], v[144:147]
	v_mfma_i32_16x16x64_i8 v[136:139], v[88:91], v[168:171], v[136:139]
	v_mfma_i32_16x16x64_i8 v[128:131], v[96:99], v[168:171], v[128:131]
	v_mfma_i32_16x16x64_i8 v[120:123], v[88:91], v[176:179], v[120:123]
	v_mfma_i32_16x16x64_i8 v[112:115], v[96:99], v[176:179], v[112:115]
	v_mfma_i32_16x16x64_i8 v[104:107], v[88:91], v[184:187], v[104:107]
	v_mfma_i32_16x16x64_i8 v[80:83], v[96:99], v[184:187], v[80:83]
	v_mfma_i32_16x16x64_i8 v[152:155], v[92:95], v[164:167], v[152:155]
	v_mfma_i32_16x16x64_i8 v[144:147], v[100:103], v[164:167], v[144:147]
	v_mfma_i32_16x16x64_i8 v[136:139], v[92:95], v[172:175], v[136:139]
	v_mfma_i32_16x16x64_i8 v[128:131], v[100:103], v[172:175], v[128:131]
	v_mfma_i32_16x16x64_i8 v[120:123], v[92:95], v[180:183], v[120:123]
	v_mfma_i32_16x16x64_i8 v[112:115], v[100:103], v[180:183], v[112:115]
	v_mfma_i32_16x16x64_i8 v[104:107], v[92:95], v[188:191], v[104:107]
	v_mfma_i32_16x16x64_i8 v[80:83], v[100:103], v[188:191], v[80:83]
	s_waitcnt vmcnt(8)
	s_barrier
	s_add_i32 s76, s78, s93
	v_lshl_add_u64 v[214:215], v[214:215], 0, s[44:45]
	s_mov_b32 m0, s76
	ds_read_b128 v[160:163], v208 offset:49152
	ds_read_b128 v[164:167], v208 offset:50176
	ds_read_b128 v[168:171], v208 offset:51200
	ds_read_b128 v[172:175], v208 offset:52224
	ds_read_b128 v[176:179], v208 offset:53248
	ds_read_b128 v[180:183], v208 offset:54272
	ds_read_b128 v[184:187], v208 offset:55296
	ds_read_b128 v[188:191], v208 offset:56320
	global_load_lds_dwordx4 v[214:215], off
	v_lshl_add_u64 v[214:215], v[216:217], 0, s[44:45]
	s_add_i32 m0, s76, 0x2000
	s_add_i32 s76, s79, s93
	global_load_lds_dwordx4 v[214:215], off
	v_lshl_add_u64 v[210:211], v[210:211], 0, s[44:45]
	s_mov_b32 m0, s76
	s_nop 0
	global_load_lds_dwordx4 v[210:211], off
	v_lshl_add_u64 v[210:211], v[212:213], 0, s[44:45]
	s_add_i32 m0, s76, 0x2000
	s_nop 0
	global_load_lds_dwordx4 v[210:211], off
	v_lshl_add_u64 v[210:211], v[218:219], 0, s[44:45]
	s_mov_b32 m0, s19
	s_nop 0
	global_load_lds_dwordx4 v[210:211], off
	v_lshl_add_u64 v[210:211], v[220:221], 0, s[44:45]
	s_mov_b32 m0, s89
	s_nop 0
	global_load_lds_dwordx4 v[210:211], off
	s_waitcnt lgkmcnt(0)
	s_waitcnt vmcnt(8)
	s_barrier
	s_waitcnt lgkmcnt(0)
	v_mfma_i32_16x16x64_i8 v[60:63], v[64:67], v[160:163], v[60:63]
	v_mfma_i32_16x16x64_i8 v[52:55], v[72:75], v[160:163], v[52:55]
	v_mfma_i32_16x16x64_i8 v[44:47], v[64:67], v[168:171], v[44:47]
	v_mfma_i32_16x16x64_i8 v[36:39], v[72:75], v[168:171], v[36:39]
	v_mfma_i32_16x16x64_i8 v[28:31], v[64:67], v[176:179], v[28:31]
	v_mfma_i32_16x16x64_i8 v[20:23], v[72:75], v[176:179], v[20:23]
	v_mfma_i32_16x16x64_i8 v[12:15], v[64:67], v[184:187], v[12:15]
	v_mfma_i32_16x16x64_i8 v[4:7], v[72:75], v[184:187], v[4:7]
	v_mfma_i32_16x16x64_i8 v[60:63], v[68:71], v[164:167], v[60:63]
	v_mfma_i32_16x16x64_i8 v[52:55], v[76:79], v[164:167], v[52:55]
	v_mfma_i32_16x16x64_i8 v[44:47], v[68:71], v[172:175], v[44:47]
	v_mfma_i32_16x16x64_i8 v[36:39], v[76:79], v[172:175], v[36:39]
	v_mfma_i32_16x16x64_i8 v[28:31], v[68:71], v[180:183], v[28:31]
	v_mfma_i32_16x16x64_i8 v[20:23], v[76:79], v[180:183], v[20:23]
	v_mfma_i32_16x16x64_i8 v[12:15], v[68:71], v[188:191], v[12:15]
	v_mfma_i32_16x16x64_i8 v[4:7], v[76:79], v[188:191], v[4:7]
	v_mfma_i32_16x16x64_i8 v[56:59], v[88:91], v[160:163], v[56:59]
	v_mfma_i32_16x16x64_i8 v[48:51], v[96:99], v[160:163], v[48:51]
	v_mfma_i32_16x16x64_i8 v[40:43], v[88:91], v[168:171], v[40:43]
	v_mfma_i32_16x16x64_i8 v[32:35], v[96:99], v[168:171], v[32:35]
	v_mfma_i32_16x16x64_i8 v[24:27], v[88:91], v[176:179], v[24:27]
	v_mfma_i32_16x16x64_i8 v[16:19], v[96:99], v[176:179], v[16:19]
	v_mfma_i32_16x16x64_i8 v[8:11], v[88:91], v[184:187], v[8:11]
	v_mfma_i32_16x16x64_i8 v[0:3], v[96:99], v[184:187], v[0:3]
	v_mfma_i32_16x16x64_i8 v[56:59], v[92:95], v[164:167], v[56:59]
	v_mfma_i32_16x16x64_i8 v[48:51], v[100:103], v[164:167], v[48:51]
	v_mfma_i32_16x16x64_i8 v[40:43], v[92:95], v[172:175], v[40:43]
	v_mfma_i32_16x16x64_i8 v[32:35], v[100:103], v[172:175], v[32:35]
	v_mfma_i32_16x16x64_i8 v[24:27], v[92:95], v[180:183], v[24:27]
	v_mfma_i32_16x16x64_i8 v[16:19], v[100:103], v[180:183], v[16:19]
	v_mfma_i32_16x16x64_i8 v[8:11], v[92:95], v[188:191], v[8:11]
	v_mfma_i32_16x16x64_i8 v[0:3], v[100:103], v[188:191], v[0:3]
	s_waitcnt vmcnt(8)
	s_barrier
	s_add_u32 s74, s74, 0x100
	s_addc_u32 s75, s75, 0
	s_cmp_ge_i32 s31, s33
	s_cbranch_scc1 .LBB0_1639

; #define G_STAGE(bufoff, gbase, voff) do { _Pragma("unroll") for (int _i = 0; _i < 2; ++_i) \
;         __builtin_amdgcn_global_load_lds((const unsigned*)((const char*)(gbase) + (voff)[_i]), (LAS unsigned*)(lds + (bufoff) + ldsw + _i * 8192), 16, 0, 0); } while (0)
; #define G_LDA(dst, b, h) do { _Pragma("unroll") for (int m = 0; m < 4; ++m) G_LD8(dst[m], lds + G_SA(b, h) + aoff + m * 2048); } while (0)
; #define G_LDB(dst, b, h) do { _Pragma("unroll") for (int n = 0; n < 2; ++n) G_LD8(dst[n], lds + G_SB(b, h) + boff + n * 2048); } while (0)
; #define G_WAIT_V(n) asm volatile("s_waitcnt vmcnt(" #n ")" ::: "memory")
; #define G_WAIT_L(n) asm volatile("s_waitcnt lgkmcnt(" #n ")" ::: "memory")
; #define G_BAR __builtin_amdgcn_s_barrier()
; #define G_SCHED __builtin_amdgcn_sched_barrier(0)
;     __device__ __forceinline__ unsigned row_off(const Unit& u, int r, LAS unsigned char* lds) const { return (unsigned)((const LAS int*)(lds + LDS_STAGE + u.q * 4096))[r] * (unsigned)rowbytes; }
;     ...
;             const char* a11 = cur.a1 + (size_t)(t + 1) * kstep;
;             const char* a02 = last ? nxt.a0 : cur.a0 + (size_t)(t + 2) * kstep; const char* a12 = last ? nxt.a1 : cur.a1 + (size_t)(t + 2) * kstep;
;             const char* b02 = last ? nxt.b0 : cur.b0 + (size_t)(t + 2) * kstep; const char* b12 = last ? nxt.b1 : cur.b1 + (size_t)(t + 2) * kstep;
;             G_LDB(B0, 0, 0); G_LDB(B1, 0, 1); G_SCHED; G_LDA(At, 0, 0); G_STAGE(G_SA(1, 1), a11, vA1);
;             if constexpr (GATHER) { if (last) { int tz = tid; asm volatile("" : "+v"(tz));
; #pragma unroll
;                 for (int i = 0; i < 2; ++i) { int R, C; stage_rc(tz * 16 + i * 8192, R, C); gc0[i] = S.row_off(nxt, R, lds) + (unsigned)C * 2u; gc1[i] = S.row_off(nxt, 128 + R, lds) + (unsigned)C * 2u; } } }
;             G_WAIT_L(0); G_BAR; G_MMA(0, 0, At, B0); G_MMA(0, 1, At, B1); G_WAIT_V(8); G_BAR; G_SCHED;
;             G_LDA(At, 0, 1); G_STAGE(G_SB(0, 0), b02, voffB); G_STAGE(G_SB(0, 1), b12, voffB); G_STAGE(G_SA(0, 0), a02, vA0);
.LBB0_1733:
	s_add_i32 s81, s80, 2
	s_add_u32 s52, s78, s48
	s_addc_u32 s53, s79, s49
	s_add_u32 s58, s44, s48
	s_addc_u32 s59, s45, s49
	s_add_u32 s86, s58, 0x100
	v_add_u32_e32 v154, s66, v137
	v_add_u32_e32 v170, s67, v137
	s_addc_u32 s87, s59, 0
	ds_read_b128 v[142:145], v154
	ds_read_b128 v[146:149], v154 offset:1024
	ds_read_b128 v[150:153], v154 offset:2048
	ds_read_b128 v[154:157], v154 offset:3072
	ds_read_b128 v[158:161], v170
	ds_read_b128 v[162:165], v170 offset:1024
	ds_read_b128 v[166:169], v170 offset:2048
	ds_read_b128 v[170:173], v170 offset:3072
	s_add_u32 s56, s29, s48
	s_addc_u32 s57, s75, s49
	s_add_u32 s82, s76, s48
	s_addc_u32 s83, s77, s49
	s_add_i32 s90, s66, s22
	s_add_i32 m0, s23, 0xc000
	s_add_i32 s89, s23, 0xe000
	s_add_i32 s84, s90, 0x2000
	s_cmp_eq_u32 s65, s80
	s_cselect_b32 s55, s37, s53
	s_cselect_b32 s54, s36, s52
	s_cselect_b32 s57, s31, s57
	s_cselect_b32 s56, s30, s56
	s_cselect_b32 s53, s39, s87
	s_cselect_b32 s52, s38, s86
	v_lshl_add_u64 v[206:207], s[58:59], 0, v[128:129]
	v_lshl_add_u64 v[206:207], v[206:207], 0, s[10:11]
	ds_read_b128 v[174:177], v138
	ds_read_b128 v[178:181], v138 offset:1024
	ds_read_b128 v[182:185], v138 offset:2048
	ds_read_b128 v[186:189], v138 offset:3072
	ds_read_b128 v[190:193], v138 offset:4096
	ds_read_b128 v[194:197], v138 offset:5120
	ds_read_b128 v[198:201], v138 offset:6144
	ds_read_b128 v[202:205], v138 offset:7168
	global_load_lds_dwordx4 v[206:207], off
	v_lshl_add_u64 v[206:207], s[58:59], 0, v[130:131]
	v_lshl_add_u64 v[206:207], v[206:207], 0, s[10:11]
	s_mov_b32 m0, s89
	v_mov_b32_e32 v131, v129
	global_load_lds_dwordx4 v[206:207], off
	s_waitcnt lgkmcnt(0)
	s_waitcnt vmcnt(8)
	s_barrier
	s_waitcnt lgkmcnt(0)
	v_mfma_scale_f32_16x16x128_f8f6f4 v[124:127], v[142:149], v[174:181], v[124:127], v139, v139 op_sel_hi:[0,0,0]
	v_mfma_scale_f32_16x16x128_f8f6f4 v[120:123], v[150:157], v[174:181], v[120:123], v139, v139 op_sel_hi:[0,0,0]
	v_mfma_scale_f32_16x16x128_f8f6f4 v[116:119], v[142:149], v[182:189], v[116:119], v139, v139 op_sel_hi:[0,0,0]
	v_mfma_scale_f32_16x16x128_f8f6f4 v[112:115], v[150:157], v[182:189], v[112:115], v139, v139 op_sel_hi:[0,0,0]
	v_mfma_scale_f32_16x16x128_f8f6f4 v[108:111], v[142:149], v[190:197], v[108:111], v139, v139 op_sel_hi:[0,0,0]
	v_mfma_scale_f32_16x16x128_f8f6f4 v[104:107], v[150:157], v[190:197], v[104:107], v139, v139 op_sel_hi:[0,0,0]
	v_mfma_scale_f32_16x16x128_f8f6f4 v[100:103], v[142:149], v[198:205], v[100:103], v139, v139 op_sel_hi:[0,0,0]
	v_mfma_scale_f32_16x16x128_f8f6f4 v[96:99], v[150:157], v[198:205], v[96:99], v139, v139 op_sel_hi:[0,0,0]
	v_mfma_scale_f32_16x16x128_f8f6f4 v[206:209], v[158:165], v[174:181], v[60:63], v139, v139 op_sel_hi:[0,0,0]
	v_mfma_scale_f32_16x16x128_f8f6f4 v[174:177], v[166:173], v[174:181], v[56:59], v139, v139 op_sel_hi:[0,0,0]
	v_mfma_scale_f32_16x16x128_f8f6f4 v[178:181], v[158:165], v[182:189], v[52:55], v139, v139 op_sel_hi:[0,0,0]
	v_mfma_scale_f32_16x16x128_f8f6f4 v[182:185], v[166:173], v[182:189], v[48:51], v139, v139 op_sel_hi:[0,0,0]
	v_mfma_scale_f32_16x16x128_f8f6f4 v[186:189], v[158:165], v[190:197], v[44:47], v139, v139 op_sel_hi:[0,0,0]
	v_mfma_scale_f32_16x16x128_f8f6f4 v[190:193], v[166:173], v[190:197], v[40:43], v139, v139 op_sel_hi:[0,0,0]
	v_mfma_scale_f32_16x16x128_f8f6f4 v[194:197], v[158:165], v[198:205], v[36:39], v139, v139 op_sel_hi:[0,0,0]
	v_mfma_scale_f32_16x16x128_f8f6f4 v[198:201], v[166:173], v[198:205], v[32:35], v139, v139 op_sel_hi:[0,0,0]
	s_waitcnt vmcnt(8)
	s_barrier
	s_mov_b32 m0, s90
	s_nop 3
	ds_read_b128 v[32:35], v138 offset:16384
	ds_read_b128 v[36:39], v138 offset:17408
	ds_read_b128 v[40:43], v138 offset:18432
	ds_read_b128 v[44:47], v138 offset:19456
	ds_read_b128 v[48:51], v138 offset:20480
	ds_read_b128 v[52:55], v138 offset:21504
	ds_read_b128 v[56:59], v138 offset:22528
	ds_read_b128 v[60:63], v138 offset:23552
	global_load_lds_dwordx4 v132, s[56:57]
	s_mov_b32 m0, s84
	s_cselect_b32 s59, s35, s83
	s_cselect_b32 s58, s34, s82
	s_add_i32 s80, s67, s22
	s_add_u32 s98, s56, 0x20000
	s_addc_u32 s99, s57, 0
	global_load_lds_dwordx4 v132, s[98:99]
	s_mov_b32 m0, s80
	v_mov_b32_e32 v133, v129
	global_load_lds_dwordx4 v132, s[58:59]
	s_add_i32 m0, s80, 0x2000
	s_add_u32 s100, s58, 0x20000
	s_addc_u32 s101, s59, 0
	global_load_lds_dwordx4 v132, s[100:101]
	s_mov_b32 m0, s23
	v_lshl_add_u64 v[246:247], s[56:57], 0, v[132:133]
	global_load_lds_dwordx4 v128, s[54:55]
	s_mov_b32 m0, s24
	v_lshl_add_u64 v[248:249], s[98:99], 0, v[132:133]
	global_load_lds_dwordx4 v130, s[54:55]
	s_waitcnt lgkmcnt(0)
	v_lshl_add_u64 v[250:251], s[100:101], 0, v[132:133]
	v_lshl_add_u64 v[252:253], s[54:55], 0, v[128:129]
	v_lshl_add_u64 v[134:135], s[54:55], 0, v[130:131]
	s_waitcnt vmcnt(8)
	s_barrier
; #define G_STAGE(bufoff, gbase, voff) do { _Pragma("unroll") for (int _i = 0; _i < 2; ++_i) \
;         __builtin_amdgcn_global_load_lds((const unsigned*)((const char*)(gbase) + (voff)[_i]), (LAS unsigned*)(lds + (bufoff) + ldsw + _i * 8192), 16, 0, 0); } while (0)
; #define G_LDA(dst, b, h) do { _Pragma("unroll") for (int m = 0; m < 4; ++m) G_LD8(dst[m], lds + G_SA(b, h) + aoff + m * 2048); } while (0)
; #define G_LDB(dst, b, h) do { _Pragma("unroll") for (int n = 0; n < 2; ++n) G_LD8(dst[n], lds + G_SB(b, h) + boff + n * 2048); } while (0)
; #define G_WAIT_V(n) asm volatile("s_waitcnt vmcnt(" #n ")" ::: "memory")
; #define G_WAIT_L(n) asm volatile("s_waitcnt lgkmcnt(" #n ")" ::: "memory")
; #define G_BAR __builtin_amdgcn_s_barrier()
; #define G_SCHED __builtin_amdgcn_sched_barrier(0)
;     ...
;             G_WAIT_L(0); G_BAR; G_MMA(1, 0, At, B0); G_MMA(1, 1, At, B1); G_WAIT_V(8); G_BAR; G_SCHED;
;             G_LDB(B0, 1, 0); G_LDB(B1, 1, 1); G_SCHED; G_LDA(At, 1, 0); G_STAGE(G_SA(0, 1), a12, vA1);
;             G_WAIT_L(0); G_BAR; G_MMA(0, 0, At, B0); G_MMA(0, 1, At, B1); G_WAIT_V(8); G_BAR; G_SCHED;
	s_waitcnt lgkmcnt(0)
	v_mfma_scale_f32_16x16x128_f8f6f4 v[92:95], v[142:149], v[32:39], v[92:95], v139, v139 op_sel_hi:[0,0,0]
	v_mfma_scale_f32_16x16x128_f8f6f4 v[88:91], v[150:157], v[32:39], v[88:91], v139, v139 op_sel_hi:[0,0,0]
	v_mfma_scale_f32_16x16x128_f8f6f4 v[84:87], v[142:149], v[40:47], v[84:87], v139, v139 op_sel_hi:[0,0,0]
	v_mfma_scale_f32_16x16x128_f8f6f4 v[80:83], v[150:157], v[40:47], v[80:83], v139, v139 op_sel_hi:[0,0,0]
	v_mfma_scale_f32_16x16x128_f8f6f4 v[76:79], v[142:149], v[48:55], v[76:79], v139, v139 op_sel_hi:[0,0,0]
	v_mfma_scale_f32_16x16x128_f8f6f4 v[72:75], v[150:157], v[48:55], v[72:75], v139, v139 op_sel_hi:[0,0,0]
	v_mfma_scale_f32_16x16x128_f8f6f4 v[202:205], v[142:149], v[56:63], v[68:71], v139, v139 op_sel_hi:[0,0,0]
	v_mfma_scale_f32_16x16x128_f8f6f4 v[210:213], v[150:157], v[56:63], v[64:67], v139, v139 op_sel_hi:[0,0,0]
	v_mfma_scale_f32_16x16x128_f8f6f4 v[214:217], v[158:165], v[32:39], v[28:31], v139, v139 op_sel_hi:[0,0,0]
	v_mfma_scale_f32_16x16x128_f8f6f4 v[218:221], v[166:173], v[32:39], v[24:27], v139, v139 op_sel_hi:[0,0,0]
	v_mfma_scale_f32_16x16x128_f8f6f4 v[222:225], v[158:165], v[40:47], v[20:23], v139, v139 op_sel_hi:[0,0,0]
	v_mfma_scale_f32_16x16x128_f8f6f4 v[226:229], v[166:173], v[40:47], v[16:19], v139, v139 op_sel_hi:[0,0,0]
	v_mfma_scale_f32_16x16x128_f8f6f4 v[230:233], v[158:165], v[48:55], v[12:15], v139, v139 op_sel_hi:[0,0,0]
	v_mfma_scale_f32_16x16x128_f8f6f4 v[234:237], v[166:173], v[48:55], v[8:11], v139, v139 op_sel_hi:[0,0,0]
	v_mfma_scale_f32_16x16x128_f8f6f4 v[238:241], v[158:165], v[56:63], v[4:7], v139, v139 op_sel_hi:[0,0,0]
	v_mfma_scale_f32_16x16x128_f8f6f4 v[242:245], v[166:173], v[56:63], v[0:3], v139, v139 op_sel_hi:[0,0,0]
	s_waitcnt vmcnt(8)
	s_barrier
	s_add_i32 s54, 0, 0x18000
	s_add_i32 s55, 0, 0x1c000
	v_add_u32_e32 v12, s54, v137
	v_add_u32_e32 v16, s55, v137
	s_nop 0
	ds_read_b128 v[0:3], v12
	ds_read_b128 v[4:7], v12 offset:1024
	ds_read_b128 v[8:11], v12 offset:2048
	ds_read_b128 v[12:15], v12 offset:3072
	ds_read_b128 v[142:145], v16
	ds_read_b128 v[146:149], v16 offset:1024
	ds_read_b128 v[150:153], v16 offset:2048
	ds_read_b128 v[154:157], v16 offset:3072
	s_mov_b32 m0, s25
	ds_read_b128 v[16:19], v138 offset:32768
	ds_read_b128 v[20:23], v138 offset:33792
	ds_read_b128 v[24:27], v138 offset:34816
	ds_read_b128 v[28:31], v138 offset:35840
	ds_read_b128 v[32:35], v138 offset:36864
	ds_read_b128 v[36:39], v138 offset:37888
	ds_read_b128 v[64:67], v138 offset:38912
	ds_read_b128 v[68:71], v138 offset:39936
	global_load_lds_dwordx4 v128, s[52:53]
	s_mov_b32 m0, s26
	s_nop 0
	global_load_lds_dwordx4 v130, s[52:53]
	s_waitcnt lgkmcnt(0)
	s_waitcnt vmcnt(8)
	s_barrier
	s_waitcnt lgkmcnt(0)
	v_mfma_scale_f32_16x16x128_f8f6f4 v[124:127], v[0:7], v[16:23], v[124:127], v139, v139 op_sel_hi:[0,0,0]
	v_mfma_scale_f32_16x16x128_f8f6f4 v[120:123], v[8:15], v[16:23], v[120:123], v139, v139 op_sel_hi:[0,0,0]
	v_mfma_scale_f32_16x16x128_f8f6f4 v[116:119], v[0:7], v[24:31], v[116:119], v139, v139 op_sel_hi:[0,0,0]
	v_mfma_scale_f32_16x16x128_f8f6f4 v[112:115], v[8:15], v[24:31], v[112:115], v139, v139 op_sel_hi:[0,0,0]
	v_mfma_scale_f32_16x16x128_f8f6f4 v[108:111], v[0:7], v[32:39], v[108:111], v139, v139 op_sel_hi:[0,0,0]
	v_mfma_scale_f32_16x16x128_f8f6f4 v[104:107], v[8:15], v[32:39], v[104:107], v139, v139 op_sel_hi:[0,0,0]
	v_mfma_scale_f32_16x16x128_f8f6f4 v[100:103], v[0:7], v[64:71], v[100:103], v139, v139 op_sel_hi:[0,0,0]
	v_mfma_scale_f32_16x16x128_f8f6f4 v[96:99], v[8:15], v[64:71], v[96:99], v139, v139 op_sel_hi:[0,0,0]
	v_mfma_scale_f32_16x16x128_f8f6f4 v[60:63], v[142:149], v[16:23], v[206:209], v139, v139 op_sel_hi:[0,0,0]
	v_mfma_scale_f32_16x16x128_f8f6f4 v[56:59], v[150:157], v[16:23], v[174:177], v139, v139 op_sel_hi:[0,0,0]
	v_mfma_scale_f32_16x16x128_f8f6f4 v[52:55], v[142:149], v[24:31], v[178:181], v139, v139 op_sel_hi:[0,0,0]
	v_mfma_scale_f32_16x16x128_f8f6f4 v[48:51], v[150:157], v[24:31], v[182:185], v139, v139 op_sel_hi:[0,0,0]
	v_mfma_scale_f32_16x16x128_f8f6f4 v[44:47], v[142:149], v[32:39], v[186:189], v139, v139 op_sel_hi:[0,0,0]
	v_mfma_scale_f32_16x16x128_f8f6f4 v[40:43], v[150:157], v[32:39], v[190:193], v139, v139 op_sel_hi:[0,0,0]
	v_mfma_scale_f32_16x16x128_f8f6f4 v[36:39], v[142:149], v[64:71], v[194:197], v139, v139 op_sel_hi:[0,0,0]
	v_mfma_scale_f32_16x16x128_f8f6f4 v[32:35], v[150:157], v[64:71], v[198:201], v139, v139 op_sel_hi:[0,0,0]
	s_waitcnt vmcnt(8)
	s_barrier
; #define G_STAGE(bufoff, gbase, voff) do { _Pragma("unroll") for (int _i = 0; _i < 2; ++_i) \
;         __builtin_amdgcn_global_load_lds((const unsigned*)((const char*)(gbase) + (voff)[_i]), (LAS unsigned*)(lds + (bufoff) + ldsw + _i * 8192), 16, 0, 0); } while (0)
; #define G_LDA(dst, b, h) do { _Pragma("unroll") for (int m = 0; m < 4; ++m) G_LD8(dst[m], lds + G_SA(b, h) + aoff + m * 2048); } while (0)
; #define G_WAIT_V(n) asm volatile("s_waitcnt vmcnt(" #n ")" ::: "memory")
; #define G_WAIT_L(n) asm volatile("s_waitcnt lgkmcnt(" #n ")" ::: "memory")
; #define G_BAR __builtin_amdgcn_s_barrier()
; #define G_SCHED __builtin_amdgcn_sched_barrier(0)
;     ...
;             G_LDA(At, 1, 1); G_STAGE(G_SB(1, 0), b02 + kstep, voffB); G_STAGE(G_SB(1, 1), b12 + kstep, voffB); G_STAGE(G_SA(1, 0), a02 + kstep, vA0);
;             G_WAIT_L(0); G_BAR; G_MMA(1, 0, At, B0); G_MMA(1, 1, At, B1); G_WAIT_V(8); G_BAR; G_SCHED;
;         }
	s_add_i32 s52, s54, s22
	v_lshl_add_u64 v[24:25], v[246:247], 0, s[10:11]
	s_mov_b32 m0, s52
	ds_read_b128 v[16:19], v138 offset:49152
	ds_read_b128 v[20:23], v138 offset:50176
	ds_read_b128 v[158:161], v138 offset:51200
	ds_read_b128 v[162:165], v138 offset:52224
	ds_read_b128 v[166:169], v138 offset:53248
	ds_read_b128 v[170:173], v138 offset:54272
	ds_read_b128 v[174:177], v138 offset:55296
	ds_read_b128 v[178:181], v138 offset:56320
	global_load_lds_dwordx4 v[24:25], off
	v_lshl_add_u64 v[24:25], v[248:249], 0, s[10:11]
	s_add_i32 m0, s52, 0x2000
	s_add_i32 s52, s55, s22
	s_sub_u32 s98, s10, 0x20000
	s_subb_u32 s99, s11, 0
	global_load_lds_dwordx4 v[24:25], off
	v_lshl_add_u64 v[24:25], v[250:251], 0, s[98:99]
	s_mov_b32 m0, s52
	s_nop 0
	global_load_lds_dwordx4 v[24:25], off
	v_lshl_add_u64 v[24:25], v[250:251], 0, s[10:11]
	s_add_i32 m0, s52, 0x2000
	s_nop 0
	global_load_lds_dwordx4 v[24:25], off
	v_lshl_add_u64 v[24:25], v[252:253], 0, s[10:11]
	s_mov_b32 m0, s62
	s_nop 0
	global_load_lds_dwordx4 v[24:25], off
	v_lshl_add_u64 v[24:25], v[134:135], 0, s[10:11]
	s_mov_b32 m0, s63
	s_nop 0
	global_load_lds_dwordx4 v[24:25], off
	s_waitcnt lgkmcnt(0)
	s_waitcnt vmcnt(8)
	s_barrier
	s_waitcnt lgkmcnt(0)
	v_mfma_scale_f32_16x16x128_f8f6f4 v[92:95], v[0:7], v[16:23], v[92:95], v139, v139 op_sel_hi:[0,0,0]
	v_mfma_scale_f32_16x16x128_f8f6f4 v[88:91], v[8:15], v[16:23], v[88:91], v139, v139 op_sel_hi:[0,0,0]
	v_mfma_scale_f32_16x16x128_f8f6f4 v[84:87], v[0:7], v[158:165], v[84:87], v139, v139 op_sel_hi:[0,0,0]
	v_mfma_scale_f32_16x16x128_f8f6f4 v[80:83], v[8:15], v[158:165], v[80:83], v139, v139 op_sel_hi:[0,0,0]
	v_mfma_scale_f32_16x16x128_f8f6f4 v[76:79], v[0:7], v[166:173], v[76:79], v139, v139 op_sel_hi:[0,0,0]
	v_mfma_scale_f32_16x16x128_f8f6f4 v[72:75], v[8:15], v[166:173], v[72:75], v139, v139 op_sel_hi:[0,0,0]
	v_mfma_scale_f32_16x16x128_f8f6f4 v[68:71], v[0:7], v[174:181], v[202:205], v139, v139 op_sel_hi:[0,0,0]
	v_mfma_scale_f32_16x16x128_f8f6f4 v[64:67], v[8:15], v[174:181], v[210:213], v139, v139 op_sel_hi:[0,0,0]
	v_mfma_scale_f32_16x16x128_f8f6f4 v[28:31], v[142:149], v[16:23], v[214:217], v139, v139 op_sel_hi:[0,0,0]
	v_mfma_scale_f32_16x16x128_f8f6f4 v[24:27], v[150:157], v[16:23], v[218:221], v139, v139 op_sel_hi:[0,0,0]
	v_mfma_scale_f32_16x16x128_f8f6f4 v[20:23], v[142:149], v[158:165], v[222:225], v139, v139 op_sel_hi:[0,0,0]
	v_mfma_scale_f32_16x16x128_f8f6f4 v[16:19], v[150:157], v[158:165], v[226:229], v139, v139 op_sel_hi:[0,0,0]
	v_mfma_scale_f32_16x16x128_f8f6f4 v[12:15], v[142:149], v[166:173], v[230:233], v139, v139 op_sel_hi:[0,0,0]
	v_mfma_scale_f32_16x16x128_f8f6f4 v[8:11], v[150:157], v[166:173], v[234:237], v139, v139 op_sel_hi:[0,0,0]
	v_mfma_scale_f32_16x16x128_f8f6f4 v[4:7], v[142:149], v[174:181], v[238:241], v139, v139 op_sel_hi:[0,0,0]
	v_mfma_scale_f32_16x16x128_f8f6f4 v[0:3], v[150:157], v[174:181], v[242:245], v139, v139 op_sel_hi:[0,0,0]
	s_waitcnt vmcnt(8)
	s_barrier
	s_add_u32 s48, s48, 0x100
	s_addc_u32 s49, s49, 0
	s_cmp_ge_i32 s81, s0
	s_cbranch_scc1 .LBB0_1735
	s_mov_b32 s80, s81
	s_branch .LBB0_1724
